# GEMM K-loops (7 non-gather loops): LDS-DMA switched to saddr form (SGPR base + 32-bit lane offset); 16 v_lshl_add_u64 per iteration removed from load segments
# speedup vs baseline: 1.0067x; 1.0065x over previous
; #define PG8_STAGE(bufoff, gbase, voff) do { _Pragma("unroll") for (int _i = 0; _i < 2; ++_i) \
;         __builtin_amdgcn_global_load_lds((const unsigned*)((const char*)(gbase) + (voff)[_i]), (PG8_LAS unsigned*)(lds + (bufoff) + ldsw + _i * 8192), 16, 0, 0); } while (0)
; #define PG8_STAGE_A(b, h, gbase, NX) do { if constexpr (AM::GATHER) { const unsigned so_[2] = {(NX) ? gno[h][0] : gao[h][0], (NX) ? gno[h][1] : gao[h][1]}; PG8_STAGE(PG8_SA(b, h), gbase, so_); } \
;         else { PG8_STAGE(PG8_SA(b, h), (gbase) + (h) * hstep, voffA); } } while (0)
; #define PG8_LDA(dst, b, h) do { _Pragma("unroll") for (int m = 0; m < 4; ++m) _Pragma("unroll") for (int k = 0; k < 2; ++k) dst[m][k] = *(const PG8_LAS bf16x8*)(lds + PG8_SA(b, h) + aoff + m * 2048 + k * 1024); } while (0)
; #define PG8_LDB(dst, b, h) do { _Pragma("unroll") for (int n = 0; n < 2; ++n) _Pragma("unroll") for (int k = 0; k < 2; ++k) dst[n][k] = *(const PG8_LAS bf16x8*)(lds + PG8_SB(b, h) + boff + n * 2048 + k * 1024); } while (0)
; #define PG8_MMA(ai, bj, At, Bt) do { __builtin_amdgcn_s_setprio(1); _Pragma("unroll") for (int m = 0; m < 4; ++m) _Pragma("unroll") for (int n = 0; n < 2; ++n) _Pragma("unroll") for (int k = 0; k < 2; ++k) \
;         acc[ai][bj][m][n] = __builtin_amdgcn_mfma_f32_16x16x32_bf16(Bt[n][k], At[m][k], acc[ai][bj][m][n], 0, 0, 0); __builtin_amdgcn_s_setprio(0); } while (0)
; #define PG8_WAIT_V(n) asm volatile("s_waitcnt vmcnt(" #n ")" ::: "memory")
; #define PG8_WAIT_L(n) asm volatile("s_waitcnt lgkmcnt(" #n ")" ::: "memory")
; #define PG8_BAR __builtin_amdgcn_s_barrier()
; template <class Epi, class Sched, class AM, bool ALIGN_EPI = false, bool SP2 = false>
; __device__ __forceinline__ void gemm_phase(PG8_LAS unsigned char* lds, const Gemm g, const Sched& S, const Epi& E, const AM& am, const int wid_in) {
;     ...
;             if constexpr (SP2) {
;             PG8_LDB(B0, 0, 0); PG8_LDB(B1, 0, 1); PG8_SCHED; PG8_LDA(At, 0, 0); PG8_STAGE_A(1, 1, a1, false);
;             PG8_WAIT_V(8); PG8_WAIT_L(0); PG8_BAR; PG8_MMA(0, 0, At, B0); PG8_MMA(0, 1, At, B1); PG8_BAR; PG8_SCHED;
;             PG8_LDA(At, 0, 1); PG8_STAGE(PG8_SB(0, 0), b2, voffB); PG8_STAGE(PG8_SB(0, 1), b2 + hstep, voffB); PG8_STAGE_A(0, 0, a2, last);
;             PG8_WAIT_V(8); PG8_WAIT_L(0); PG8_BAR; PG8_MMA(1, 0, At, B0); PG8_MMA(1, 1, At, B1); PG8_BAR; PG8_SCHED;
.LBB0_847:
	ds_read_b128 v[152:155], v148
	ds_read_b128 v[156:159], v148 offset:1024
	ds_read_b128 v[160:163], v148 offset:2048
	ds_read_b128 v[164:167], v148 offset:3072
	ds_read_b128 v[168:171], v149
	ds_read_b128 v[172:175], v149 offset:1024
	ds_read_b128 v[176:179], v149 offset:2048
	ds_read_b128 v[180:183], v149 offset:3072
	s_add_u32 s26, s24, 0xfffc0080
	s_addc_u32 s27, s25, -1
	s_cmp_eq_u32 s57, 12
	s_cselect_b32 s29, s17, s27
	s_cselect_b32 s28, s52, s26
	s_cselect_b32 s27, s15, s56
	s_cselect_b32 s26, s53, s55
	s_add_i32 m0, s21, 0xc000
	ds_read_b128 v[184:187], v150
	ds_read_b128 v[188:191], v150 offset:1024
	ds_read_b128 v[192:195], v150 offset:2048
	ds_read_b128 v[196:199], v150 offset:3072
	ds_read_b128 v[200:203], v150 offset:4096
	ds_read_b128 v[204:207], v150 offset:5120
	ds_read_b128 v[208:211], v150 offset:6144
	ds_read_b128 v[212:215], v150 offset:7168
	global_load_lds_dwordx4 v136, s[24:25]
	s_add_i32 m0, s21, 0xe000
	s_nop 0
	global_load_lds_dwordx4 v138, s[24:25]
	s_waitcnt vmcnt(8)
	s_waitcnt lgkmcnt(0)
	s_barrier
	s_setprio 1
	s_waitcnt lgkmcnt(0)
	v_mfma_f32_16x16x32_bf16 v[124:127], v[152:155], v[184:187], v[124:127]
	v_mfma_f32_16x16x32_bf16 v[120:123], v[160:163], v[184:187], v[120:123]
	v_mfma_f32_16x16x32_bf16 v[108:111], v[152:155], v[192:195], v[108:111]
	v_mfma_f32_16x16x32_bf16 v[104:107], v[160:163], v[192:195], v[104:107]
	v_mfma_f32_16x16x32_bf16 v[92:95], v[152:155], v[200:203], v[92:95]
	v_mfma_f32_16x16x32_bf16 v[88:91], v[160:163], v[200:203], v[88:91]
	v_mfma_f32_16x16x32_bf16 v[76:79], v[152:155], v[208:211], v[76:79]
	v_mfma_f32_16x16x32_bf16 v[72:75], v[160:163], v[208:211], v[72:75]
	v_mfma_f32_16x16x32_bf16 v[124:127], v[156:159], v[188:191], v[124:127]
	v_mfma_f32_16x16x32_bf16 v[120:123], v[164:167], v[188:191], v[120:123]
	v_mfma_f32_16x16x32_bf16 v[108:111], v[156:159], v[196:199], v[108:111]
	v_mfma_f32_16x16x32_bf16 v[104:107], v[164:167], v[196:199], v[104:107]
	v_mfma_f32_16x16x32_bf16 v[92:95], v[156:159], v[204:207], v[92:95]
	v_mfma_f32_16x16x32_bf16 v[88:91], v[164:167], v[204:207], v[88:91]
	v_mfma_f32_16x16x32_bf16 v[76:79], v[156:159], v[212:215], v[76:79]
	v_mfma_f32_16x16x32_bf16 v[72:75], v[164:167], v[212:215], v[72:75]
	s_setprio 0
	s_setprio 1
	v_mfma_f32_16x16x32_bf16 v[116:119], v[168:171], v[184:187], v[116:119]
	v_mfma_f32_16x16x32_bf16 v[112:115], v[176:179], v[184:187], v[112:115]
	v_mfma_f32_16x16x32_bf16 v[100:103], v[168:171], v[192:195], v[100:103]
	v_mfma_f32_16x16x32_bf16 v[96:99], v[176:179], v[192:195], v[96:99]
	v_mfma_f32_16x16x32_bf16 v[84:87], v[168:171], v[200:203], v[84:87]
	v_mfma_f32_16x16x32_bf16 v[80:83], v[176:179], v[200:203], v[80:83]
	v_mfma_f32_16x16x32_bf16 v[68:71], v[168:171], v[208:211], v[68:71]
	v_mfma_f32_16x16x32_bf16 v[64:67], v[176:179], v[208:211], v[64:67]
	v_mfma_f32_16x16x32_bf16 v[116:119], v[172:175], v[188:191], v[116:119]
	v_mfma_f32_16x16x32_bf16 v[112:115], v[180:183], v[188:191], v[112:115]
	v_mfma_f32_16x16x32_bf16 v[100:103], v[172:175], v[196:199], v[100:103]
	v_mfma_f32_16x16x32_bf16 v[96:99], v[180:183], v[196:199], v[96:99]
	v_mfma_f32_16x16x32_bf16 v[84:87], v[172:175], v[204:207], v[84:87]
	v_mfma_f32_16x16x32_bf16 v[80:83], v[180:183], v[204:207], v[80:83]
	v_mfma_f32_16x16x32_bf16 v[68:71], v[172:175], v[212:215], v[68:71]
	v_mfma_f32_16x16x32_bf16 v[64:67], v[180:183], v[212:215], v[64:67]
	s_setprio 0
	s_barrier
	s_add_u32 s98, s26, s10
	s_addc_u32 s99, s27, s11
	s_add_u32 s100, s28, s10
	s_addc_u32 s101, s29, s11
	s_add_i32 s58, s46, s36
	s_mov_b32 m0, s58
	ds_read_b128 v[184:187], v150 offset:16384
	ds_read_b128 v[188:191], v150 offset:17408
	ds_read_b128 v[192:195], v150 offset:18432
	ds_read_b128 v[196:199], v150 offset:19456
	ds_read_b128 v[200:203], v150 offset:20480
	ds_read_b128 v[204:207], v150 offset:21504
	ds_read_b128 v[208:211], v150 offset:22528
	ds_read_b128 v[212:215], v150 offset:23552
	global_load_lds_dwordx4 v132, s[26:27]
	s_add_i32 m0, s58, 0x2000
	s_add_u32 s58, s26, 0x40000
	s_addc_u32 s59, s27, 0
	s_add_i32 s60, s47, s36
	global_load_lds_dwordx4 v128, s[26:27]
	s_mov_b32 m0, s60
	s_nop 0
	global_load_lds_dwordx4 v132, s[58:59]
	s_add_i32 m0, s60, 0x2000
	s_nop 0
	global_load_lds_dwordx4 v128, s[58:59]
	s_mov_b32 m0, s21
	s_nop 0
	global_load_lds_dwordx4 v134, s[28:29]
	s_mov_b32 m0, s37
	s_nop 0
	global_load_lds_dwordx4 v130, s[28:29]
	s_waitcnt vmcnt(8)
	s_waitcnt lgkmcnt(0)
	s_barrier
	s_setprio 1
	s_waitcnt lgkmcnt(0)
	v_mfma_f32_16x16x32_bf16 v[60:63], v[152:155], v[184:187], v[60:63]
	v_mfma_f32_16x16x32_bf16 v[56:59], v[160:163], v[184:187], v[56:59]
	v_mfma_f32_16x16x32_bf16 v[44:47], v[152:155], v[192:195], v[44:47]
	v_mfma_f32_16x16x32_bf16 v[40:43], v[160:163], v[192:195], v[40:43]
	v_mfma_f32_16x16x32_bf16 v[28:31], v[152:155], v[200:203], v[28:31]
	v_mfma_f32_16x16x32_bf16 v[24:27], v[160:163], v[200:203], v[24:27]
	v_mfma_f32_16x16x32_bf16 v[12:15], v[152:155], v[208:211], v[12:15]
	v_mfma_f32_16x16x32_bf16 v[8:11], v[160:163], v[208:211], v[8:11]
	v_mfma_f32_16x16x32_bf16 v[60:63], v[156:159], v[188:191], v[60:63]
	v_mfma_f32_16x16x32_bf16 v[56:59], v[164:167], v[188:191], v[56:59]
	v_mfma_f32_16x16x32_bf16 v[44:47], v[156:159], v[196:199], v[44:47]
	v_mfma_f32_16x16x32_bf16 v[40:43], v[164:167], v[196:199], v[40:43]
	v_mfma_f32_16x16x32_bf16 v[28:31], v[156:159], v[204:207], v[28:31]
	v_mfma_f32_16x16x32_bf16 v[24:27], v[164:167], v[204:207], v[24:27]
	v_mfma_f32_16x16x32_bf16 v[12:15], v[156:159], v[212:215], v[12:15]
	v_mfma_f32_16x16x32_bf16 v[8:11], v[164:167], v[212:215], v[8:11]
	s_setprio 0
	s_setprio 1
	v_mfma_f32_16x16x32_bf16 v[52:55], v[168:171], v[184:187], v[52:55]
	v_mfma_f32_16x16x32_bf16 v[48:51], v[176:179], v[184:187], v[48:51]
	v_mfma_f32_16x16x32_bf16 v[36:39], v[168:171], v[192:195], v[36:39]
	v_mfma_f32_16x16x32_bf16 v[32:35], v[176:179], v[192:195], v[32:35]
	v_mfma_f32_16x16x32_bf16 v[20:23], v[168:171], v[200:203], v[20:23]
	v_mfma_f32_16x16x32_bf16 v[16:19], v[176:179], v[200:203], v[16:19]
	v_mfma_f32_16x16x32_bf16 v[4:7], v[168:171], v[208:211], v[4:7]
	v_mfma_f32_16x16x32_bf16 v[0:3], v[176:179], v[208:211], v[0:3]
	v_mfma_f32_16x16x32_bf16 v[52:55], v[172:175], v[188:191], v[52:55]
	v_mfma_f32_16x16x32_bf16 v[48:51], v[180:183], v[188:191], v[48:51]
	v_mfma_f32_16x16x32_bf16 v[36:39], v[172:175], v[196:199], v[36:39]
	v_mfma_f32_16x16x32_bf16 v[32:35], v[180:183], v[196:199], v[32:35]
	v_mfma_f32_16x16x32_bf16 v[20:23], v[172:175], v[204:207], v[20:23]
	v_mfma_f32_16x16x32_bf16 v[16:19], v[180:183], v[204:207], v[16:19]
	v_mfma_f32_16x16x32_bf16 v[4:7], v[172:175], v[212:215], v[4:7]
	v_mfma_f32_16x16x32_bf16 v[0:3], v[180:183], v[212:215], v[0:3]
	s_setprio 0
	s_barrier
; #define PG8_STAGE(bufoff, gbase, voff) do { _Pragma("unroll") for (int _i = 0; _i < 2; ++_i) \
;         __builtin_amdgcn_global_load_lds((const unsigned*)((const char*)(gbase) + (voff)[_i]), (PG8_LAS unsigned*)(lds + (bufoff) + ldsw + _i * 8192), 16, 0, 0); } while (0)
; #define PG8_STAGE_A(b, h, gbase, NX) do { if constexpr (AM::GATHER) { const unsigned so_[2] = {(NX) ? gno[h][0] : gao[h][0], (NX) ? gno[h][1] : gao[h][1]}; PG8_STAGE(PG8_SA(b, h), gbase, so_); } \
;         else { PG8_STAGE(PG8_SA(b, h), (gbase) + (h) * hstep, voffA); } } while (0)
; #define PG8_LDA(dst, b, h) do { _Pragma("unroll") for (int m = 0; m < 4; ++m) _Pragma("unroll") for (int k = 0; k < 2; ++k) dst[m][k] = *(const PG8_LAS bf16x8*)(lds + PG8_SA(b, h) + aoff + m * 2048 + k * 1024); } while (0)
; #define PG8_LDB(dst, b, h) do { _Pragma("unroll") for (int n = 0; n < 2; ++n) _Pragma("unroll") for (int k = 0; k < 2; ++k) dst[n][k] = *(const PG8_LAS bf16x8*)(lds + PG8_SB(b, h) + boff + n * 2048 + k * 1024); } while (0)
; #define PG8_MMA(ai, bj, At, Bt) do { __builtin_amdgcn_s_setprio(1); _Pragma("unroll") for (int m = 0; m < 4; ++m) _Pragma("unroll") for (int n = 0; n < 2; ++n) _Pragma("unroll") for (int k = 0; k < 2; ++k) \
;         acc[ai][bj][m][n] = __builtin_amdgcn_mfma_f32_16x16x32_bf16(Bt[n][k], At[m][k], acc[ai][bj][m][n], 0, 0, 0); __builtin_amdgcn_s_setprio(0); } while (0)
; #define PG8_WAIT_V(n) asm volatile("s_waitcnt vmcnt(" #n ")" ::: "memory")
; #define PG8_WAIT_L(n) asm volatile("s_waitcnt lgkmcnt(" #n ")" ::: "memory")
; #define PG8_BAR __builtin_amdgcn_s_barrier()
; #define PG8_SCHED __builtin_amdgcn_sched_barrier(0)
; template <class Epi, class Sched, class AM, bool ALIGN_EPI = false, bool SP2 = false>
; __device__ __forceinline__ void gemm_phase(PG8_LAS unsigned char* lds, const Gemm g, const Sched& S, const Epi& E, const AM& am, const int wid_in) {
;     ...
;             PG8_LDB(B0, 1, 0); PG8_LDB(B1, 1, 1); PG8_SCHED; PG8_LDA(At, 1, 0); PG8_STAGE_A(0, 1, a2, last);
;             PG8_WAIT_V(8); PG8_WAIT_L(0); PG8_BAR; PG8_MMA(0, 0, At, B0); PG8_MMA(0, 1, At, B1); PG8_BAR; PG8_SCHED;
;             PG8_LDA(At, 1, 1); PG8_STAGE(PG8_SB(1, 0), b3, voffB); PG8_STAGE(PG8_SB(1, 1), b3 + hstep, voffB); PG8_STAGE_A(1, 0, a3, last);
;             PG8_WAIT_V(8); PG8_WAIT_L(0); PG8_BAR; PG8_MMA(1, 0, At, B0); PG8_MMA(1, 1, At, B1); PG8_BAR; PG8_SCHED;
	s_add_i32 s58, 0, 0x18000
	v_add_u32_e32 v151, s58, v144
	s_add_i32 s59, 0, 0x1c000
	ds_read_b128 v[152:155], v151
	ds_read_b128 v[156:159], v151 offset:1024
	ds_read_b128 v[160:163], v151 offset:2048
	ds_read_b128 v[164:167], v151 offset:3072
	v_add_u32_e32 v151, s59, v144
	ds_read_b128 v[168:171], v151
	ds_read_b128 v[172:175], v151 offset:1024
	ds_read_b128 v[176:179], v151 offset:2048
	ds_read_b128 v[180:183], v151 offset:3072
	s_add_u32 s28, s28, 0x40000
	s_addc_u32 s29, s29, 0
	s_mov_b32 m0, s38
	ds_read_b128 v[184:187], v150 offset:32768
	ds_read_b128 v[188:191], v150 offset:33792
	ds_read_b128 v[192:195], v150 offset:34816
	ds_read_b128 v[196:199], v150 offset:35840
	ds_read_b128 v[200:203], v150 offset:36864
	ds_read_b128 v[204:207], v150 offset:37888
	ds_read_b128 v[208:211], v150 offset:38912
	ds_read_b128 v[212:215], v150 offset:39936
	global_load_lds_dwordx4 v134, s[28:29]
	s_mov_b32 m0, s39
	s_nop 0
	global_load_lds_dwordx4 v130, s[28:29]
	s_waitcnt vmcnt(8)
	s_waitcnt lgkmcnt(0)
	s_barrier
	s_setprio 1
	s_waitcnt lgkmcnt(0)
	v_mfma_f32_16x16x32_bf16 v[124:127], v[152:155], v[184:187], v[124:127]
	v_mfma_f32_16x16x32_bf16 v[120:123], v[160:163], v[184:187], v[120:123]
	v_mfma_f32_16x16x32_bf16 v[108:111], v[152:155], v[192:195], v[108:111]
	v_mfma_f32_16x16x32_bf16 v[104:107], v[160:163], v[192:195], v[104:107]
	v_mfma_f32_16x16x32_bf16 v[92:95], v[152:155], v[200:203], v[92:95]
	v_mfma_f32_16x16x32_bf16 v[88:91], v[160:163], v[200:203], v[88:91]
	v_mfma_f32_16x16x32_bf16 v[76:79], v[152:155], v[208:211], v[76:79]
	v_mfma_f32_16x16x32_bf16 v[72:75], v[160:163], v[208:211], v[72:75]
	v_mfma_f32_16x16x32_bf16 v[124:127], v[156:159], v[188:191], v[124:127]
	v_mfma_f32_16x16x32_bf16 v[120:123], v[164:167], v[188:191], v[120:123]
	v_mfma_f32_16x16x32_bf16 v[108:111], v[156:159], v[196:199], v[108:111]
	v_mfma_f32_16x16x32_bf16 v[104:107], v[164:167], v[196:199], v[104:107]
	v_mfma_f32_16x16x32_bf16 v[92:95], v[156:159], v[204:207], v[92:95]
	v_mfma_f32_16x16x32_bf16 v[88:91], v[164:167], v[204:207], v[88:91]
	v_mfma_f32_16x16x32_bf16 v[76:79], v[156:159], v[212:215], v[76:79]
	v_mfma_f32_16x16x32_bf16 v[72:75], v[164:167], v[212:215], v[72:75]
	s_setprio 0
	s_setprio 1
	v_mfma_f32_16x16x32_bf16 v[116:119], v[168:171], v[184:187], v[116:119]
	v_mfma_f32_16x16x32_bf16 v[112:115], v[176:179], v[184:187], v[112:115]
	v_mfma_f32_16x16x32_bf16 v[100:103], v[168:171], v[192:195], v[100:103]
	v_mfma_f32_16x16x32_bf16 v[96:99], v[176:179], v[192:195], v[96:99]
	v_mfma_f32_16x16x32_bf16 v[84:87], v[168:171], v[200:203], v[84:87]
	v_mfma_f32_16x16x32_bf16 v[80:83], v[176:179], v[200:203], v[80:83]
	v_mfma_f32_16x16x32_bf16 v[68:71], v[168:171], v[208:211], v[68:71]
	v_mfma_f32_16x16x32_bf16 v[64:67], v[176:179], v[208:211], v[64:67]
	v_mfma_f32_16x16x32_bf16 v[116:119], v[172:175], v[188:191], v[116:119]
	v_mfma_f32_16x16x32_bf16 v[112:115], v[180:183], v[188:191], v[112:115]
	v_mfma_f32_16x16x32_bf16 v[100:103], v[172:175], v[196:199], v[100:103]
	v_mfma_f32_16x16x32_bf16 v[96:99], v[180:183], v[196:199], v[96:99]
	v_mfma_f32_16x16x32_bf16 v[84:87], v[172:175], v[204:207], v[84:87]
	v_mfma_f32_16x16x32_bf16 v[80:83], v[180:183], v[204:207], v[80:83]
	v_mfma_f32_16x16x32_bf16 v[68:71], v[172:175], v[212:215], v[68:71]
	v_mfma_f32_16x16x32_bf16 v[64:67], v[180:183], v[212:215], v[64:67]
	s_setprio 0
	s_barrier
	s_add_i32 s28, s58, s36
	s_mov_b32 m0, s28
	ds_read_b128 v[184:187], v150 offset:49152
	ds_read_b128 v[188:191], v150 offset:50176
	ds_read_b128 v[192:195], v150 offset:51200
	ds_read_b128 v[196:199], v150 offset:52224
	ds_read_b128 v[200:203], v150 offset:53248
	ds_read_b128 v[204:207], v150 offset:54272
	ds_read_b128 v[208:211], v150 offset:55296
	ds_read_b128 v[212:215], v150 offset:56320
	global_load_lds_dwordx4 v132, s[98:99]
	s_add_i32 m0, s28, 0x2000
	s_add_u32 s26, s26, 0x40080
	s_addc_u32 s27, s27, 0
	s_add_i32 s28, s59, s36
	global_load_lds_dwordx4 v128, s[98:99]
	s_mov_b32 m0, s28
	s_nop 0
	global_load_lds_dwordx4 v132, s[26:27]
	s_add_i32 m0, s28, 0x2000
	s_nop 0
	global_load_lds_dwordx4 v128, s[26:27]
	s_mov_b32 m0, s42
	s_nop 0
	global_load_lds_dwordx4 v134, s[100:101]
	s_mov_b32 m0, s43
	s_nop 0
	global_load_lds_dwordx4 v130, s[100:101]
	s_waitcnt vmcnt(8)
	s_waitcnt lgkmcnt(0)
	s_barrier
	s_setprio 1
	s_waitcnt lgkmcnt(0)
	v_mfma_f32_16x16x32_bf16 v[60:63], v[152:155], v[184:187], v[60:63]
	v_mfma_f32_16x16x32_bf16 v[56:59], v[160:163], v[184:187], v[56:59]
	v_mfma_f32_16x16x32_bf16 v[44:47], v[152:155], v[192:195], v[44:47]
	v_mfma_f32_16x16x32_bf16 v[40:43], v[160:163], v[192:195], v[40:43]
	v_mfma_f32_16x16x32_bf16 v[28:31], v[152:155], v[200:203], v[28:31]
	v_mfma_f32_16x16x32_bf16 v[24:27], v[160:163], v[200:203], v[24:27]
	v_mfma_f32_16x16x32_bf16 v[12:15], v[152:155], v[208:211], v[12:15]
	v_mfma_f32_16x16x32_bf16 v[8:11], v[160:163], v[208:211], v[8:11]
	v_mfma_f32_16x16x32_bf16 v[60:63], v[156:159], v[188:191], v[60:63]
	v_mfma_f32_16x16x32_bf16 v[56:59], v[164:167], v[188:191], v[56:59]
	v_mfma_f32_16x16x32_bf16 v[44:47], v[156:159], v[196:199], v[44:47]
	v_mfma_f32_16x16x32_bf16 v[40:43], v[164:167], v[196:199], v[40:43]
	v_mfma_f32_16x16x32_bf16 v[28:31], v[156:159], v[204:207], v[28:31]
	v_mfma_f32_16x16x32_bf16 v[24:27], v[164:167], v[204:207], v[24:27]
	v_mfma_f32_16x16x32_bf16 v[12:15], v[156:159], v[212:215], v[12:15]
	v_mfma_f32_16x16x32_bf16 v[8:11], v[164:167], v[212:215], v[8:11]
	s_setprio 0
	s_setprio 1
	v_mfma_f32_16x16x32_bf16 v[52:55], v[168:171], v[184:187], v[52:55]
	v_mfma_f32_16x16x32_bf16 v[48:51], v[176:179], v[184:187], v[48:51]
	v_mfma_f32_16x16x32_bf16 v[36:39], v[168:171], v[192:195], v[36:39]
	v_mfma_f32_16x16x32_bf16 v[32:35], v[176:179], v[192:195], v[32:35]
	v_mfma_f32_16x16x32_bf16 v[20:23], v[168:171], v[200:203], v[20:23]
	v_mfma_f32_16x16x32_bf16 v[16:19], v[176:179], v[200:203], v[16:19]
	v_mfma_f32_16x16x32_bf16 v[4:7], v[168:171], v[208:211], v[4:7]
	v_mfma_f32_16x16x32_bf16 v[0:3], v[176:179], v[208:211], v[0:3]
	v_mfma_f32_16x16x32_bf16 v[52:55], v[172:175], v[188:191], v[52:55]
	v_mfma_f32_16x16x32_bf16 v[48:51], v[180:183], v[188:191], v[48:51]
	v_mfma_f32_16x16x32_bf16 v[36:39], v[172:175], v[196:199], v[36:39]
	v_mfma_f32_16x16x32_bf16 v[32:35], v[180:183], v[196:199], v[32:35]
	v_mfma_f32_16x16x32_bf16 v[20:23], v[172:175], v[204:207], v[20:23]
	v_mfma_f32_16x16x32_bf16 v[16:19], v[180:183], v[204:207], v[16:19]
	v_mfma_f32_16x16x32_bf16 v[4:7], v[172:175], v[212:215], v[4:7]
	v_mfma_f32_16x16x32_bf16 v[0:3], v[180:183], v[212:215], v[0:3]
	s_setprio 0
	s_barrier
	s_add_i32 s57, s57, 2
	s_add_u32 s24, s24, 0x100
	s_addc_u32 s25, s25, 0
	s_add_u32 s55, s55, 0x100
	s_addc_u32 s56, s56, 0
	s_cmp_gt_u32 s57, 13
	s_cbranch_scc0 .LBB0_847
	s_and_b64 vcc, exec, s[12:13]
	s_cbranch_vccz .LBB0_850
	s_barrier

; #define PG8_STAGE(bufoff, gbase, voff) do { _Pragma("unroll") for (int _i = 0; _i < 2; ++_i) \
;         __builtin_amdgcn_global_load_lds((const unsigned*)((const char*)(gbase) + (voff)[_i]), (PG8_LAS unsigned*)(lds + (bufoff) + ldsw + _i * 8192), 16, 0, 0); } while (0)
; #define PG8_STAGE_A(b, h, gbase, NX) do { if constexpr (AM::GATHER) { const unsigned so_[2] = {(NX) ? gno[h][0] : gao[h][0], (NX) ? gno[h][1] : gao[h][1]}; PG8_STAGE(PG8_SA(b, h), gbase, so_); } \
;         else { PG8_STAGE(PG8_SA(b, h), (gbase) + (h) * hstep, voffA); } } while (0)
; #define PG8_LDA(dst, b, h) do { _Pragma("unroll") for (int m = 0; m < 4; ++m) _Pragma("unroll") for (int k = 0; k < 2; ++k) dst[m][k] = *(const PG8_LAS bf16x8*)(lds + PG8_SA(b, h) + aoff + m * 2048 + k * 1024); } while (0)
; #define PG8_LDB(dst, b, h) do { _Pragma("unroll") for (int n = 0; n < 2; ++n) _Pragma("unroll") for (int k = 0; k < 2; ++k) dst[n][k] = *(const PG8_LAS bf16x8*)(lds + PG8_SB(b, h) + boff + n * 2048 + k * 1024); } while (0)
; #define PG8_MMA(ai, bj, At, Bt) do { __builtin_amdgcn_s_setprio(1); _Pragma("unroll") for (int m = 0; m < 4; ++m) _Pragma("unroll") for (int n = 0; n < 2; ++n) _Pragma("unroll") for (int k = 0; k < 2; ++k) \
;         acc[ai][bj][m][n] = __builtin_amdgcn_mfma_f32_16x16x32_bf16(Bt[n][k], At[m][k], acc[ai][bj][m][n], 0, 0, 0); __builtin_amdgcn_s_setprio(0); } while (0)
; #define PG8_WAIT_V(n) asm volatile("s_waitcnt vmcnt(" #n ")" ::: "memory")
; #define PG8_WAIT_L(n) asm volatile("s_waitcnt lgkmcnt(" #n ")" ::: "memory")
; #define PG8_BAR __builtin_amdgcn_s_barrier()
; template <class Epi, class Sched, class AM, bool ALIGN_EPI = false, bool SP2 = false>
; __device__ __forceinline__ void gemm_phase(PG8_LAS unsigned char* lds, const Gemm g, const Sched& S, const Epi& E, const AM& am, const int wid_in) {
;     ...
;             if constexpr (SP2) {
;             PG8_LDB(B0, 0, 0); PG8_LDB(B1, 0, 1); PG8_SCHED; PG8_LDA(At, 0, 0); PG8_STAGE_A(1, 1, a1, false);
;             PG8_WAIT_V(8); PG8_WAIT_L(0); PG8_BAR; PG8_MMA(0, 0, At, B0); PG8_MMA(0, 1, At, B1); PG8_BAR; PG8_SCHED;
;             PG8_LDA(At, 0, 1); PG8_STAGE(PG8_SB(0, 0), b2, voffB); PG8_STAGE(PG8_SB(0, 1), b2 + hstep, voffB); PG8_STAGE_A(0, 0, a2, last);
;             PG8_WAIT_V(8); PG8_WAIT_L(0); PG8_BAR; PG8_MMA(1, 0, At, B0); PG8_MMA(1, 1, At, B1); PG8_BAR; PG8_SCHED;
.LBB0_947:
	ds_read_b128 v[114:117], v222
	ds_read_b128 v[118:121], v222 offset:1024
	ds_read_b128 v[122:125], v222 offset:2048
	ds_read_b128 v[130:133], v222 offset:3072
	ds_read_b128 v[134:137], v223
	ds_read_b128 v[138:141], v223 offset:1024
	ds_read_b128 v[150:153], v223 offset:2048
	ds_read_b128 v[158:161], v223 offset:3072
	s_add_u32 s14, s12, 0xfffc0080
	s_addc_u32 s15, s13, -1
	s_cmp_eq_u32 s52, 12
	s_cselect_b32 s17, s43, s15
	s_cselect_b32 s16, s48, s14
	s_cselect_b32 s15, s41, s51
	s_cselect_b32 s14, s49, s50
	s_add_i32 m0, s60, 0xc000
	ds_read_b128 v[162:165], v224
	ds_read_b128 v[166:169], v224 offset:1024
	ds_read_b128 v[170:173], v224 offset:2048
	ds_read_b128 v[174:177], v224 offset:3072
	ds_read_b128 v[178:181], v224 offset:4096
	ds_read_b128 v[182:185], v224 offset:5120
	ds_read_b128 v[186:189], v224 offset:6144
	ds_read_b128 v[190:193], v224 offset:7168
	global_load_lds_dwordx4 v204, s[12:13]
	s_add_i32 m0, s60, 0xe000
	s_nop 0
	global_load_lds_dwordx4 v206, s[12:13]
	s_waitcnt vmcnt(8)
	s_waitcnt lgkmcnt(0)
	s_barrier
	s_setprio 1
	s_waitcnt lgkmcnt(0)
	v_mfma_f32_16x16x32_bf16 v[154:157], v[114:117], v[162:165], v[154:157]
	v_mfma_f32_16x16x32_bf16 v[146:149], v[122:125], v[162:165], v[146:149]
	v_mfma_f32_16x16x32_bf16 v[142:145], v[114:117], v[170:173], v[142:145]
	v_mfma_f32_16x16x32_bf16 v[126:129], v[122:125], v[170:173], v[126:129]
	v_mfma_f32_16x16x32_bf16 v[110:113], v[114:117], v[178:181], v[110:113]
	v_mfma_f32_16x16x32_bf16 v[106:109], v[122:125], v[178:181], v[106:109]
	v_mfma_f32_16x16x32_bf16 v[102:105], v[114:117], v[186:189], v[102:105]
	v_mfma_f32_16x16x32_bf16 v[98:101], v[122:125], v[186:189], v[98:101]
	v_mfma_f32_16x16x32_bf16 v[154:157], v[118:121], v[166:169], v[154:157]
	v_mfma_f32_16x16x32_bf16 v[146:149], v[130:133], v[166:169], v[146:149]
	v_mfma_f32_16x16x32_bf16 v[142:145], v[118:121], v[174:177], v[142:145]
	v_mfma_f32_16x16x32_bf16 v[126:129], v[130:133], v[174:177], v[126:129]
	v_mfma_f32_16x16x32_bf16 v[110:113], v[118:121], v[182:185], v[110:113]
	v_mfma_f32_16x16x32_bf16 v[106:109], v[130:133], v[182:185], v[106:109]
	v_mfma_f32_16x16x32_bf16 v[102:105], v[118:121], v[190:193], v[102:105]
	v_mfma_f32_16x16x32_bf16 v[98:101], v[130:133], v[190:193], v[98:101]
	s_setprio 0
	s_setprio 1
	v_mfma_f32_16x16x32_bf16 v[60:63], v[134:137], v[162:165], v[60:63]
	v_mfma_f32_16x16x32_bf16 v[56:59], v[150:153], v[162:165], v[56:59]
	v_mfma_f32_16x16x32_bf16 v[52:55], v[134:137], v[170:173], v[52:55]
	v_mfma_f32_16x16x32_bf16 v[48:51], v[150:153], v[170:173], v[48:51]
	v_mfma_f32_16x16x32_bf16 v[44:47], v[134:137], v[178:181], v[44:47]
	v_mfma_f32_16x16x32_bf16 v[40:43], v[150:153], v[178:181], v[40:43]
	v_mfma_f32_16x16x32_bf16 v[36:39], v[134:137], v[186:189], v[36:39]
	v_mfma_f32_16x16x32_bf16 v[32:35], v[150:153], v[186:189], v[32:35]
	v_mfma_f32_16x16x32_bf16 v[60:63], v[138:141], v[166:169], v[60:63]
	v_mfma_f32_16x16x32_bf16 v[56:59], v[158:161], v[166:169], v[56:59]
	v_mfma_f32_16x16x32_bf16 v[52:55], v[138:141], v[174:177], v[52:55]
	v_mfma_f32_16x16x32_bf16 v[48:51], v[158:161], v[174:177], v[48:51]
	v_mfma_f32_16x16x32_bf16 v[44:47], v[138:141], v[182:185], v[44:47]
	v_mfma_f32_16x16x32_bf16 v[40:43], v[158:161], v[182:185], v[40:43]
	v_mfma_f32_16x16x32_bf16 v[36:39], v[138:141], v[190:193], v[36:39]
	v_mfma_f32_16x16x32_bf16 v[32:35], v[158:161], v[190:193], v[32:35]
	s_setprio 0
	s_barrier
	s_add_u32 s98, s14, s30
	s_addc_u32 s99, s15, s31
	s_add_u32 s100, s16, s30
	s_addc_u32 s101, s17, s31
	s_add_i32 s53, s73, s59
	s_mov_b32 m0, s53
	ds_read_b128 v[162:165], v224 offset:16384
	ds_read_b128 v[166:169], v224 offset:17408
	ds_read_b128 v[170:173], v224 offset:18432
	ds_read_b128 v[174:177], v224 offset:19456
	ds_read_b128 v[178:181], v224 offset:20480
	ds_read_b128 v[182:185], v224 offset:21504
	ds_read_b128 v[186:189], v224 offset:22528
	ds_read_b128 v[190:193], v224 offset:23552
	global_load_lds_dwordx4 v198, s[14:15]
	s_add_i32 m0, s53, 0x2000
	s_add_u32 s76, s14, 0x40000
	s_addc_u32 s77, s15, 0
	s_add_i32 s53, s74, s59
	global_load_lds_dwordx4 v194, s[14:15]
	s_mov_b32 m0, s53
	s_nop 0
	global_load_lds_dwordx4 v198, s[76:77]
	s_add_i32 m0, s53, 0x2000
	s_nop 0
	global_load_lds_dwordx4 v194, s[76:77]
	s_mov_b32 m0, s60
	s_nop 0
	global_load_lds_dwordx4 v200, s[16:17]
	s_mov_b32 m0, s61
	s_nop 0
	global_load_lds_dwordx4 v196, s[16:17]
	s_waitcnt vmcnt(8)
	s_waitcnt lgkmcnt(0)
	s_barrier
	s_setprio 1
	s_waitcnt lgkmcnt(0)
	v_mfma_f32_16x16x32_bf16 v[94:97], v[114:117], v[162:165], v[94:97]
	v_mfma_f32_16x16x32_bf16 v[88:91], v[122:125], v[162:165], v[90:93]
	v_mfma_f32_16x16x32_bf16 v[84:87], v[114:117], v[170:173], v[84:87]
	v_mfma_f32_16x16x32_bf16 v[80:83], v[122:125], v[170:173], v[80:83]
	v_mfma_f32_16x16x32_bf16 v[76:79], v[114:117], v[178:181], v[76:79]
	v_mfma_f32_16x16x32_bf16 v[72:75], v[122:125], v[178:181], v[72:75]
	v_mfma_f32_16x16x32_bf16 v[68:71], v[114:117], v[186:189], v[68:71]
	v_mfma_f32_16x16x32_bf16 v[64:67], v[122:125], v[186:189], v[64:67]
	v_mfma_f32_16x16x32_bf16 v[94:97], v[118:121], v[166:169], v[94:97]
	v_mfma_f32_16x16x32_bf16 v[88:91], v[130:133], v[166:169], v[88:91]
	v_mfma_f32_16x16x32_bf16 v[84:87], v[118:121], v[174:177], v[84:87]
	v_mfma_f32_16x16x32_bf16 v[80:83], v[130:133], v[174:177], v[80:83]
	v_mfma_f32_16x16x32_bf16 v[76:79], v[118:121], v[182:185], v[76:79]
	v_mfma_f32_16x16x32_bf16 v[72:75], v[130:133], v[182:185], v[72:75]
	v_mfma_f32_16x16x32_bf16 v[68:71], v[118:121], v[190:193], v[68:71]
	v_mfma_f32_16x16x32_bf16 v[64:67], v[130:133], v[190:193], v[64:67]
	s_setprio 0
	s_setprio 1
	v_mfma_f32_16x16x32_bf16 v[28:31], v[134:137], v[162:165], v[28:31]
	v_mfma_f32_16x16x32_bf16 v[24:27], v[150:153], v[162:165], v[24:27]
	v_mfma_f32_16x16x32_bf16 v[20:23], v[134:137], v[170:173], v[20:23]
	v_mfma_f32_16x16x32_bf16 v[16:19], v[150:153], v[170:173], v[16:19]
	v_mfma_f32_16x16x32_bf16 v[12:15], v[134:137], v[178:181], v[12:15]
	v_mfma_f32_16x16x32_bf16 v[8:11], v[150:153], v[178:181], v[8:11]
	v_mfma_f32_16x16x32_bf16 v[4:7], v[134:137], v[186:189], v[4:7]
	v_mfma_f32_16x16x32_bf16 v[0:3], v[150:153], v[186:189], v[0:3]
	v_mfma_f32_16x16x32_bf16 v[28:31], v[138:141], v[166:169], v[28:31]
	v_mfma_f32_16x16x32_bf16 v[24:27], v[158:161], v[166:169], v[24:27]
	v_mfma_f32_16x16x32_bf16 v[20:23], v[138:141], v[174:177], v[20:23]
	v_mfma_f32_16x16x32_bf16 v[16:19], v[158:161], v[174:177], v[16:19]
	v_mfma_f32_16x16x32_bf16 v[12:15], v[138:141], v[182:185], v[12:15]
	v_mfma_f32_16x16x32_bf16 v[8:11], v[158:161], v[182:185], v[8:11]
	v_mfma_f32_16x16x32_bf16 v[4:7], v[138:141], v[190:193], v[4:7]
	v_mfma_f32_16x16x32_bf16 v[0:3], v[158:161], v[190:193], v[0:3]
	s_setprio 0
	s_barrier
; #define PG8_STAGE(bufoff, gbase, voff) do { _Pragma("unroll") for (int _i = 0; _i < 2; ++_i) \
;         __builtin_amdgcn_global_load_lds((const unsigned*)((const char*)(gbase) + (voff)[_i]), (PG8_LAS unsigned*)(lds + (bufoff) + ldsw + _i * 8192), 16, 0, 0); } while (0)
; #define PG8_STAGE_A(b, h, gbase, NX) do { if constexpr (AM::GATHER) { const unsigned so_[2] = {(NX) ? gno[h][0] : gao[h][0], (NX) ? gno[h][1] : gao[h][1]}; PG8_STAGE(PG8_SA(b, h), gbase, so_); } \
;         else { PG8_STAGE(PG8_SA(b, h), (gbase) + (h) * hstep, voffA); } } while (0)
; #define PG8_LDA(dst, b, h) do { _Pragma("unroll") for (int m = 0; m < 4; ++m) _Pragma("unroll") for (int k = 0; k < 2; ++k) dst[m][k] = *(const PG8_LAS bf16x8*)(lds + PG8_SA(b, h) + aoff + m * 2048 + k * 1024); } while (0)
; #define PG8_LDB(dst, b, h) do { _Pragma("unroll") for (int n = 0; n < 2; ++n) _Pragma("unroll") for (int k = 0; k < 2; ++k) dst[n][k] = *(const PG8_LAS bf16x8*)(lds + PG8_SB(b, h) + boff + n * 2048 + k * 1024); } while (0)
; #define PG8_MMA(ai, bj, At, Bt) do { __builtin_amdgcn_s_setprio(1); _Pragma("unroll") for (int m = 0; m < 4; ++m) _Pragma("unroll") for (int n = 0; n < 2; ++n) _Pragma("unroll") for (int k = 0; k < 2; ++k) \
;         acc[ai][bj][m][n] = __builtin_amdgcn_mfma_f32_16x16x32_bf16(Bt[n][k], At[m][k], acc[ai][bj][m][n], 0, 0, 0); __builtin_amdgcn_s_setprio(0); } while (0)
; #define PG8_WAIT_V(n) asm volatile("s_waitcnt vmcnt(" #n ")" ::: "memory")
; #define PG8_WAIT_L(n) asm volatile("s_waitcnt lgkmcnt(" #n ")" ::: "memory")
; #define PG8_BAR __builtin_amdgcn_s_barrier()
; #define PG8_SCHED __builtin_amdgcn_sched_barrier(0)
; template <class Epi, class Sched, class AM, bool ALIGN_EPI = false, bool SP2 = false>
; __device__ __forceinline__ void gemm_phase(PG8_LAS unsigned char* lds, const Gemm g, const Sched& S, const Epi& E, const AM& am, const int wid_in) {
;     ...
;             PG8_LDB(B0, 1, 0); PG8_LDB(B1, 1, 1); PG8_SCHED; PG8_LDA(At, 1, 0); PG8_STAGE_A(0, 1, a2, last);
;             PG8_WAIT_V(8); PG8_WAIT_L(0); PG8_BAR; PG8_MMA(0, 0, At, B0); PG8_MMA(0, 1, At, B1); PG8_BAR; PG8_SCHED;
;             PG8_LDA(At, 1, 1); PG8_STAGE(PG8_SB(1, 0), b3, voffB); PG8_STAGE(PG8_SB(1, 1), b3 + hstep, voffB); PG8_STAGE_A(1, 0, a3, last);
;             PG8_WAIT_V(8); PG8_WAIT_L(0); PG8_BAR; PG8_MMA(1, 0, At, B0); PG8_MMA(1, 1, At, B1); PG8_BAR; PG8_SCHED;
	s_add_i32 s53, 0, 0x18000
	v_add_u32_e32 v92, s53, v218
	s_add_i32 s76, 0, 0x1c000
	ds_read_b128 v[114:117], v92
	ds_read_b128 v[118:121], v92 offset:1024
	ds_read_b128 v[122:125], v92 offset:2048
	ds_read_b128 v[130:133], v92 offset:3072
	v_add_u32_e32 v92, s76, v218
	ds_read_b128 v[134:137], v92
	ds_read_b128 v[138:141], v92 offset:1024
	ds_read_b128 v[150:153], v92 offset:2048
	ds_read_b128 v[158:161], v92 offset:3072
	s_add_u32 s16, s16, 0x40000
	s_addc_u32 s17, s17, 0
	s_mov_b32 m0, s62
	ds_read_b128 v[162:165], v224 offset:32768
	ds_read_b128 v[166:169], v224 offset:33792
	ds_read_b128 v[170:173], v224 offset:34816
	ds_read_b128 v[174:177], v224 offset:35840
	ds_read_b128 v[178:181], v224 offset:36864
	ds_read_b128 v[182:185], v224 offset:37888
	ds_read_b128 v[186:189], v224 offset:38912
	ds_read_b128 v[190:193], v224 offset:39936
	global_load_lds_dwordx4 v200, s[16:17]
	s_mov_b32 m0, s63
	s_nop 0
	global_load_lds_dwordx4 v196, s[16:17]
	s_waitcnt vmcnt(8)
	s_waitcnt lgkmcnt(0)
	s_barrier
	s_setprio 1
	s_waitcnt lgkmcnt(0)
	v_mfma_f32_16x16x32_bf16 v[154:157], v[114:117], v[162:165], v[154:157]
	v_mfma_f32_16x16x32_bf16 v[146:149], v[122:125], v[162:165], v[146:149]
	v_mfma_f32_16x16x32_bf16 v[142:145], v[114:117], v[170:173], v[142:145]
	v_mfma_f32_16x16x32_bf16 v[126:129], v[122:125], v[170:173], v[126:129]
	v_mfma_f32_16x16x32_bf16 v[110:113], v[114:117], v[178:181], v[110:113]
	v_mfma_f32_16x16x32_bf16 v[106:109], v[122:125], v[178:181], v[106:109]
	v_mfma_f32_16x16x32_bf16 v[102:105], v[114:117], v[186:189], v[102:105]
	v_mfma_f32_16x16x32_bf16 v[98:101], v[122:125], v[186:189], v[98:101]
	v_mfma_f32_16x16x32_bf16 v[154:157], v[118:121], v[166:169], v[154:157]
	v_mfma_f32_16x16x32_bf16 v[146:149], v[130:133], v[166:169], v[146:149]
	v_mfma_f32_16x16x32_bf16 v[142:145], v[118:121], v[174:177], v[142:145]
	v_mfma_f32_16x16x32_bf16 v[126:129], v[130:133], v[174:177], v[126:129]
	v_mfma_f32_16x16x32_bf16 v[110:113], v[118:121], v[182:185], v[110:113]
	v_mfma_f32_16x16x32_bf16 v[106:109], v[130:133], v[182:185], v[106:109]
	v_mfma_f32_16x16x32_bf16 v[102:105], v[118:121], v[190:193], v[102:105]
	v_mfma_f32_16x16x32_bf16 v[98:101], v[130:133], v[190:193], v[98:101]
	s_setprio 0
	s_setprio 1
	v_mfma_f32_16x16x32_bf16 v[60:63], v[134:137], v[162:165], v[60:63]
	v_mfma_f32_16x16x32_bf16 v[56:59], v[150:153], v[162:165], v[56:59]
	v_mfma_f32_16x16x32_bf16 v[52:55], v[134:137], v[170:173], v[52:55]
	v_mfma_f32_16x16x32_bf16 v[48:51], v[150:153], v[170:173], v[48:51]
	v_mfma_f32_16x16x32_bf16 v[44:47], v[134:137], v[178:181], v[44:47]
	v_mfma_f32_16x16x32_bf16 v[40:43], v[150:153], v[178:181], v[40:43]
	v_mfma_f32_16x16x32_bf16 v[36:39], v[134:137], v[186:189], v[36:39]
	v_mfma_f32_16x16x32_bf16 v[32:35], v[150:153], v[186:189], v[32:35]
	v_mfma_f32_16x16x32_bf16 v[60:63], v[138:141], v[166:169], v[60:63]
	v_mfma_f32_16x16x32_bf16 v[56:59], v[158:161], v[166:169], v[56:59]
	v_mfma_f32_16x16x32_bf16 v[52:55], v[138:141], v[174:177], v[52:55]
	v_mfma_f32_16x16x32_bf16 v[48:51], v[158:161], v[174:177], v[48:51]
	v_mfma_f32_16x16x32_bf16 v[44:47], v[138:141], v[182:185], v[44:47]
	v_mfma_f32_16x16x32_bf16 v[40:43], v[158:161], v[182:185], v[40:43]
	v_mfma_f32_16x16x32_bf16 v[36:39], v[138:141], v[190:193], v[36:39]
	v_mfma_f32_16x16x32_bf16 v[32:35], v[158:161], v[190:193], v[32:35]
	s_setprio 0
	s_barrier
	s_add_i32 s16, s53, s59
	s_mov_b32 m0, s16
	ds_read_b128 v[162:165], v224 offset:49152
	ds_read_b128 v[166:169], v224 offset:50176
	ds_read_b128 v[170:173], v224 offset:51200
	ds_read_b128 v[174:177], v224 offset:52224
	ds_read_b128 v[178:181], v224 offset:53248
	ds_read_b128 v[182:185], v224 offset:54272
	ds_read_b128 v[186:189], v224 offset:55296
	ds_read_b128 v[190:193], v224 offset:56320
	global_load_lds_dwordx4 v198, s[98:99]
	s_add_i32 m0, s16, 0x2000
	s_add_u32 s14, s14, 0x40080
	s_addc_u32 s15, s15, 0
	s_add_i32 s16, s76, s59
	global_load_lds_dwordx4 v194, s[98:99]
	s_mov_b32 m0, s16
	s_nop 0
	global_load_lds_dwordx4 v198, s[14:15]
	s_add_i32 m0, s16, 0x2000
	s_nop 0
	global_load_lds_dwordx4 v194, s[14:15]
	s_mov_b32 m0, s68
	s_nop 0
	global_load_lds_dwordx4 v200, s[100:101]
	s_mov_b32 m0, s69
	s_nop 0
	global_load_lds_dwordx4 v196, s[100:101]
	s_waitcnt vmcnt(8)
	s_waitcnt lgkmcnt(0)
	s_barrier
	s_setprio 1
	s_waitcnt lgkmcnt(0)
	v_mfma_f32_16x16x32_bf16 v[92:95], v[114:117], v[162:165], v[94:97]
	v_mfma_f32_16x16x32_bf16 v[88:91], v[122:125], v[162:165], v[88:91]
	v_mfma_f32_16x16x32_bf16 v[84:87], v[114:117], v[170:173], v[84:87]
	v_mfma_f32_16x16x32_bf16 v[80:83], v[122:125], v[170:173], v[80:83]
	v_mfma_f32_16x16x32_bf16 v[76:79], v[114:117], v[178:181], v[76:79]
	v_mfma_f32_16x16x32_bf16 v[72:75], v[122:125], v[178:181], v[72:75]
	v_mfma_f32_16x16x32_bf16 v[68:71], v[114:117], v[186:189], v[68:71]
	v_mfma_f32_16x16x32_bf16 v[64:67], v[122:125], v[186:189], v[64:67]
	v_mfma_f32_16x16x32_bf16 v[94:97], v[118:121], v[166:169], v[92:95]
	v_mfma_f32_16x16x32_bf16 v[90:93], v[130:133], v[166:169], v[88:91]
	v_mfma_f32_16x16x32_bf16 v[84:87], v[118:121], v[174:177], v[84:87]
	v_mfma_f32_16x16x32_bf16 v[80:83], v[130:133], v[174:177], v[80:83]
	v_mfma_f32_16x16x32_bf16 v[76:79], v[118:121], v[182:185], v[76:79]
	v_mfma_f32_16x16x32_bf16 v[72:75], v[130:133], v[182:185], v[72:75]
	v_mfma_f32_16x16x32_bf16 v[68:71], v[118:121], v[190:193], v[68:71]
	v_mfma_f32_16x16x32_bf16 v[64:67], v[130:133], v[190:193], v[64:67]
	s_setprio 0
	s_setprio 1
	v_mfma_f32_16x16x32_bf16 v[28:31], v[134:137], v[162:165], v[28:31]
	v_mfma_f32_16x16x32_bf16 v[24:27], v[150:153], v[162:165], v[24:27]
	v_mfma_f32_16x16x32_bf16 v[20:23], v[134:137], v[170:173], v[20:23]
	v_mfma_f32_16x16x32_bf16 v[16:19], v[150:153], v[170:173], v[16:19]
	v_mfma_f32_16x16x32_bf16 v[12:15], v[134:137], v[178:181], v[12:15]
	v_mfma_f32_16x16x32_bf16 v[8:11], v[150:153], v[178:181], v[8:11]
	v_mfma_f32_16x16x32_bf16 v[4:7], v[134:137], v[186:189], v[4:7]
	v_mfma_f32_16x16x32_bf16 v[0:3], v[150:153], v[186:189], v[0:3]
	v_mfma_f32_16x16x32_bf16 v[28:31], v[138:141], v[166:169], v[28:31]
	v_mfma_f32_16x16x32_bf16 v[24:27], v[158:161], v[166:169], v[24:27]
	v_mfma_f32_16x16x32_bf16 v[20:23], v[138:141], v[174:177], v[20:23]
	v_mfma_f32_16x16x32_bf16 v[16:19], v[158:161], v[174:177], v[16:19]
	v_mfma_f32_16x16x32_bf16 v[12:15], v[138:141], v[182:185], v[12:15]
	v_mfma_f32_16x16x32_bf16 v[8:11], v[158:161], v[182:185], v[8:11]
	v_mfma_f32_16x16x32_bf16 v[4:7], v[138:141], v[190:193], v[4:7]
	v_mfma_f32_16x16x32_bf16 v[0:3], v[158:161], v[190:193], v[0:3]
	s_setprio 0
	s_barrier
	s_add_i32 s52, s52, 2
	s_add_u32 s12, s12, 0x100
	s_addc_u32 s13, s13, 0
	s_add_u32 s50, s50, 0x100
	s_addc_u32 s51, s51, 0
	s_cmp_gt_u32 s52, 13
	s_cbranch_scc0 .LBB0_947
	s_and_b64 vcc, exec, s[34:35]
	s_cbranch_vccz .LBB0_950
	s_barrier

; #define PG8_STAGE(bufoff, gbase, voff) do { _Pragma("unroll") for (int _i = 0; _i < 2; ++_i) \
;         __builtin_amdgcn_global_load_lds((const unsigned*)((const char*)(gbase) + (voff)[_i]), (PG8_LAS unsigned*)(lds + (bufoff) + ldsw + _i * 8192), 16, 0, 0); } while (0)
; #define PG8_STAGE_A(b, h, gbase, NX) do { if constexpr (AM::GATHER) { const unsigned so_[2] = {(NX) ? gno[h][0] : gao[h][0], (NX) ? gno[h][1] : gao[h][1]}; PG8_STAGE(PG8_SA(b, h), gbase, so_); } \
;         else { PG8_STAGE(PG8_SA(b, h), (gbase) + (h) * hstep, voffA); } } while (0)
; #define PG8_LDA(dst, b, h) do { _Pragma("unroll") for (int m = 0; m < 4; ++m) _Pragma("unroll") for (int k = 0; k < 2; ++k) dst[m][k] = *(const PG8_LAS bf16x8*)(lds + PG8_SA(b, h) + aoff + m * 2048 + k * 1024); } while (0)
; #define PG8_LDB(dst, b, h) do { _Pragma("unroll") for (int n = 0; n < 2; ++n) _Pragma("unroll") for (int k = 0; k < 2; ++k) dst[n][k] = *(const PG8_LAS bf16x8*)(lds + PG8_SB(b, h) + boff + n * 2048 + k * 1024); } while (0)
; #define PG8_MMA(ai, bj, At, Bt) do { __builtin_amdgcn_s_setprio(1); _Pragma("unroll") for (int m = 0; m < 4; ++m) _Pragma("unroll") for (int n = 0; n < 2; ++n) _Pragma("unroll") for (int k = 0; k < 2; ++k) \
;         acc[ai][bj][m][n] = __builtin_amdgcn_mfma_f32_16x16x32_bf16(Bt[n][k], At[m][k], acc[ai][bj][m][n], 0, 0, 0); __builtin_amdgcn_s_setprio(0); } while (0)
; #define PG8_WAIT_V(n) asm volatile("s_waitcnt vmcnt(" #n ")" ::: "memory")
; #define PG8_WAIT_L(n) asm volatile("s_waitcnt lgkmcnt(" #n ")" ::: "memory")
; #define PG8_BAR __builtin_amdgcn_s_barrier()
; template <class Epi, class Sched, class AM, bool ALIGN_EPI = false, bool SP2 = false>
; __device__ __forceinline__ void gemm_phase(PG8_LAS unsigned char* lds, const Gemm g, const Sched& S, const Epi& E, const AM& am, const int wid_in) {
;     ...
;             if constexpr (SP2) {
;             PG8_LDB(B0, 0, 0); PG8_LDB(B1, 0, 1); PG8_SCHED; PG8_LDA(At, 0, 0); PG8_STAGE_A(1, 1, a1, false);
;             PG8_WAIT_V(8); PG8_WAIT_L(0); PG8_BAR; PG8_MMA(0, 0, At, B0); PG8_MMA(0, 1, At, B1); PG8_BAR; PG8_SCHED;
;             PG8_LDA(At, 0, 1); PG8_STAGE(PG8_SB(0, 0), b2, voffB); PG8_STAGE(PG8_SB(0, 1), b2 + hstep, voffB); PG8_STAGE_A(0, 0, a2, last);
;             PG8_WAIT_V(8); PG8_WAIT_L(0); PG8_BAR; PG8_MMA(1, 0, At, B0); PG8_MMA(1, 1, At, B1); PG8_BAR; PG8_SCHED;
.LBB0_1055:
	ds_read_b128 v[128:131], v175
	ds_read_b128 v[132:135], v175 offset:1024
	ds_read_b128 v[136:139], v175 offset:2048
	ds_read_b128 v[140:143], v175 offset:3072
	ds_read_b128 v[164:167], v176
	ds_read_b128 v[178:181], v176 offset:1024
	ds_read_b128 v[182:185], v176 offset:2048
	ds_read_b128 v[186:189], v176 offset:3072
	s_add_u32 s38, s36, 0xfffc0080
	s_addc_u32 s39, s37, -1
	s_cmp_eq_u32 s68, 12
	s_cselect_b32 s41, s27, s39
	s_cselect_b32 s40, s64, s38
	s_cselect_b32 s39, s25, s67
	s_cselect_b32 s38, s65, s66
	s_add_i32 m0, s35, 0xc000
	ds_read_b128 v[190:193], v177
	ds_read_b128 v[194:197], v177 offset:1024
	ds_read_b128 v[198:201], v177 offset:2048
	ds_read_b128 v[202:205], v177 offset:3072
	ds_read_b128 v[206:209], v177 offset:4096
	ds_read_b128 v[210:213], v177 offset:5120
	ds_read_b128 v[214:217], v177 offset:6144
	ds_read_b128 v[218:221], v177 offset:7168
	global_load_lds_dwordx4 v154, s[36:37]
	s_add_i32 m0, s35, 0xe000
	s_nop 0
	global_load_lds_dwordx4 v156, s[36:37]
	s_waitcnt vmcnt(8)
	s_waitcnt lgkmcnt(0)
	s_barrier
	s_setprio 1
	s_waitcnt lgkmcnt(0)
	v_mfma_f32_16x16x32_bf16 v[124:127], v[128:131], v[190:193], v[124:127]
	v_mfma_f32_16x16x32_bf16 v[120:123], v[136:139], v[190:193], v[120:123]
	v_mfma_f32_16x16x32_bf16 v[116:119], v[128:131], v[198:201], v[116:119]
	v_mfma_f32_16x16x32_bf16 v[112:115], v[136:139], v[198:201], v[112:115]
	v_mfma_f32_16x16x32_bf16 v[92:95], v[128:131], v[206:209], v[92:95]
	v_mfma_f32_16x16x32_bf16 v[88:91], v[136:139], v[206:209], v[88:91]
	v_mfma_f32_16x16x32_bf16 v[76:79], v[128:131], v[214:217], v[76:79]
	v_mfma_f32_16x16x32_bf16 v[72:75], v[136:139], v[214:217], v[72:75]
	v_mfma_f32_16x16x32_bf16 v[124:127], v[132:135], v[194:197], v[124:127]
	v_mfma_f32_16x16x32_bf16 v[120:123], v[140:143], v[194:197], v[120:123]
	v_mfma_f32_16x16x32_bf16 v[116:119], v[132:135], v[202:205], v[116:119]
	v_mfma_f32_16x16x32_bf16 v[112:115], v[140:143], v[202:205], v[112:115]
	v_mfma_f32_16x16x32_bf16 v[92:95], v[132:135], v[210:213], v[92:95]
	v_mfma_f32_16x16x32_bf16 v[88:91], v[140:143], v[210:213], v[88:91]
	v_mfma_f32_16x16x32_bf16 v[76:79], v[132:135], v[218:221], v[76:79]
	v_mfma_f32_16x16x32_bf16 v[72:75], v[140:143], v[218:221], v[72:75]
	s_setprio 0
	s_setprio 1
	v_mfma_f32_16x16x32_bf16 v[108:111], v[164:167], v[190:193], v[108:111]
	v_mfma_f32_16x16x32_bf16 v[104:107], v[182:185], v[190:193], v[104:107]
	v_mfma_f32_16x16x32_bf16 v[100:103], v[164:167], v[198:201], v[100:103]
	v_mfma_f32_16x16x32_bf16 v[96:99], v[182:185], v[198:201], v[96:99]
	v_mfma_f32_16x16x32_bf16 v[84:87], v[164:167], v[206:209], v[84:87]
	v_mfma_f32_16x16x32_bf16 v[80:83], v[182:185], v[206:209], v[80:83]
	v_mfma_f32_16x16x32_bf16 v[68:71], v[164:167], v[214:217], v[68:71]
	v_mfma_f32_16x16x32_bf16 v[64:67], v[182:185], v[214:217], v[64:67]
	v_mfma_f32_16x16x32_bf16 v[108:111], v[178:181], v[194:197], v[108:111]
	v_mfma_f32_16x16x32_bf16 v[104:107], v[186:189], v[194:197], v[104:107]
	v_mfma_f32_16x16x32_bf16 v[100:103], v[178:181], v[202:205], v[100:103]
	v_mfma_f32_16x16x32_bf16 v[96:99], v[186:189], v[202:205], v[96:99]
	v_mfma_f32_16x16x32_bf16 v[84:87], v[178:181], v[210:213], v[84:87]
	v_mfma_f32_16x16x32_bf16 v[80:83], v[186:189], v[210:213], v[80:83]
	v_mfma_f32_16x16x32_bf16 v[68:71], v[178:181], v[218:221], v[68:71]
	v_mfma_f32_16x16x32_bf16 v[64:67], v[186:189], v[218:221], v[64:67]
	s_setprio 0
	s_barrier
	s_add_u32 s98, s38, s12
	s_addc_u32 s99, s39, s13
	s_add_u32 s100, s40, s12
	s_addc_u32 s101, s41, s13
	s_add_i32 s69, s57, s46
	s_mov_b32 m0, s69
	ds_read_b128 v[190:193], v177 offset:16384
	ds_read_b128 v[194:197], v177 offset:17408
	ds_read_b128 v[198:201], v177 offset:18432
	ds_read_b128 v[202:205], v177 offset:19456
	ds_read_b128 v[206:209], v177 offset:20480
	ds_read_b128 v[210:213], v177 offset:21504
	ds_read_b128 v[214:217], v177 offset:22528
	ds_read_b128 v[218:221], v177 offset:23552
	global_load_lds_dwordx4 v148, s[38:39]
	s_add_i32 m0, s69, 0x2000
	s_add_u32 s70, s38, 0x40000
	s_addc_u32 s71, s39, 0
	s_add_i32 s69, s58, s46
	global_load_lds_dwordx4 v144, s[38:39]
	s_mov_b32 m0, s69
	s_nop 0
	global_load_lds_dwordx4 v148, s[70:71]
	s_add_i32 m0, s69, 0x2000
	s_nop 0
	global_load_lds_dwordx4 v144, s[70:71]
	s_mov_b32 m0, s35
	s_nop 0
	global_load_lds_dwordx4 v150, s[40:41]
	s_mov_b32 m0, s47
	s_nop 0
	global_load_lds_dwordx4 v146, s[40:41]
	s_waitcnt vmcnt(8)
	s_waitcnt lgkmcnt(0)
	s_barrier
	s_setprio 1
	s_waitcnt lgkmcnt(0)
	v_mfma_f32_16x16x32_bf16 v[60:63], v[128:131], v[190:193], v[60:63]
	v_mfma_f32_16x16x32_bf16 v[56:59], v[136:139], v[190:193], v[56:59]
	v_mfma_f32_16x16x32_bf16 v[44:47], v[128:131], v[198:201], v[44:47]
	v_mfma_f32_16x16x32_bf16 v[40:43], v[136:139], v[198:201], v[40:43]
	v_mfma_f32_16x16x32_bf16 v[28:31], v[128:131], v[206:209], v[28:31]
	v_mfma_f32_16x16x32_bf16 v[24:27], v[136:139], v[206:209], v[24:27]
	v_mfma_f32_16x16x32_bf16 v[12:15], v[128:131], v[214:217], v[12:15]
	v_mfma_f32_16x16x32_bf16 v[8:11], v[136:139], v[214:217], v[8:11]
	v_mfma_f32_16x16x32_bf16 v[60:63], v[132:135], v[194:197], v[60:63]
	v_mfma_f32_16x16x32_bf16 v[56:59], v[140:143], v[194:197], v[56:59]
	v_mfma_f32_16x16x32_bf16 v[44:47], v[132:135], v[202:205], v[44:47]
	v_mfma_f32_16x16x32_bf16 v[40:43], v[140:143], v[202:205], v[40:43]
	v_mfma_f32_16x16x32_bf16 v[28:31], v[132:135], v[210:213], v[28:31]
	v_mfma_f32_16x16x32_bf16 v[24:27], v[140:143], v[210:213], v[24:27]
	v_mfma_f32_16x16x32_bf16 v[12:15], v[132:135], v[218:221], v[12:15]
	v_mfma_f32_16x16x32_bf16 v[8:11], v[140:143], v[218:221], v[8:11]
	s_setprio 0
	s_setprio 1
	v_mfma_f32_16x16x32_bf16 v[52:55], v[164:167], v[190:193], v[52:55]
	v_mfma_f32_16x16x32_bf16 v[48:51], v[182:185], v[190:193], v[48:51]
	v_mfma_f32_16x16x32_bf16 v[36:39], v[164:167], v[198:201], v[36:39]
	v_mfma_f32_16x16x32_bf16 v[32:35], v[182:185], v[198:201], v[32:35]
	v_mfma_f32_16x16x32_bf16 v[20:23], v[164:167], v[206:209], v[20:23]
	v_mfma_f32_16x16x32_bf16 v[16:19], v[182:185], v[206:209], v[16:19]
	v_mfma_f32_16x16x32_bf16 v[4:7], v[164:167], v[214:217], v[4:7]
	v_mfma_f32_16x16x32_bf16 v[0:3], v[182:185], v[214:217], v[0:3]
	v_mfma_f32_16x16x32_bf16 v[52:55], v[178:181], v[194:197], v[52:55]
	v_mfma_f32_16x16x32_bf16 v[48:51], v[186:189], v[194:197], v[48:51]
	v_mfma_f32_16x16x32_bf16 v[36:39], v[178:181], v[202:205], v[36:39]
	v_mfma_f32_16x16x32_bf16 v[32:35], v[186:189], v[202:205], v[32:35]
	v_mfma_f32_16x16x32_bf16 v[20:23], v[178:181], v[210:213], v[20:23]
	v_mfma_f32_16x16x32_bf16 v[16:19], v[186:189], v[210:213], v[16:19]
	v_mfma_f32_16x16x32_bf16 v[4:7], v[178:181], v[218:221], v[4:7]
	v_mfma_f32_16x16x32_bf16 v[0:3], v[186:189], v[218:221], v[0:3]
	s_setprio 0
	s_barrier
; #define PG8_STAGE(bufoff, gbase, voff) do { _Pragma("unroll") for (int _i = 0; _i < 2; ++_i) \
;         __builtin_amdgcn_global_load_lds((const unsigned*)((const char*)(gbase) + (voff)[_i]), (PG8_LAS unsigned*)(lds + (bufoff) + ldsw + _i * 8192), 16, 0, 0); } while (0)
; #define PG8_STAGE_A(b, h, gbase, NX) do { if constexpr (AM::GATHER) { const unsigned so_[2] = {(NX) ? gno[h][0] : gao[h][0], (NX) ? gno[h][1] : gao[h][1]}; PG8_STAGE(PG8_SA(b, h), gbase, so_); } \
;         else { PG8_STAGE(PG8_SA(b, h), (gbase) + (h) * hstep, voffA); } } while (0)
; #define PG8_LDA(dst, b, h) do { _Pragma("unroll") for (int m = 0; m < 4; ++m) _Pragma("unroll") for (int k = 0; k < 2; ++k) dst[m][k] = *(const PG8_LAS bf16x8*)(lds + PG8_SA(b, h) + aoff + m * 2048 + k * 1024); } while (0)
; #define PG8_LDB(dst, b, h) do { _Pragma("unroll") for (int n = 0; n < 2; ++n) _Pragma("unroll") for (int k = 0; k < 2; ++k) dst[n][k] = *(const PG8_LAS bf16x8*)(lds + PG8_SB(b, h) + boff + n * 2048 + k * 1024); } while (0)
; #define PG8_MMA(ai, bj, At, Bt) do { __builtin_amdgcn_s_setprio(1); _Pragma("unroll") for (int m = 0; m < 4; ++m) _Pragma("unroll") for (int n = 0; n < 2; ++n) _Pragma("unroll") for (int k = 0; k < 2; ++k) \
;         acc[ai][bj][m][n] = __builtin_amdgcn_mfma_f32_16x16x32_bf16(Bt[n][k], At[m][k], acc[ai][bj][m][n], 0, 0, 0); __builtin_amdgcn_s_setprio(0); } while (0)
; #define PG8_WAIT_V(n) asm volatile("s_waitcnt vmcnt(" #n ")" ::: "memory")
; #define PG8_WAIT_L(n) asm volatile("s_waitcnt lgkmcnt(" #n ")" ::: "memory")
; #define PG8_BAR __builtin_amdgcn_s_barrier()
; #define PG8_SCHED __builtin_amdgcn_sched_barrier(0)
; template <class Epi, class Sched, class AM, bool ALIGN_EPI = false, bool SP2 = false>
; __device__ __forceinline__ void gemm_phase(PG8_LAS unsigned char* lds, const Gemm g, const Sched& S, const Epi& E, const AM& am, const int wid_in) {
;     ...
;             PG8_LDB(B0, 1, 0); PG8_LDB(B1, 1, 1); PG8_SCHED; PG8_LDA(At, 1, 0); PG8_STAGE_A(0, 1, a2, last);
;             PG8_WAIT_V(8); PG8_WAIT_L(0); PG8_BAR; PG8_MMA(0, 0, At, B0); PG8_MMA(0, 1, At, B1); PG8_BAR; PG8_SCHED;
;             PG8_LDA(At, 1, 1); PG8_STAGE(PG8_SB(1, 0), b3, voffB); PG8_STAGE(PG8_SB(1, 1), b3 + hstep, voffB); PG8_STAGE_A(1, 0, a3, last);
;             PG8_WAIT_V(8); PG8_WAIT_L(0); PG8_BAR; PG8_MMA(1, 0, At, B0); PG8_MMA(1, 1, At, B1); PG8_BAR; PG8_SCHED;
	s_add_i32 s69, 0, 0x18000
	s_add_i32 s70, 0, 0x1c000
	v_add_u32_e32 v140, s69, v171
	v_add_u32_e32 v186, s70, v171
	ds_read_b128 v[128:131], v140
	ds_read_b128 v[132:135], v140 offset:1024
	ds_read_b128 v[136:139], v140 offset:2048
	ds_read_b128 v[140:143], v140 offset:3072
	ds_read_b128 v[164:167], v186
	ds_read_b128 v[178:181], v186 offset:1024
	ds_read_b128 v[182:185], v186 offset:2048
	ds_read_b128 v[186:189], v186 offset:3072
	s_add_u32 s40, s40, 0x40000
	s_addc_u32 s41, s41, 0
	s_mov_b32 m0, s48
	ds_read_b128 v[190:193], v177 offset:32768
	ds_read_b128 v[194:197], v177 offset:33792
	ds_read_b128 v[198:201], v177 offset:34816
	ds_read_b128 v[202:205], v177 offset:35840
	ds_read_b128 v[206:209], v177 offset:36864
	ds_read_b128 v[210:213], v177 offset:37888
	ds_read_b128 v[214:217], v177 offset:38912
	ds_read_b128 v[218:221], v177 offset:39936
	global_load_lds_dwordx4 v150, s[40:41]
	s_mov_b32 m0, s49
	s_nop 0
	global_load_lds_dwordx4 v146, s[40:41]
	s_waitcnt vmcnt(8)
	s_waitcnt lgkmcnt(0)
	s_barrier
	s_setprio 1
	s_waitcnt lgkmcnt(0)
	v_mfma_f32_16x16x32_bf16 v[124:127], v[128:131], v[190:193], v[124:127]
	v_mfma_f32_16x16x32_bf16 v[120:123], v[136:139], v[190:193], v[120:123]
	v_mfma_f32_16x16x32_bf16 v[116:119], v[128:131], v[198:201], v[116:119]
	v_mfma_f32_16x16x32_bf16 v[112:115], v[136:139], v[198:201], v[112:115]
	v_mfma_f32_16x16x32_bf16 v[92:95], v[128:131], v[206:209], v[92:95]
	v_mfma_f32_16x16x32_bf16 v[88:91], v[136:139], v[206:209], v[88:91]
	v_mfma_f32_16x16x32_bf16 v[76:79], v[128:131], v[214:217], v[76:79]
	v_mfma_f32_16x16x32_bf16 v[72:75], v[136:139], v[214:217], v[72:75]
	v_mfma_f32_16x16x32_bf16 v[124:127], v[132:135], v[194:197], v[124:127]
	v_mfma_f32_16x16x32_bf16 v[120:123], v[140:143], v[194:197], v[120:123]
	v_mfma_f32_16x16x32_bf16 v[116:119], v[132:135], v[202:205], v[116:119]
	v_mfma_f32_16x16x32_bf16 v[112:115], v[140:143], v[202:205], v[112:115]
	v_mfma_f32_16x16x32_bf16 v[92:95], v[132:135], v[210:213], v[92:95]
	v_mfma_f32_16x16x32_bf16 v[88:91], v[140:143], v[210:213], v[88:91]
	v_mfma_f32_16x16x32_bf16 v[76:79], v[132:135], v[218:221], v[76:79]
	v_mfma_f32_16x16x32_bf16 v[72:75], v[140:143], v[218:221], v[72:75]
	s_setprio 0
	s_setprio 1
	v_mfma_f32_16x16x32_bf16 v[108:111], v[164:167], v[190:193], v[108:111]
	v_mfma_f32_16x16x32_bf16 v[104:107], v[182:185], v[190:193], v[104:107]
	v_mfma_f32_16x16x32_bf16 v[100:103], v[164:167], v[198:201], v[100:103]
	v_mfma_f32_16x16x32_bf16 v[96:99], v[182:185], v[198:201], v[96:99]
	v_mfma_f32_16x16x32_bf16 v[84:87], v[164:167], v[206:209], v[84:87]
	v_mfma_f32_16x16x32_bf16 v[80:83], v[182:185], v[206:209], v[80:83]
	v_mfma_f32_16x16x32_bf16 v[68:71], v[164:167], v[214:217], v[68:71]
	v_mfma_f32_16x16x32_bf16 v[64:67], v[182:185], v[214:217], v[64:67]
	v_mfma_f32_16x16x32_bf16 v[108:111], v[178:181], v[194:197], v[108:111]
	v_mfma_f32_16x16x32_bf16 v[104:107], v[186:189], v[194:197], v[104:107]
	v_mfma_f32_16x16x32_bf16 v[100:103], v[178:181], v[202:205], v[100:103]
	v_mfma_f32_16x16x32_bf16 v[96:99], v[186:189], v[202:205], v[96:99]
	v_mfma_f32_16x16x32_bf16 v[84:87], v[178:181], v[210:213], v[84:87]
	v_mfma_f32_16x16x32_bf16 v[80:83], v[186:189], v[210:213], v[80:83]
	v_mfma_f32_16x16x32_bf16 v[68:71], v[178:181], v[218:221], v[68:71]
	v_mfma_f32_16x16x32_bf16 v[64:67], v[186:189], v[218:221], v[64:67]
	s_setprio 0
	s_barrier
	s_add_i32 s40, s69, s46
	s_mov_b32 m0, s40
	ds_read_b128 v[190:193], v177 offset:49152
	ds_read_b128 v[194:197], v177 offset:50176
	ds_read_b128 v[198:201], v177 offset:51200
	ds_read_b128 v[202:205], v177 offset:52224
	ds_read_b128 v[206:209], v177 offset:53248
	ds_read_b128 v[210:213], v177 offset:54272
	ds_read_b128 v[214:217], v177 offset:55296
	ds_read_b128 v[218:221], v177 offset:56320
	global_load_lds_dwordx4 v148, s[98:99]
	s_add_i32 m0, s40, 0x2000
	s_add_u32 s38, s38, 0x40080
	s_addc_u32 s39, s39, 0
	s_add_i32 s40, s70, s46
	global_load_lds_dwordx4 v144, s[98:99]
	s_mov_b32 m0, s40
	s_nop 0
	global_load_lds_dwordx4 v148, s[38:39]
	s_add_i32 m0, s40, 0x2000
	s_nop 0
	global_load_lds_dwordx4 v144, s[38:39]
	s_mov_b32 m0, s55
	s_nop 0
	global_load_lds_dwordx4 v150, s[100:101]
	s_mov_b32 m0, s56
	s_nop 0
	global_load_lds_dwordx4 v146, s[100:101]
	s_waitcnt vmcnt(8)
	s_waitcnt lgkmcnt(0)
	s_barrier
	s_setprio 1
	s_waitcnt lgkmcnt(0)
	v_mfma_f32_16x16x32_bf16 v[60:63], v[128:131], v[190:193], v[60:63]
	v_mfma_f32_16x16x32_bf16 v[56:59], v[136:139], v[190:193], v[56:59]
	v_mfma_f32_16x16x32_bf16 v[44:47], v[128:131], v[198:201], v[44:47]
	v_mfma_f32_16x16x32_bf16 v[40:43], v[136:139], v[198:201], v[40:43]
	v_mfma_f32_16x16x32_bf16 v[28:31], v[128:131], v[206:209], v[28:31]
	v_mfma_f32_16x16x32_bf16 v[24:27], v[136:139], v[206:209], v[24:27]
	v_mfma_f32_16x16x32_bf16 v[12:15], v[128:131], v[214:217], v[12:15]
	v_mfma_f32_16x16x32_bf16 v[8:11], v[136:139], v[214:217], v[8:11]
	v_mfma_f32_16x16x32_bf16 v[60:63], v[132:135], v[194:197], v[60:63]
	v_mfma_f32_16x16x32_bf16 v[56:59], v[140:143], v[194:197], v[56:59]
	v_mfma_f32_16x16x32_bf16 v[44:47], v[132:135], v[202:205], v[44:47]
	v_mfma_f32_16x16x32_bf16 v[40:43], v[140:143], v[202:205], v[40:43]
	v_mfma_f32_16x16x32_bf16 v[28:31], v[132:135], v[210:213], v[28:31]
	v_mfma_f32_16x16x32_bf16 v[24:27], v[140:143], v[210:213], v[24:27]
	v_mfma_f32_16x16x32_bf16 v[12:15], v[132:135], v[218:221], v[12:15]
	v_mfma_f32_16x16x32_bf16 v[8:11], v[140:143], v[218:221], v[8:11]
	s_setprio 0
	s_setprio 1
	v_mfma_f32_16x16x32_bf16 v[52:55], v[164:167], v[190:193], v[52:55]
	v_mfma_f32_16x16x32_bf16 v[48:51], v[182:185], v[190:193], v[48:51]
	v_mfma_f32_16x16x32_bf16 v[36:39], v[164:167], v[198:201], v[36:39]
	v_mfma_f32_16x16x32_bf16 v[32:35], v[182:185], v[198:201], v[32:35]
	v_mfma_f32_16x16x32_bf16 v[20:23], v[164:167], v[206:209], v[20:23]
	v_mfma_f32_16x16x32_bf16 v[16:19], v[182:185], v[206:209], v[16:19]
	v_mfma_f32_16x16x32_bf16 v[4:7], v[164:167], v[214:217], v[4:7]
	v_mfma_f32_16x16x32_bf16 v[0:3], v[182:185], v[214:217], v[0:3]
	v_mfma_f32_16x16x32_bf16 v[52:55], v[178:181], v[194:197], v[52:55]
	v_mfma_f32_16x16x32_bf16 v[48:51], v[186:189], v[194:197], v[48:51]
	v_mfma_f32_16x16x32_bf16 v[36:39], v[178:181], v[202:205], v[36:39]
	v_mfma_f32_16x16x32_bf16 v[32:35], v[186:189], v[202:205], v[32:35]
	v_mfma_f32_16x16x32_bf16 v[20:23], v[178:181], v[210:213], v[20:23]
	v_mfma_f32_16x16x32_bf16 v[16:19], v[186:189], v[210:213], v[16:19]
	v_mfma_f32_16x16x32_bf16 v[4:7], v[178:181], v[218:221], v[4:7]
	v_mfma_f32_16x16x32_bf16 v[0:3], v[186:189], v[218:221], v[0:3]
	s_setprio 0
	s_barrier
	s_add_i32 s68, s68, 2
	s_add_u32 s36, s36, 0x100
	s_addc_u32 s37, s37, 0
	s_add_u32 s66, s66, 0x100
	s_addc_u32 s67, s67, 0
	s_cmp_gt_u32 s68, 13
	s_cbranch_scc0 .LBB0_1055
	s_and_b64 vcc, exec, s[14:15]
	s_cbranch_vccz .LBB0_1058
	s_barrier

; #define PG8_STAGE(bufoff, gbase, voff) do { _Pragma("unroll") for (int _i = 0; _i < 2; ++_i) \
;         __builtin_amdgcn_global_load_lds((const unsigned*)((const char*)(gbase) + (voff)[_i]), (PG8_LAS unsigned*)(lds + (bufoff) + ldsw + _i * 8192), 16, 0, 0); } while (0)
; #define PG8_STAGE_A(b, h, gbase, NX) do { if constexpr (AM::GATHER) { const unsigned so_[2] = {(NX) ? gno[h][0] : gao[h][0], (NX) ? gno[h][1] : gao[h][1]}; PG8_STAGE(PG8_SA(b, h), gbase, so_); } \
;         else { PG8_STAGE(PG8_SA(b, h), (gbase) + (h) * hstep, voffA); } } while (0)
; #define PG8_LDA(dst, b, h) do { _Pragma("unroll") for (int m = 0; m < 4; ++m) _Pragma("unroll") for (int k = 0; k < 2; ++k) dst[m][k] = *(const PG8_LAS bf16x8*)(lds + PG8_SA(b, h) + aoff + m * 2048 + k * 1024); } while (0)
; #define PG8_LDB(dst, b, h) do { _Pragma("unroll") for (int n = 0; n < 2; ++n) _Pragma("unroll") for (int k = 0; k < 2; ++k) dst[n][k] = *(const PG8_LAS bf16x8*)(lds + PG8_SB(b, h) + boff + n * 2048 + k * 1024); } while (0)
; #define PG8_MMA(ai, bj, At, Bt) do { __builtin_amdgcn_s_setprio(1); _Pragma("unroll") for (int m = 0; m < 4; ++m) _Pragma("unroll") for (int n = 0; n < 2; ++n) _Pragma("unroll") for (int k = 0; k < 2; ++k) \
;         acc[ai][bj][m][n] = __builtin_amdgcn_mfma_f32_16x16x32_bf16(Bt[n][k], At[m][k], acc[ai][bj][m][n], 0, 0, 0); __builtin_amdgcn_s_setprio(0); } while (0)
; #define PG8_WAIT_V(n) asm volatile("s_waitcnt vmcnt(" #n ")" ::: "memory")
; #define PG8_WAIT_L(n) asm volatile("s_waitcnt lgkmcnt(" #n ")" ::: "memory")
; #define PG8_BAR __builtin_amdgcn_s_barrier()
; template <class Epi, class Sched, class AM, bool ALIGN_EPI = false, bool SP2 = false>
; __device__ __forceinline__ void gemm_phase(PG8_LAS unsigned char* lds, const Gemm g, const Sched& S, const Epi& E, const AM& am, const int wid_in) {
;     ...
;             if constexpr (SP2) {
;             PG8_LDB(B0, 0, 0); PG8_LDB(B1, 0, 1); PG8_SCHED; PG8_LDA(At, 0, 0); PG8_STAGE_A(1, 1, a1, false);
;             PG8_WAIT_V(8); PG8_WAIT_L(0); PG8_BAR; PG8_MMA(0, 0, At, B0); PG8_MMA(0, 1, At, B1); PG8_BAR; PG8_SCHED;
;             PG8_LDA(At, 0, 1); PG8_STAGE(PG8_SB(0, 0), b2, voffB); PG8_STAGE(PG8_SB(0, 1), b2 + hstep, voffB); PG8_STAGE_A(0, 0, a2, last);
;             PG8_WAIT_V(8); PG8_WAIT_L(0); PG8_BAR; PG8_MMA(1, 0, At, B0); PG8_MMA(1, 1, At, B1); PG8_BAR; PG8_SCHED;
.LBB0_1650:
	ds_read_b128 v[144:147], v159
	ds_read_b128 v[162:165], v159 offset:1024
	ds_read_b128 v[166:169], v159 offset:2048
	ds_read_b128 v[170:173], v159 offset:3072
	ds_read_b128 v[174:177], v160
	ds_read_b128 v[178:181], v160 offset:1024
	ds_read_b128 v[182:185], v160 offset:2048
	ds_read_b128 v[186:189], v160 offset:3072
	s_add_u32 s28, s26, 0xfffe0080
	s_addc_u32 s29, s27, -1
	s_cmp_eq_u32 s63, 4
	s_cselect_b32 s31, s13, s29
	s_cselect_b32 s30, s59, s28
	s_cselect_b32 s29, s15, s62
	s_cselect_b32 s28, s60, s61
	s_add_i32 m0, s23, 0xc000
	ds_read_b128 v[190:193], v161
	ds_read_b128 v[194:197], v161 offset:1024
	ds_read_b128 v[198:201], v161 offset:2048
	ds_read_b128 v[202:205], v161 offset:3072
	ds_read_b128 v[206:209], v161 offset:4096
	ds_read_b128 v[210:213], v161 offset:5120
	ds_read_b128 v[214:217], v161 offset:6144
	ds_read_b128 v[218:221], v161 offset:7168
	global_load_lds_dwordx4 v138, s[26:27]
	s_add_i32 m0, s23, 0xe000
	s_nop 0
	global_load_lds_dwordx4 v140, s[26:27]
	s_waitcnt vmcnt(8)
	s_waitcnt lgkmcnt(0)
	s_barrier
	s_setprio 1
	s_waitcnt lgkmcnt(0)
	v_mfma_f32_16x16x32_bf16 v[124:127], v[144:147], v[190:193], v[124:127]
	v_mfma_f32_16x16x32_bf16 v[120:123], v[166:169], v[190:193], v[120:123]
	v_mfma_f32_16x16x32_bf16 v[116:119], v[144:147], v[198:201], v[116:119]
	v_mfma_f32_16x16x32_bf16 v[112:115], v[166:169], v[198:201], v[112:115]
	v_mfma_f32_16x16x32_bf16 v[100:103], v[144:147], v[206:209], v[100:103]
	v_mfma_f32_16x16x32_bf16 v[96:99], v[166:169], v[206:209], v[96:99]
	v_mfma_f32_16x16x32_bf16 v[84:87], v[144:147], v[214:217], v[84:87]
	v_mfma_f32_16x16x32_bf16 v[76:79], v[166:169], v[214:217], v[76:79]
	v_mfma_f32_16x16x32_bf16 v[124:127], v[162:165], v[194:197], v[124:127]
	v_mfma_f32_16x16x32_bf16 v[120:123], v[170:173], v[194:197], v[120:123]
	v_mfma_f32_16x16x32_bf16 v[116:119], v[162:165], v[202:205], v[116:119]
	v_mfma_f32_16x16x32_bf16 v[112:115], v[170:173], v[202:205], v[112:115]
	v_mfma_f32_16x16x32_bf16 v[100:103], v[162:165], v[210:213], v[100:103]
	v_mfma_f32_16x16x32_bf16 v[96:99], v[170:173], v[210:213], v[96:99]
	v_mfma_f32_16x16x32_bf16 v[84:87], v[162:165], v[218:221], v[84:87]
	v_mfma_f32_16x16x32_bf16 v[76:79], v[170:173], v[218:221], v[76:79]
	s_setprio 0
	s_setprio 1
	v_mfma_f32_16x16x32_bf16 v[108:111], v[174:177], v[190:193], v[108:111]
	v_mfma_f32_16x16x32_bf16 v[104:107], v[182:185], v[190:193], v[104:107]
	v_mfma_f32_16x16x32_bf16 v[92:95], v[174:177], v[198:201], v[92:95]
	v_mfma_f32_16x16x32_bf16 v[88:91], v[182:185], v[198:201], v[88:91]
	v_mfma_f32_16x16x32_bf16 v[80:83], v[174:177], v[206:209], v[80:83]
	v_mfma_f32_16x16x32_bf16 v[72:75], v[182:185], v[206:209], v[72:75]
	v_mfma_f32_16x16x32_bf16 v[68:71], v[174:177], v[214:217], v[68:71]
	v_mfma_f32_16x16x32_bf16 v[64:67], v[182:185], v[214:217], v[64:67]
	v_mfma_f32_16x16x32_bf16 v[108:111], v[178:181], v[194:197], v[108:111]
	v_mfma_f32_16x16x32_bf16 v[104:107], v[186:189], v[194:197], v[104:107]
	v_mfma_f32_16x16x32_bf16 v[92:95], v[178:181], v[202:205], v[92:95]
	v_mfma_f32_16x16x32_bf16 v[88:91], v[186:189], v[202:205], v[88:91]
	v_mfma_f32_16x16x32_bf16 v[80:83], v[178:181], v[210:213], v[80:83]
	v_mfma_f32_16x16x32_bf16 v[72:75], v[186:189], v[210:213], v[72:75]
	v_mfma_f32_16x16x32_bf16 v[68:71], v[178:181], v[218:221], v[68:71]
	v_mfma_f32_16x16x32_bf16 v[64:67], v[186:189], v[218:221], v[64:67]
	s_setprio 0
	s_barrier
	s_add_u32 s98, s28, s8
	s_addc_u32 s99, s29, s9
	s_add_u32 s100, s30, s8
	s_addc_u32 s101, s31, s9
	s_add_i32 s64, s55, s39
	s_mov_b32 m0, s64
	ds_read_b128 v[190:193], v161 offset:16384
	ds_read_b128 v[194:197], v161 offset:17408
	ds_read_b128 v[198:201], v161 offset:18432
	ds_read_b128 v[202:205], v161 offset:19456
	ds_read_b128 v[206:209], v161 offset:20480
	ds_read_b128 v[210:213], v161 offset:21504
	ds_read_b128 v[214:217], v161 offset:22528
	ds_read_b128 v[218:221], v161 offset:23552
	global_load_lds_dwordx4 v130, s[28:29]
	s_add_i32 m0, s64, 0x2000
	s_add_u32 s64, s28, 0x20000
	s_addc_u32 s65, s29, 0
	s_add_i32 s66, s56, s39
	global_load_lds_dwordx4 v134, s[28:29]
	s_mov_b32 m0, s66
	s_nop 0
	global_load_lds_dwordx4 v130, s[64:65]
	s_add_i32 m0, s66, 0x2000
	s_nop 0
	global_load_lds_dwordx4 v134, s[64:65]
	s_mov_b32 m0, s23
	s_nop 0
	global_load_lds_dwordx4 v128, s[30:31]
	s_mov_b32 m0, s25
	s_nop 0
	global_load_lds_dwordx4 v132, s[30:31]
	s_waitcnt vmcnt(8)
	s_waitcnt lgkmcnt(0)
	s_barrier
	s_setprio 1
	s_waitcnt lgkmcnt(0)
	v_mfma_f32_16x16x32_bf16 v[60:63], v[144:147], v[190:193], v[60:63]
	v_mfma_f32_16x16x32_bf16 v[56:59], v[166:169], v[190:193], v[56:59]
	v_mfma_f32_16x16x32_bf16 v[44:47], v[144:147], v[198:201], v[44:47]
	v_mfma_f32_16x16x32_bf16 v[40:43], v[166:169], v[198:201], v[40:43]
	v_mfma_f32_16x16x32_bf16 v[28:31], v[144:147], v[206:209], v[28:31]
	v_mfma_f32_16x16x32_bf16 v[24:27], v[166:169], v[206:209], v[24:27]
	v_mfma_f32_16x16x32_bf16 v[12:15], v[144:147], v[214:217], v[12:15]
	v_mfma_f32_16x16x32_bf16 v[8:11], v[166:169], v[214:217], v[8:11]
	v_mfma_f32_16x16x32_bf16 v[60:63], v[162:165], v[194:197], v[60:63]
	v_mfma_f32_16x16x32_bf16 v[56:59], v[170:173], v[194:197], v[56:59]
	v_mfma_f32_16x16x32_bf16 v[44:47], v[162:165], v[202:205], v[44:47]
	v_mfma_f32_16x16x32_bf16 v[40:43], v[170:173], v[202:205], v[40:43]
	v_mfma_f32_16x16x32_bf16 v[28:31], v[162:165], v[210:213], v[28:31]
	v_mfma_f32_16x16x32_bf16 v[24:27], v[170:173], v[210:213], v[24:27]
	v_mfma_f32_16x16x32_bf16 v[12:15], v[162:165], v[218:221], v[12:15]
	v_mfma_f32_16x16x32_bf16 v[8:11], v[170:173], v[218:221], v[8:11]
	s_setprio 0
	s_setprio 1
	v_mfma_f32_16x16x32_bf16 v[52:55], v[174:177], v[190:193], v[52:55]
	v_mfma_f32_16x16x32_bf16 v[48:51], v[182:185], v[190:193], v[48:51]
	v_mfma_f32_16x16x32_bf16 v[36:39], v[174:177], v[198:201], v[36:39]
	v_mfma_f32_16x16x32_bf16 v[32:35], v[182:185], v[198:201], v[32:35]
	v_mfma_f32_16x16x32_bf16 v[20:23], v[174:177], v[206:209], v[20:23]
	v_mfma_f32_16x16x32_bf16 v[16:19], v[182:185], v[206:209], v[16:19]
	v_mfma_f32_16x16x32_bf16 v[4:7], v[174:177], v[214:217], v[4:7]
	v_mfma_f32_16x16x32_bf16 v[0:3], v[182:185], v[214:217], v[0:3]
	v_mfma_f32_16x16x32_bf16 v[52:55], v[178:181], v[194:197], v[52:55]
	v_mfma_f32_16x16x32_bf16 v[48:51], v[186:189], v[194:197], v[48:51]
	v_mfma_f32_16x16x32_bf16 v[36:39], v[178:181], v[202:205], v[36:39]
	v_mfma_f32_16x16x32_bf16 v[32:35], v[186:189], v[202:205], v[32:35]
	v_mfma_f32_16x16x32_bf16 v[20:23], v[178:181], v[210:213], v[20:23]
	v_mfma_f32_16x16x32_bf16 v[16:19], v[186:189], v[210:213], v[16:19]
	v_mfma_f32_16x16x32_bf16 v[4:7], v[178:181], v[218:221], v[4:7]
	v_mfma_f32_16x16x32_bf16 v[0:3], v[186:189], v[218:221], v[0:3]
	s_setprio 0
	s_barrier
; #define PG8_STAGE(bufoff, gbase, voff) do { _Pragma("unroll") for (int _i = 0; _i < 2; ++_i) \
;         __builtin_amdgcn_global_load_lds((const unsigned*)((const char*)(gbase) + (voff)[_i]), (PG8_LAS unsigned*)(lds + (bufoff) + ldsw + _i * 8192), 16, 0, 0); } while (0)
; #define PG8_STAGE_A(b, h, gbase, NX) do { if constexpr (AM::GATHER) { const unsigned so_[2] = {(NX) ? gno[h][0] : gao[h][0], (NX) ? gno[h][1] : gao[h][1]}; PG8_STAGE(PG8_SA(b, h), gbase, so_); } \
;         else { PG8_STAGE(PG8_SA(b, h), (gbase) + (h) * hstep, voffA); } } while (0)
; #define PG8_LDA(dst, b, h) do { _Pragma("unroll") for (int m = 0; m < 4; ++m) _Pragma("unroll") for (int k = 0; k < 2; ++k) dst[m][k] = *(const PG8_LAS bf16x8*)(lds + PG8_SA(b, h) + aoff + m * 2048 + k * 1024); } while (0)
; #define PG8_LDB(dst, b, h) do { _Pragma("unroll") for (int n = 0; n < 2; ++n) _Pragma("unroll") for (int k = 0; k < 2; ++k) dst[n][k] = *(const PG8_LAS bf16x8*)(lds + PG8_SB(b, h) + boff + n * 2048 + k * 1024); } while (0)
; #define PG8_MMA(ai, bj, At, Bt) do { __builtin_amdgcn_s_setprio(1); _Pragma("unroll") for (int m = 0; m < 4; ++m) _Pragma("unroll") for (int n = 0; n < 2; ++n) _Pragma("unroll") for (int k = 0; k < 2; ++k) \
;         acc[ai][bj][m][n] = __builtin_amdgcn_mfma_f32_16x16x32_bf16(Bt[n][k], At[m][k], acc[ai][bj][m][n], 0, 0, 0); __builtin_amdgcn_s_setprio(0); } while (0)
; #define PG8_WAIT_V(n) asm volatile("s_waitcnt vmcnt(" #n ")" ::: "memory")
; #define PG8_WAIT_L(n) asm volatile("s_waitcnt lgkmcnt(" #n ")" ::: "memory")
; #define PG8_BAR __builtin_amdgcn_s_barrier()
; #define PG8_SCHED __builtin_amdgcn_sched_barrier(0)
; template <class Epi, class Sched, class AM, bool ALIGN_EPI = false, bool SP2 = false>
; __device__ __forceinline__ void gemm_phase(PG8_LAS unsigned char* lds, const Gemm g, const Sched& S, const Epi& E, const AM& am, const int wid_in) {
;     ...
;             PG8_LDB(B0, 1, 0); PG8_LDB(B1, 1, 1); PG8_SCHED; PG8_LDA(At, 1, 0); PG8_STAGE_A(0, 1, a2, last);
;             PG8_WAIT_V(8); PG8_WAIT_L(0); PG8_BAR; PG8_MMA(0, 0, At, B0); PG8_MMA(0, 1, At, B1); PG8_BAR; PG8_SCHED;
;             PG8_LDA(At, 1, 1); PG8_STAGE(PG8_SB(1, 0), b3, voffB); PG8_STAGE(PG8_SB(1, 1), b3 + hstep, voffB); PG8_STAGE_A(1, 0, a3, last);
;             PG8_WAIT_V(8); PG8_WAIT_L(0); PG8_BAR; PG8_MMA(1, 0, At, B0); PG8_MMA(1, 1, At, B1); PG8_BAR; PG8_SCHED;
	s_add_i32 s64, 0, 0x18000
	v_add_u32_e32 v148, s64, v151
	s_add_i32 s65, 0, 0x1c000
	ds_read_b128 v[144:147], v148
	ds_read_b128 v[162:165], v148 offset:1024
	ds_read_b128 v[166:169], v148 offset:2048
	ds_read_b128 v[170:173], v148 offset:3072
	v_add_u32_e32 v148, s65, v151
	ds_read_b128 v[174:177], v148
	ds_read_b128 v[178:181], v148 offset:1024
	ds_read_b128 v[182:185], v148 offset:2048
	ds_read_b128 v[186:189], v148 offset:3072
	s_add_u32 s30, s30, 0x20000
	s_addc_u32 s31, s31, 0
	s_mov_b32 m0, s42
	ds_read_b128 v[190:193], v161 offset:32768
	ds_read_b128 v[194:197], v161 offset:33792
	ds_read_b128 v[198:201], v161 offset:34816
	ds_read_b128 v[202:205], v161 offset:35840
	ds_read_b128 v[206:209], v161 offset:36864
	ds_read_b128 v[210:213], v161 offset:37888
	ds_read_b128 v[214:217], v161 offset:38912
	ds_read_b128 v[218:221], v161 offset:39936
	global_load_lds_dwordx4 v128, s[30:31]
	s_mov_b32 m0, s43
	s_nop 0
	global_load_lds_dwordx4 v132, s[30:31]
	s_waitcnt vmcnt(8)
	s_waitcnt lgkmcnt(0)
	s_barrier
	s_setprio 1
	s_waitcnt lgkmcnt(0)
	v_mfma_f32_16x16x32_bf16 v[124:127], v[144:147], v[190:193], v[124:127]
	v_mfma_f32_16x16x32_bf16 v[120:123], v[166:169], v[190:193], v[120:123]
	v_mfma_f32_16x16x32_bf16 v[116:119], v[144:147], v[198:201], v[116:119]
	v_mfma_f32_16x16x32_bf16 v[112:115], v[166:169], v[198:201], v[112:115]
	v_mfma_f32_16x16x32_bf16 v[100:103], v[144:147], v[206:209], v[100:103]
	v_mfma_f32_16x16x32_bf16 v[96:99], v[166:169], v[206:209], v[96:99]
	v_mfma_f32_16x16x32_bf16 v[84:87], v[144:147], v[214:217], v[84:87]
	v_mfma_f32_16x16x32_bf16 v[76:79], v[166:169], v[214:217], v[76:79]
	v_mfma_f32_16x16x32_bf16 v[124:127], v[162:165], v[194:197], v[124:127]
	v_mfma_f32_16x16x32_bf16 v[120:123], v[170:173], v[194:197], v[120:123]
	v_mfma_f32_16x16x32_bf16 v[116:119], v[162:165], v[202:205], v[116:119]
	v_mfma_f32_16x16x32_bf16 v[112:115], v[170:173], v[202:205], v[112:115]
	v_mfma_f32_16x16x32_bf16 v[100:103], v[162:165], v[210:213], v[100:103]
	v_mfma_f32_16x16x32_bf16 v[96:99], v[170:173], v[210:213], v[96:99]
	v_mfma_f32_16x16x32_bf16 v[84:87], v[162:165], v[218:221], v[84:87]
	v_mfma_f32_16x16x32_bf16 v[76:79], v[170:173], v[218:221], v[76:79]
	s_setprio 0
	s_setprio 1
	v_mfma_f32_16x16x32_bf16 v[108:111], v[174:177], v[190:193], v[108:111]
	v_mfma_f32_16x16x32_bf16 v[104:107], v[182:185], v[190:193], v[104:107]
	v_mfma_f32_16x16x32_bf16 v[92:95], v[174:177], v[198:201], v[92:95]
	v_mfma_f32_16x16x32_bf16 v[88:91], v[182:185], v[198:201], v[88:91]
	v_mfma_f32_16x16x32_bf16 v[80:83], v[174:177], v[206:209], v[80:83]
	v_mfma_f32_16x16x32_bf16 v[72:75], v[182:185], v[206:209], v[72:75]
	v_mfma_f32_16x16x32_bf16 v[68:71], v[174:177], v[214:217], v[68:71]
	v_mfma_f32_16x16x32_bf16 v[64:67], v[182:185], v[214:217], v[64:67]
	v_mfma_f32_16x16x32_bf16 v[108:111], v[178:181], v[194:197], v[108:111]
	v_mfma_f32_16x16x32_bf16 v[104:107], v[186:189], v[194:197], v[104:107]
	v_mfma_f32_16x16x32_bf16 v[92:95], v[178:181], v[202:205], v[92:95]
	v_mfma_f32_16x16x32_bf16 v[88:91], v[186:189], v[202:205], v[88:91]
	v_mfma_f32_16x16x32_bf16 v[80:83], v[178:181], v[210:213], v[80:83]
	v_mfma_f32_16x16x32_bf16 v[72:75], v[186:189], v[210:213], v[72:75]
	v_mfma_f32_16x16x32_bf16 v[68:71], v[178:181], v[218:221], v[68:71]
	v_mfma_f32_16x16x32_bf16 v[64:67], v[186:189], v[218:221], v[64:67]
	s_setprio 0
	s_barrier
	s_add_i32 s30, s64, s39
	s_mov_b32 m0, s30
	ds_read_b128 v[190:193], v161 offset:49152
	ds_read_b128 v[194:197], v161 offset:50176
	ds_read_b128 v[198:201], v161 offset:51200
	ds_read_b128 v[202:205], v161 offset:52224
	ds_read_b128 v[206:209], v161 offset:53248
	ds_read_b128 v[210:213], v161 offset:54272
	ds_read_b128 v[214:217], v161 offset:55296
	ds_read_b128 v[218:221], v161 offset:56320
	global_load_lds_dwordx4 v130, s[98:99]
	s_add_i32 m0, s30, 0x2000
	s_add_u32 s28, s28, 0x20080
	s_addc_u32 s29, s29, 0
	s_add_i32 s30, s65, s39
	global_load_lds_dwordx4 v134, s[98:99]
	s_mov_b32 m0, s30
	s_nop 0
	global_load_lds_dwordx4 v130, s[28:29]
	s_add_i32 m0, s30, 0x2000
	s_nop 0
	global_load_lds_dwordx4 v134, s[28:29]
	s_mov_b32 m0, s47
	s_nop 0
	global_load_lds_dwordx4 v128, s[100:101]
	s_mov_b32 m0, s48
	s_nop 0
	global_load_lds_dwordx4 v132, s[100:101]
	s_waitcnt vmcnt(8)
	s_waitcnt lgkmcnt(0)
	s_barrier
	s_setprio 1
	s_waitcnt lgkmcnt(0)
	v_mfma_f32_16x16x32_bf16 v[60:63], v[144:147], v[190:193], v[60:63]
	v_mfma_f32_16x16x32_bf16 v[56:59], v[166:169], v[190:193], v[56:59]
	v_mfma_f32_16x16x32_bf16 v[44:47], v[144:147], v[198:201], v[44:47]
	v_mfma_f32_16x16x32_bf16 v[40:43], v[166:169], v[198:201], v[40:43]
	v_mfma_f32_16x16x32_bf16 v[28:31], v[144:147], v[206:209], v[28:31]
	v_mfma_f32_16x16x32_bf16 v[24:27], v[166:169], v[206:209], v[24:27]
	v_mfma_f32_16x16x32_bf16 v[12:15], v[144:147], v[214:217], v[12:15]
	v_mfma_f32_16x16x32_bf16 v[8:11], v[166:169], v[214:217], v[8:11]
	v_mfma_f32_16x16x32_bf16 v[60:63], v[162:165], v[194:197], v[60:63]
	v_mfma_f32_16x16x32_bf16 v[56:59], v[170:173], v[194:197], v[56:59]
	v_mfma_f32_16x16x32_bf16 v[44:47], v[162:165], v[202:205], v[44:47]
	v_mfma_f32_16x16x32_bf16 v[40:43], v[170:173], v[202:205], v[40:43]
	v_mfma_f32_16x16x32_bf16 v[28:31], v[162:165], v[210:213], v[28:31]
	v_mfma_f32_16x16x32_bf16 v[24:27], v[170:173], v[210:213], v[24:27]
	v_mfma_f32_16x16x32_bf16 v[12:15], v[162:165], v[218:221], v[12:15]
	v_mfma_f32_16x16x32_bf16 v[8:11], v[170:173], v[218:221], v[8:11]
	s_setprio 0
	s_setprio 1
	v_mfma_f32_16x16x32_bf16 v[52:55], v[174:177], v[190:193], v[52:55]
	v_mfma_f32_16x16x32_bf16 v[48:51], v[182:185], v[190:193], v[48:51]
	v_mfma_f32_16x16x32_bf16 v[36:39], v[174:177], v[198:201], v[36:39]
	v_mfma_f32_16x16x32_bf16 v[32:35], v[182:185], v[198:201], v[32:35]
	v_mfma_f32_16x16x32_bf16 v[20:23], v[174:177], v[206:209], v[20:23]
	v_mfma_f32_16x16x32_bf16 v[16:19], v[182:185], v[206:209], v[16:19]
	v_mfma_f32_16x16x32_bf16 v[4:7], v[174:177], v[214:217], v[4:7]
	v_mfma_f32_16x16x32_bf16 v[0:3], v[182:185], v[214:217], v[0:3]
	v_mfma_f32_16x16x32_bf16 v[52:55], v[178:181], v[194:197], v[52:55]
	v_mfma_f32_16x16x32_bf16 v[48:51], v[186:189], v[194:197], v[48:51]
	v_mfma_f32_16x16x32_bf16 v[36:39], v[178:181], v[202:205], v[36:39]
	v_mfma_f32_16x16x32_bf16 v[32:35], v[186:189], v[202:205], v[32:35]
	v_mfma_f32_16x16x32_bf16 v[20:23], v[178:181], v[210:213], v[20:23]
	v_mfma_f32_16x16x32_bf16 v[16:19], v[186:189], v[210:213], v[16:19]
	v_mfma_f32_16x16x32_bf16 v[4:7], v[178:181], v[218:221], v[4:7]
	v_mfma_f32_16x16x32_bf16 v[0:3], v[186:189], v[218:221], v[0:3]
	s_setprio 0
	s_barrier
	s_add_i32 s63, s63, 2
	s_add_u32 s26, s26, 0x100
	s_addc_u32 s27, s27, 0
	s_add_u32 s61, s61, 0x100
	s_addc_u32 s62, s62, 0
	s_cmp_gt_u32 s63, 5
	s_cbranch_scc0 .LBB0_1650
	s_and_b64 vcc, exec, s[10:11]
	s_cbranch_vccz .LBB0_1653
	s_barrier

; #define PG8_STAGE(bufoff, gbase, voff) do { _Pragma("unroll") for (int _i = 0; _i < 2; ++_i) \
;         __builtin_amdgcn_global_load_lds((const unsigned*)((const char*)(gbase) + (voff)[_i]), (PG8_LAS unsigned*)(lds + (bufoff) + ldsw + _i * 8192), 16, 0, 0); } while (0)
; #define PG8_STAGE_A(b, h, gbase, NX) do { if constexpr (AM::GATHER) { const unsigned so_[2] = {(NX) ? gno[h][0] : gao[h][0], (NX) ? gno[h][1] : gao[h][1]}; PG8_STAGE(PG8_SA(b, h), gbase, so_); } \
;         else { PG8_STAGE(PG8_SA(b, h), (gbase) + (h) * hstep, voffA); } } while (0)
; #define PG8_LDA(dst, b, h) do { _Pragma("unroll") for (int m = 0; m < 4; ++m) _Pragma("unroll") for (int k = 0; k < 2; ++k) dst[m][k] = *(const PG8_LAS bf16x8*)(lds + PG8_SA(b, h) + aoff + m * 2048 + k * 1024); } while (0)
; #define PG8_LDB(dst, b, h) do { _Pragma("unroll") for (int n = 0; n < 2; ++n) _Pragma("unroll") for (int k = 0; k < 2; ++k) dst[n][k] = *(const PG8_LAS bf16x8*)(lds + PG8_SB(b, h) + boff + n * 2048 + k * 1024); } while (0)
; #define PG8_MMA(ai, bj, At, Bt) do { __builtin_amdgcn_s_setprio(1); _Pragma("unroll") for (int m = 0; m < 4; ++m) _Pragma("unroll") for (int n = 0; n < 2; ++n) _Pragma("unroll") for (int k = 0; k < 2; ++k) \
;         acc[ai][bj][m][n] = __builtin_amdgcn_mfma_f32_16x16x32_bf16(Bt[n][k], At[m][k], acc[ai][bj][m][n], 0, 0, 0); __builtin_amdgcn_s_setprio(0); } while (0)
; #define PG8_WAIT_V(n) asm volatile("s_waitcnt vmcnt(" #n ")" ::: "memory")
; #define PG8_WAIT_L(n) asm volatile("s_waitcnt lgkmcnt(" #n ")" ::: "memory")
; #define PG8_BAR __builtin_amdgcn_s_barrier()
; template <class Epi, class Sched, class AM, bool ALIGN_EPI = false, bool SP2 = false>
; __device__ __forceinline__ void gemm_phase(PG8_LAS unsigned char* lds, const Gemm g, const Sched& S, const Epi& E, const AM& am, const int wid_in) {
;     ...
;             if constexpr (SP2) {
;             PG8_LDB(B0, 0, 0); PG8_LDB(B1, 0, 1); PG8_SCHED; PG8_LDA(At, 0, 0); PG8_STAGE_A(1, 1, a1, false);
;             PG8_WAIT_V(8); PG8_WAIT_L(0); PG8_BAR; PG8_MMA(0, 0, At, B0); PG8_MMA(0, 1, At, B1); PG8_BAR; PG8_SCHED;
;             PG8_LDA(At, 0, 1); PG8_STAGE(PG8_SB(0, 0), b2, voffB); PG8_STAGE(PG8_SB(0, 1), b2 + hstep, voffB); PG8_STAGE_A(0, 0, a2, last);
;             PG8_WAIT_V(8); PG8_WAIT_L(0); PG8_BAR; PG8_MMA(1, 0, At, B0); PG8_MMA(1, 1, At, B1); PG8_BAR; PG8_SCHED;
.LBB0_1821:
	ds_read_b128 v[128:131], v180
	ds_read_b128 v[132:135], v180 offset:1024
	ds_read_b128 v[136:139], v180 offset:2048
	ds_read_b128 v[140:143], v180 offset:3072
	ds_read_b128 v[144:147], v181
	ds_read_b128 v[172:175], v181 offset:1024
	ds_read_b128 v[184:187], v181 offset:2048
	ds_read_b128 v[188:191], v181 offset:3072
	s_add_u32 s28, s26, 0xfffc0080
	s_addc_u32 s29, s27, -1
	s_cmp_eq_u32 s56, 12
	s_cselect_b32 s31, s19, s29
	s_cselect_b32 s30, s52, s28
	s_cselect_b32 s29, s17, s55
	s_cselect_b32 s28, s53, s54
	s_add_i32 m0, s40, 0xc000
	ds_read_b128 v[192:195], v182
	ds_read_b128 v[196:199], v182 offset:1024
	ds_read_b128 v[200:203], v182 offset:2048
	ds_read_b128 v[204:207], v182 offset:3072
	ds_read_b128 v[208:211], v182 offset:4096
	ds_read_b128 v[212:215], v182 offset:5120
	ds_read_b128 v[216:219], v182 offset:6144
	ds_read_b128 v[220:223], v182 offset:7168
	global_load_lds_dwordx4 v164, s[26:27]
	s_add_i32 m0, s40, 0xe000
	s_nop 0
	global_load_lds_dwordx4 v166, s[26:27]
	s_waitcnt vmcnt(8)
	s_waitcnt lgkmcnt(0)
	s_barrier
	s_setprio 1
	s_waitcnt lgkmcnt(0)
	v_mfma_f32_16x16x32_bf16 v[124:127], v[128:131], v[192:195], v[124:127]
	v_mfma_f32_16x16x32_bf16 v[120:123], v[136:139], v[192:195], v[120:123]
	v_mfma_f32_16x16x32_bf16 v[108:111], v[128:131], v[200:203], v[108:111]
	v_mfma_f32_16x16x32_bf16 v[104:107], v[136:139], v[200:203], v[104:107]
	v_mfma_f32_16x16x32_bf16 v[92:95], v[128:131], v[208:211], v[92:95]
	v_mfma_f32_16x16x32_bf16 v[88:91], v[136:139], v[208:211], v[88:91]
	v_mfma_f32_16x16x32_bf16 v[76:79], v[128:131], v[216:219], v[76:79]
	v_mfma_f32_16x16x32_bf16 v[72:75], v[136:139], v[216:219], v[72:75]
	v_mfma_f32_16x16x32_bf16 v[124:127], v[132:135], v[196:199], v[124:127]
	v_mfma_f32_16x16x32_bf16 v[120:123], v[140:143], v[196:199], v[120:123]
	v_mfma_f32_16x16x32_bf16 v[108:111], v[132:135], v[204:207], v[108:111]
	v_mfma_f32_16x16x32_bf16 v[104:107], v[140:143], v[204:207], v[104:107]
	v_mfma_f32_16x16x32_bf16 v[92:95], v[132:135], v[212:215], v[92:95]
	v_mfma_f32_16x16x32_bf16 v[88:91], v[140:143], v[212:215], v[88:91]
	v_mfma_f32_16x16x32_bf16 v[76:79], v[132:135], v[220:223], v[76:79]
	v_mfma_f32_16x16x32_bf16 v[72:75], v[140:143], v[220:223], v[72:75]
	s_setprio 0
	s_setprio 1
	v_mfma_f32_16x16x32_bf16 v[116:119], v[144:147], v[192:195], v[116:119]
	v_mfma_f32_16x16x32_bf16 v[112:115], v[184:187], v[192:195], v[112:115]
	v_mfma_f32_16x16x32_bf16 v[100:103], v[144:147], v[200:203], v[100:103]
	v_mfma_f32_16x16x32_bf16 v[96:99], v[184:187], v[200:203], v[96:99]
	v_mfma_f32_16x16x32_bf16 v[84:87], v[144:147], v[208:211], v[84:87]
	v_mfma_f32_16x16x32_bf16 v[80:83], v[184:187], v[208:211], v[80:83]
	v_mfma_f32_16x16x32_bf16 v[68:71], v[144:147], v[216:219], v[68:71]
	v_mfma_f32_16x16x32_bf16 v[64:67], v[184:187], v[216:219], v[64:67]
	v_mfma_f32_16x16x32_bf16 v[116:119], v[172:175], v[196:199], v[116:119]
	v_mfma_f32_16x16x32_bf16 v[112:115], v[188:191], v[196:199], v[112:115]
	v_mfma_f32_16x16x32_bf16 v[100:103], v[172:175], v[204:207], v[100:103]
	v_mfma_f32_16x16x32_bf16 v[96:99], v[188:191], v[204:207], v[96:99]
	v_mfma_f32_16x16x32_bf16 v[84:87], v[172:175], v[212:215], v[84:87]
	v_mfma_f32_16x16x32_bf16 v[80:83], v[188:191], v[212:215], v[80:83]
	v_mfma_f32_16x16x32_bf16 v[68:71], v[172:175], v[220:223], v[68:71]
	v_mfma_f32_16x16x32_bf16 v[64:67], v[188:191], v[220:223], v[64:67]
	s_setprio 0
	s_barrier
	s_add_u32 s98, s28, s10
	s_addc_u32 s99, s29, s11
	s_add_u32 s100, s30, s10
	s_addc_u32 s101, s31, s11
	s_add_i32 s57, s48, s38
	s_mov_b32 m0, s57
	ds_read_b128 v[192:195], v182 offset:16384
	ds_read_b128 v[196:199], v182 offset:17408
	ds_read_b128 v[200:203], v182 offset:18432
	ds_read_b128 v[204:207], v182 offset:19456
	ds_read_b128 v[208:211], v182 offset:20480
	ds_read_b128 v[212:215], v182 offset:21504
	ds_read_b128 v[216:219], v182 offset:22528
	ds_read_b128 v[220:223], v182 offset:23552
	global_load_lds_dwordx4 v154, s[28:29]
	s_add_i32 m0, s57, 0x2000
	s_add_u32 s58, s28, 0x40000
	s_addc_u32 s59, s29, 0
	s_add_i32 s57, s49, s38
	global_load_lds_dwordx4 v150, s[28:29]
	s_mov_b32 m0, s57
	s_nop 0
	global_load_lds_dwordx4 v154, s[58:59]
	s_add_i32 m0, s57, 0x2000
	s_nop 0
	global_load_lds_dwordx4 v150, s[58:59]
	s_mov_b32 m0, s40
	s_nop 0
	global_load_lds_dwordx4 v156, s[30:31]
	s_mov_b32 m0, s41
	s_nop 0
	global_load_lds_dwordx4 v152, s[30:31]
	s_waitcnt vmcnt(8)
	s_waitcnt lgkmcnt(0)
	s_barrier
	s_setprio 1
	s_waitcnt lgkmcnt(0)
	v_mfma_f32_16x16x32_bf16 v[60:63], v[128:131], v[192:195], v[60:63]
	v_mfma_f32_16x16x32_bf16 v[56:59], v[136:139], v[192:195], v[56:59]
	v_mfma_f32_16x16x32_bf16 v[44:47], v[128:131], v[200:203], v[44:47]
	v_mfma_f32_16x16x32_bf16 v[40:43], v[136:139], v[200:203], v[40:43]
	v_mfma_f32_16x16x32_bf16 v[28:31], v[128:131], v[208:211], v[28:31]
	v_mfma_f32_16x16x32_bf16 v[24:27], v[136:139], v[208:211], v[24:27]
	v_mfma_f32_16x16x32_bf16 v[12:15], v[128:131], v[216:219], v[12:15]
	v_mfma_f32_16x16x32_bf16 v[8:11], v[136:139], v[216:219], v[8:11]
	v_mfma_f32_16x16x32_bf16 v[60:63], v[132:135], v[196:199], v[60:63]
	v_mfma_f32_16x16x32_bf16 v[56:59], v[140:143], v[196:199], v[56:59]
	v_mfma_f32_16x16x32_bf16 v[44:47], v[132:135], v[204:207], v[44:47]
	v_mfma_f32_16x16x32_bf16 v[40:43], v[140:143], v[204:207], v[40:43]
	v_mfma_f32_16x16x32_bf16 v[28:31], v[132:135], v[212:215], v[28:31]
	v_mfma_f32_16x16x32_bf16 v[24:27], v[140:143], v[212:215], v[24:27]
	v_mfma_f32_16x16x32_bf16 v[12:15], v[132:135], v[220:223], v[12:15]
	v_mfma_f32_16x16x32_bf16 v[8:11], v[140:143], v[220:223], v[8:11]
	s_setprio 0
	s_setprio 1
	v_mfma_f32_16x16x32_bf16 v[52:55], v[144:147], v[192:195], v[52:55]
	v_mfma_f32_16x16x32_bf16 v[48:51], v[184:187], v[192:195], v[48:51]
	v_mfma_f32_16x16x32_bf16 v[36:39], v[144:147], v[200:203], v[36:39]
	v_mfma_f32_16x16x32_bf16 v[32:35], v[184:187], v[200:203], v[32:35]
	v_mfma_f32_16x16x32_bf16 v[20:23], v[144:147], v[208:211], v[20:23]
	v_mfma_f32_16x16x32_bf16 v[16:19], v[184:187], v[208:211], v[16:19]
	v_mfma_f32_16x16x32_bf16 v[4:7], v[144:147], v[216:219], v[4:7]
	v_mfma_f32_16x16x32_bf16 v[0:3], v[184:187], v[216:219], v[0:3]
	v_mfma_f32_16x16x32_bf16 v[52:55], v[172:175], v[196:199], v[52:55]
	v_mfma_f32_16x16x32_bf16 v[48:51], v[188:191], v[196:199], v[48:51]
	v_mfma_f32_16x16x32_bf16 v[36:39], v[172:175], v[204:207], v[36:39]
	v_mfma_f32_16x16x32_bf16 v[32:35], v[188:191], v[204:207], v[32:35]
	v_mfma_f32_16x16x32_bf16 v[20:23], v[172:175], v[212:215], v[20:23]
	v_mfma_f32_16x16x32_bf16 v[16:19], v[188:191], v[212:215], v[16:19]
	v_mfma_f32_16x16x32_bf16 v[4:7], v[172:175], v[220:223], v[4:7]
	v_mfma_f32_16x16x32_bf16 v[0:3], v[188:191], v[220:223], v[0:3]
	s_setprio 0
	s_barrier
; #define PG8_STAGE(bufoff, gbase, voff) do { _Pragma("unroll") for (int _i = 0; _i < 2; ++_i) \
;         __builtin_amdgcn_global_load_lds((const unsigned*)((const char*)(gbase) + (voff)[_i]), (PG8_LAS unsigned*)(lds + (bufoff) + ldsw + _i * 8192), 16, 0, 0); } while (0)
; #define PG8_STAGE_A(b, h, gbase, NX) do { if constexpr (AM::GATHER) { const unsigned so_[2] = {(NX) ? gno[h][0] : gao[h][0], (NX) ? gno[h][1] : gao[h][1]}; PG8_STAGE(PG8_SA(b, h), gbase, so_); } \
;         else { PG8_STAGE(PG8_SA(b, h), (gbase) + (h) * hstep, voffA); } } while (0)
; #define PG8_LDA(dst, b, h) do { _Pragma("unroll") for (int m = 0; m < 4; ++m) _Pragma("unroll") for (int k = 0; k < 2; ++k) dst[m][k] = *(const PG8_LAS bf16x8*)(lds + PG8_SA(b, h) + aoff + m * 2048 + k * 1024); } while (0)
; #define PG8_LDB(dst, b, h) do { _Pragma("unroll") for (int n = 0; n < 2; ++n) _Pragma("unroll") for (int k = 0; k < 2; ++k) dst[n][k] = *(const PG8_LAS bf16x8*)(lds + PG8_SB(b, h) + boff + n * 2048 + k * 1024); } while (0)
; #define PG8_MMA(ai, bj, At, Bt) do { __builtin_amdgcn_s_setprio(1); _Pragma("unroll") for (int m = 0; m < 4; ++m) _Pragma("unroll") for (int n = 0; n < 2; ++n) _Pragma("unroll") for (int k = 0; k < 2; ++k) \
;         acc[ai][bj][m][n] = __builtin_amdgcn_mfma_f32_16x16x32_bf16(Bt[n][k], At[m][k], acc[ai][bj][m][n], 0, 0, 0); __builtin_amdgcn_s_setprio(0); } while (0)
; #define PG8_WAIT_V(n) asm volatile("s_waitcnt vmcnt(" #n ")" ::: "memory")
; #define PG8_WAIT_L(n) asm volatile("s_waitcnt lgkmcnt(" #n ")" ::: "memory")
; #define PG8_BAR __builtin_amdgcn_s_barrier()
; #define PG8_SCHED __builtin_amdgcn_sched_barrier(0)
; template <class Epi, class Sched, class AM, bool ALIGN_EPI = false, bool SP2 = false>
; __device__ __forceinline__ void gemm_phase(PG8_LAS unsigned char* lds, const Gemm g, const Sched& S, const Epi& E, const AM& am, const int wid_in) {
;     ...
;             PG8_LDB(B0, 1, 0); PG8_LDB(B1, 1, 1); PG8_SCHED; PG8_LDA(At, 1, 0); PG8_STAGE_A(0, 1, a2, last);
;             PG8_WAIT_V(8); PG8_WAIT_L(0); PG8_BAR; PG8_MMA(0, 0, At, B0); PG8_MMA(0, 1, At, B1); PG8_BAR; PG8_SCHED;
;             PG8_LDA(At, 1, 1); PG8_STAGE(PG8_SB(1, 0), b3, voffB); PG8_STAGE(PG8_SB(1, 1), b3 + hstep, voffB); PG8_STAGE_A(1, 0, a3, last);
;             PG8_WAIT_V(8); PG8_WAIT_L(0); PG8_BAR; PG8_MMA(1, 0, At, B0); PG8_MMA(1, 1, At, B1); PG8_BAR; PG8_SCHED;
	s_add_i32 s57, 0, 0x18000
	s_add_i32 s58, 0, 0x1c000
	v_add_u32_e32 v140, s57, v177
	v_add_u32_e32 v188, s58, v177
	ds_read_b128 v[128:131], v140
	ds_read_b128 v[132:135], v140 offset:1024
	ds_read_b128 v[136:139], v140 offset:2048
	ds_read_b128 v[140:143], v140 offset:3072
	ds_read_b128 v[144:147], v188
	ds_read_b128 v[172:175], v188 offset:1024
	ds_read_b128 v[184:187], v188 offset:2048
	ds_read_b128 v[188:191], v188 offset:3072
	s_add_u32 s30, s30, 0x40000
	s_addc_u32 s31, s31, 0
	s_mov_b32 m0, s42
	ds_read_b128 v[192:195], v182 offset:32768
	ds_read_b128 v[196:199], v182 offset:33792
	ds_read_b128 v[200:203], v182 offset:34816
	ds_read_b128 v[204:207], v182 offset:35840
	ds_read_b128 v[208:211], v182 offset:36864
	ds_read_b128 v[212:215], v182 offset:37888
	ds_read_b128 v[216:219], v182 offset:38912
	ds_read_b128 v[220:223], v182 offset:39936
	global_load_lds_dwordx4 v156, s[30:31]
	s_mov_b32 m0, s43
	s_nop 0
	global_load_lds_dwordx4 v152, s[30:31]
	s_waitcnt vmcnt(8)
	s_waitcnt lgkmcnt(0)
	s_barrier
	s_setprio 1
	s_waitcnt lgkmcnt(0)
	v_mfma_f32_16x16x32_bf16 v[124:127], v[128:131], v[192:195], v[124:127]
	v_mfma_f32_16x16x32_bf16 v[120:123], v[136:139], v[192:195], v[120:123]
	v_mfma_f32_16x16x32_bf16 v[108:111], v[128:131], v[200:203], v[108:111]
	v_mfma_f32_16x16x32_bf16 v[104:107], v[136:139], v[200:203], v[104:107]
	v_mfma_f32_16x16x32_bf16 v[92:95], v[128:131], v[208:211], v[92:95]
	v_mfma_f32_16x16x32_bf16 v[88:91], v[136:139], v[208:211], v[88:91]
	v_mfma_f32_16x16x32_bf16 v[76:79], v[128:131], v[216:219], v[76:79]
	v_mfma_f32_16x16x32_bf16 v[72:75], v[136:139], v[216:219], v[72:75]
	v_mfma_f32_16x16x32_bf16 v[124:127], v[132:135], v[196:199], v[124:127]
	v_mfma_f32_16x16x32_bf16 v[120:123], v[140:143], v[196:199], v[120:123]
	v_mfma_f32_16x16x32_bf16 v[108:111], v[132:135], v[204:207], v[108:111]
	v_mfma_f32_16x16x32_bf16 v[104:107], v[140:143], v[204:207], v[104:107]
	v_mfma_f32_16x16x32_bf16 v[92:95], v[132:135], v[212:215], v[92:95]
	v_mfma_f32_16x16x32_bf16 v[88:91], v[140:143], v[212:215], v[88:91]
	v_mfma_f32_16x16x32_bf16 v[76:79], v[132:135], v[220:223], v[76:79]
	v_mfma_f32_16x16x32_bf16 v[72:75], v[140:143], v[220:223], v[72:75]
	s_setprio 0
	s_setprio 1
	v_mfma_f32_16x16x32_bf16 v[116:119], v[144:147], v[192:195], v[116:119]
	v_mfma_f32_16x16x32_bf16 v[112:115], v[184:187], v[192:195], v[112:115]
	v_mfma_f32_16x16x32_bf16 v[100:103], v[144:147], v[200:203], v[100:103]
	v_mfma_f32_16x16x32_bf16 v[96:99], v[184:187], v[200:203], v[96:99]
	v_mfma_f32_16x16x32_bf16 v[84:87], v[144:147], v[208:211], v[84:87]
	v_mfma_f32_16x16x32_bf16 v[80:83], v[184:187], v[208:211], v[80:83]
	v_mfma_f32_16x16x32_bf16 v[68:71], v[144:147], v[216:219], v[68:71]
	v_mfma_f32_16x16x32_bf16 v[64:67], v[184:187], v[216:219], v[64:67]
	v_mfma_f32_16x16x32_bf16 v[116:119], v[172:175], v[196:199], v[116:119]
	v_mfma_f32_16x16x32_bf16 v[112:115], v[188:191], v[196:199], v[112:115]
	v_mfma_f32_16x16x32_bf16 v[100:103], v[172:175], v[204:207], v[100:103]
	v_mfma_f32_16x16x32_bf16 v[96:99], v[188:191], v[204:207], v[96:99]
	v_mfma_f32_16x16x32_bf16 v[84:87], v[172:175], v[212:215], v[84:87]
	v_mfma_f32_16x16x32_bf16 v[80:83], v[188:191], v[212:215], v[80:83]
	v_mfma_f32_16x16x32_bf16 v[68:71], v[172:175], v[220:223], v[68:71]
	v_mfma_f32_16x16x32_bf16 v[64:67], v[188:191], v[220:223], v[64:67]
	s_setprio 0
	s_barrier
	s_add_i32 s30, s57, s38
	s_mov_b32 m0, s30
	ds_read_b128 v[192:195], v182 offset:49152
	ds_read_b128 v[196:199], v182 offset:50176
	ds_read_b128 v[200:203], v182 offset:51200
	ds_read_b128 v[204:207], v182 offset:52224
	ds_read_b128 v[208:211], v182 offset:53248
	ds_read_b128 v[212:215], v182 offset:54272
	ds_read_b128 v[216:219], v182 offset:55296
	ds_read_b128 v[220:223], v182 offset:56320
	global_load_lds_dwordx4 v154, s[98:99]
	s_add_i32 m0, s30, 0x2000
	s_add_u32 s28, s28, 0x40080
	s_addc_u32 s29, s29, 0
	s_add_i32 s30, s58, s38
	global_load_lds_dwordx4 v150, s[98:99]
	s_mov_b32 m0, s30
	s_nop 0
	global_load_lds_dwordx4 v154, s[28:29]
	s_add_i32 m0, s30, 0x2000
	s_nop 0
	global_load_lds_dwordx4 v150, s[28:29]
	s_mov_b32 m0, s45
	s_nop 0
	global_load_lds_dwordx4 v156, s[100:101]
	s_mov_b32 m0, s46
	s_nop 0
	global_load_lds_dwordx4 v152, s[100:101]
	s_waitcnt vmcnt(8)
	s_waitcnt lgkmcnt(0)
	s_barrier
	s_setprio 1
	s_waitcnt lgkmcnt(0)
	v_mfma_f32_16x16x32_bf16 v[60:63], v[128:131], v[192:195], v[60:63]
	v_mfma_f32_16x16x32_bf16 v[56:59], v[136:139], v[192:195], v[56:59]
	v_mfma_f32_16x16x32_bf16 v[44:47], v[128:131], v[200:203], v[44:47]
	v_mfma_f32_16x16x32_bf16 v[40:43], v[136:139], v[200:203], v[40:43]
	v_mfma_f32_16x16x32_bf16 v[28:31], v[128:131], v[208:211], v[28:31]
	v_mfma_f32_16x16x32_bf16 v[24:27], v[136:139], v[208:211], v[24:27]
	v_mfma_f32_16x16x32_bf16 v[12:15], v[128:131], v[216:219], v[12:15]
	v_mfma_f32_16x16x32_bf16 v[8:11], v[136:139], v[216:219], v[8:11]
	v_mfma_f32_16x16x32_bf16 v[60:63], v[132:135], v[196:199], v[60:63]
	v_mfma_f32_16x16x32_bf16 v[56:59], v[140:143], v[196:199], v[56:59]
	v_mfma_f32_16x16x32_bf16 v[44:47], v[132:135], v[204:207], v[44:47]
	v_mfma_f32_16x16x32_bf16 v[40:43], v[140:143], v[204:207], v[40:43]
	v_mfma_f32_16x16x32_bf16 v[28:31], v[132:135], v[212:215], v[28:31]
	v_mfma_f32_16x16x32_bf16 v[24:27], v[140:143], v[212:215], v[24:27]
	v_mfma_f32_16x16x32_bf16 v[12:15], v[132:135], v[220:223], v[12:15]
	v_mfma_f32_16x16x32_bf16 v[8:11], v[140:143], v[220:223], v[8:11]
	s_setprio 0
	s_setprio 1
	v_mfma_f32_16x16x32_bf16 v[52:55], v[144:147], v[192:195], v[52:55]
	v_mfma_f32_16x16x32_bf16 v[48:51], v[184:187], v[192:195], v[48:51]
	v_mfma_f32_16x16x32_bf16 v[36:39], v[144:147], v[200:203], v[36:39]
	v_mfma_f32_16x16x32_bf16 v[32:35], v[184:187], v[200:203], v[32:35]
	v_mfma_f32_16x16x32_bf16 v[20:23], v[144:147], v[208:211], v[20:23]
	v_mfma_f32_16x16x32_bf16 v[16:19], v[184:187], v[208:211], v[16:19]
	v_mfma_f32_16x16x32_bf16 v[4:7], v[144:147], v[216:219], v[4:7]
	v_mfma_f32_16x16x32_bf16 v[0:3], v[184:187], v[216:219], v[0:3]
	v_mfma_f32_16x16x32_bf16 v[52:55], v[172:175], v[196:199], v[52:55]
	v_mfma_f32_16x16x32_bf16 v[48:51], v[188:191], v[196:199], v[48:51]
	v_mfma_f32_16x16x32_bf16 v[36:39], v[172:175], v[204:207], v[36:39]
	v_mfma_f32_16x16x32_bf16 v[32:35], v[188:191], v[204:207], v[32:35]
	v_mfma_f32_16x16x32_bf16 v[20:23], v[172:175], v[212:215], v[20:23]
	v_mfma_f32_16x16x32_bf16 v[16:19], v[188:191], v[212:215], v[16:19]
	v_mfma_f32_16x16x32_bf16 v[4:7], v[172:175], v[220:223], v[4:7]
	v_mfma_f32_16x16x32_bf16 v[0:3], v[188:191], v[220:223], v[0:3]
	s_setprio 0
	s_barrier
	s_add_i32 s56, s56, 2
	s_add_u32 s26, s26, 0x100
	s_addc_u32 s27, s27, 0
	s_add_u32 s54, s54, 0x100
	s_addc_u32 s55, s55, 0
	s_cmp_gt_u32 s56, 13
	s_cbranch_scc0 .LBB0_1821
	s_and_b64 vcc, exec, s[12:13]
	s_cbranch_vccz .LBB0_1824
	s_barrier

; __host__ __device__ __forceinline__ size_t qkv_block(int typ, int g, int b, int h) { return (size_t)((((typ * 3 + g) * 16 + b) * 8 + h)) * (4096 * 64); }
; __host__ __device__ __forceinline__ int qkv_row(int pos, int g) { const int dsh = 2 * g; return ((pos & ((1 << dsh) - 1)) << (12 - dsh)) + (pos >> dsh); }
; __device__ __forceinline__ u32x4 pack8(const f32x4 v0, const f32x4 v1) { u32x4 w; w.x = cvt_pk_bf16(v0[0], v0[1]); w.y = cvt_pk_bf16(v0[2], v0[3]); w.z = cvt_pk_bf16(v1[0], v1[1]); w.w = cvt_pk_bf16(v1[2], v1[3]); return w; }
;     __device__ __forceinline__ void operator()(const f32x4 (&acc)[2][2][4][2], const Unit& u, int wr, int wc, int fr, int fq) const {
;     ...
;         const int typ = (u.pn % 6) >> 1, gq_ = u.pn / 6;
;         const bool rl = (typ < 2) && ((wc & 1) == 0) && (fq < 2);
;         const float sc = (typ == 0) ? QSCALE : 1.0f;
; #pragma unroll
;         for (int ai = 0; ai < 2; ++ai)
; #pragma unroll
;         for (int mp = 0; mp < 2; ++mp) {
;             f32x4 csv[2], snv[2];
; #pragma unroll
;             for (int mm = 0; mm < 2; ++mm) { const int pos = (row0 + ai * HALF + (2 * mp + mm) * 16) & (SEQ - 1);
;                 csv[mm] = *(const f32x4*)(rope + pos * 8 + 4 * (fq & 1)); snv[mm] = *(const f32x4*)(rope + 4096 * 8 + pos * 8 + 4 * (fq & 1)); }
; #pragma unroll
;             for (int mm = 0; mm < 2; ++mm) {
;                 const int m = 2 * mp + mm, row = row0 + ai * HALF + m * 16;
;                 f32x4 cs = {1.f, 1.f, 1.f, 1.f}, sn = {0.f, 0.f, 0.f, 0.f};
;                 if (rl) { cs = csv[mm]; sn = snv[mm]; }
; #pragma unroll
;                 for (int bj = 0; bj < 2; ++bj) {
;                     const f32x4 x1 = acc[ai][bj][m][0], x2 = acc[ai][bj][m][1];
;                     const f32x4 r1 = (x1 * cs - x2 * sn) * sc, r2 = (x2 * cs + x1 * sn) * sc;
;                     { const int tok = row_off + row - fr + tr_, hh = 4 * (u.pn & 1) + 2 * bj + (wc >> 1);
;                       *(u32x4*)(O + qkv_block(typ, gq_, tok >> 12, hh) + (size_t)qkv_row(tok & (SEQ - 1), gq_) * 64 + 32 * (wc & 1) + 8 * tq_) = xpose4x16(pack8(r1, r2), sa_); }
.LBB0_1825:
	s_mul_hi_i32 s17, s51, 0x2aaaaaab
	s_lshl_b32 s19, s24, 8
	s_lshr_b32 s24, s17, 31
	s_add_i32 s17, s17, s24
	s_mul_i32 s24, s17, 6
	s_add_i32 s19, s19, s44
	s_sub_i32 s28, s51, s24
	v_or_b32_e32 v128, s19, v176
	s_ashr_i32 s29, s28, 1
	s_cmp_lt_i32 s29, 2
	v_lshlrev_b32_e32 v185, 3, v128
	s_cselect_b64 s[24:25], -1, 0
	v_and_b32_e32 v129, 0x7e78, v185
	s_and_b64 s[24:25], s[14:15], s[24:25]
	v_mov_b32_e32 v128, 0
	v_mov_b32_e32 v132, 1.0
	v_lshlrev_b32_e32 v174, 2, v129
	v_mov_b32_e32 v134, 1.0
	v_mov_b32_e32 v135, 1.0
	v_mov_b32_e32 v136, 1.0
	v_mov_b32_e32 v137, 1.0
	v_mov_b32_e32 v138, 0
	v_mov_b32_e32 v139, 0
	v_mov_b32_e32 v140, 0
	v_mov_b32_e32 v141, 0
	v_mov_b32_e32 v142, 0
	v_mov_b32_e32 v143, 0
	v_mov_b32_e32 v144, 0
	v_mov_b32_e32 v145, 0
	v_mov_b32_e32 v146, 1.0
	v_mov_b32_e32 v147, 1.0
	v_mov_b32_e32 v148, 1.0
	v_mov_b32_e32 v149, 1.0
	s_and_saveexec_b64 s[26:27], s[24:25]
	s_cbranch_execz .LBB0_1827
	v_mov_b32_e32 v175, v159
	v_lshl_add_u64 v[134:135], v[162:163], 0, v[174:175]
	v_lshl_add_u64 v[130:131], v[160:161], 0, v[174:175]
	global_load_dwordx4 v[138:141], v[134:135], off offset:512
	global_load_dwordx4 v[142:145], v[134:135], off
	s_nop 0
	global_load_dwordx4 v[134:137], v[130:131], off offset:512
	global_load_dwordx4 v[146:149], v[130:131], off
.LBB0_1827:
	s_or_b64 exec, exec, s[26:27]
	s_cmp_lt_u32 s28, 2
	s_cselect_b64 vcc, -1, 0
	v_add_u32_e32 v184, s19, v178
	s_lshl_b32 s19, s51, 2
	s_waitcnt vmcnt(0)
	v_pk_mul_f32 v[186:187], v[120:121], v[142:143]
	v_pk_mul_f32 v[120:121], v[120:121], v[146:147]
	v_cndmask_b32_e32 v172, 1.0, v183, vcc
	s_and_b32 s19, s19, 4
	v_pk_mul_f32 v[130:131], v[122:123], v[144:145]
	v_pk_fma_f32 v[186:187], v[124:125], v[146:147], v[186:187] neg_lo:[0,0,1] neg_hi:[0,0,1]
	v_pk_fma_f32 v[120:121], v[124:125], v[142:143], v[120:121]
	s_or_b32 s28, s19, s47
	s_mul_i32 s19, s29, 3
	v_pk_fma_f32 v[130:131], v[126:127], v[148:149], v[130:131] neg_lo:[0,0,1] neg_hi:[0,0,1]
	v_pk_mul_f32 v[186:187], v[172:173], v[186:187] op_sel_hi:[0,1]
	v_pk_mul_f32 v[122:123], v[122:123], v[148:149]
	v_pk_mul_f32 v[120:121], v[172:173], v[120:121] op_sel_hi:[0,1]
	v_cvt_pk_bf16_f32 v124, v186, v187
	s_add_i32 s19, s19, s17
	v_pk_mul_f32 v[130:131], v[172:173], v[130:131] op_sel_hi:[0,1]
	v_pk_fma_f32 v[122:123], v[126:127], v[144:145], v[122:123]
	v_cvt_pk_bf16_f32 v125, v130, v131
	v_cvt_pk_bf16_f32 v126, v120, v121
	ds_bpermute_b32 v120, v179, v124
	v_ashrrev_i32_e32 v124, 9, v184
	s_lshl_b32 s29, s19, 7
	v_and_b32_e32 v124, -8, v124
	s_lshl_b32 s17, s17, 1
	v_add_u32_e32 v129, s29, v124
	s_sub_i32 s19, 12, s17
	v_pk_mul_f32 v[122:123], v[172:173], v[122:123] op_sel_hi:[0,1]
	v_or_b32_e32 v124, s28, v129
	v_cvt_pk_bf16_f32 v123, v122, v123
	ds_bpermute_b32 v121, v179, v125
	ds_bpermute_b32 v122, v179, v126
	v_ashrrev_i32_e32 v125, 31, v124
	v_and_b32_e32 v126, 0xfff, v184
	v_lshlrev_b32_e32 v127, s19, v184
	ds_bpermute_b32 v123, v179, v123
	v_lshlrev_b64 v[124:125], 19, v[124:125]
	v_and_b32_e32 v127, 0xfff, v127
	v_lshrrev_b32_e32 v126, s17, v126
	v_lshl_add_u64 v[124:125], s[6:7], 0, v[124:125]
	v_add_lshl_u32 v126, v127, v126, 7
	v_mov_b32_e32 v127, v159
	v_lshl_add_u64 v[124:125], v[124:125], 0, v[126:127]
	v_lshl_add_u64 v[124:125], v[124:125], 0, s[2:3]
	v_lshl_add_u64 v[124:125], v[124:125], 0, v[158:159]
	s_waitcnt lgkmcnt(0)
	global_store_dwordx4 v[124:125], v[120:123], off
	s_or_b32 s30, s28, 2
	v_mov_b32_e32 v133, 1.0
	v_pk_mul_f32 v[122:123], v[112:113], v[142:143]
	v_pk_mul_f32 v[112:113], v[112:113], v[146:147]
	v_pk_mul_f32 v[120:121], v[114:115], v[144:145]
	v_pk_fma_f32 v[122:123], v[116:117], v[146:147], v[122:123] neg_lo:[0,0,1] neg_hi:[0,0,1]
	v_pk_mul_f32 v[114:115], v[114:115], v[148:149]
	v_pk_fma_f32 v[112:113], v[116:117], v[142:143], v[112:113]
	v_pk_fma_f32 v[120:121], v[118:119], v[148:149], v[120:121] neg_lo:[0,0,1] neg_hi:[0,0,1]
	v_pk_mul_f32 v[122:123], v[172:173], v[122:123] op_sel_hi:[0,1]
	v_pk_fma_f32 v[114:115], v[118:119], v[144:145], v[114:115]
	v_pk_mul_f32 v[112:113], v[172:173], v[112:113] op_sel_hi:[0,1]
	v_cvt_pk_bf16_f32 v116, v122, v123
	v_pk_mul_f32 v[120:121], v[172:173], v[120:121] op_sel_hi:[0,1]
	v_pk_mul_f32 v[114:115], v[172:173], v[114:115] op_sel_hi:[0,1]
	v_cvt_pk_bf16_f32 v117, v120, v121
	v_cvt_pk_bf16_f32 v118, v112, v113
	ds_bpermute_b32 v112, v179, v116
	v_or_b32_e32 v116, s30, v129
	v_cvt_pk_bf16_f32 v115, v114, v115
	ds_bpermute_b32 v113, v179, v117
	v_ashrrev_i32_e32 v117, 31, v116
	ds_bpermute_b32 v114, v179, v118
	ds_bpermute_b32 v115, v179, v115
	v_lshlrev_b64 v[116:117], 19, v[116:117]
	v_lshl_add_u64 v[116:117], s[6:7], 0, v[116:117]
	v_lshl_add_u64 v[116:117], v[116:117], 0, v[126:127]
	v_lshl_add_u64 v[116:117], v[116:117], 0, s[2:3]
	v_lshl_add_u64 v[116:117], v[116:117], 0, v[158:159]
	s_waitcnt lgkmcnt(0)
; __host__ __device__ __forceinline__ size_t qkv_block(int typ, int g, int b, int h) { return (size_t)((((typ * 3 + g) * 16 + b) * 8 + h)) * (4096 * 64); }
; __host__ __device__ __forceinline__ int qkv_row(int pos, int g) { const int dsh = 2 * g; return ((pos & ((1 << dsh) - 1)) << (12 - dsh)) + (pos >> dsh); }
; __device__ __forceinline__ u32x4 pack8(const f32x4 v0, const f32x4 v1) { u32x4 w; w.x = cvt_pk_bf16(v0[0], v0[1]); w.y = cvt_pk_bf16(v0[2], v0[3]); w.z = cvt_pk_bf16(v1[0], v1[1]); w.w = cvt_pk_bf16(v1[2], v1[3]); return w; }
;     __device__ __forceinline__ void operator()(const f32x4 (&acc)[2][2][4][2], const Unit& u, int wr, int wc, int fr, int fq) const {
;     ...
;             for (int mm = 0; mm < 2; ++mm) { const int pos = (row0 + ai * HALF + (2 * mp + mm) * 16) & (SEQ - 1);
;                 csv[mm] = *(const f32x4*)(rope + pos * 8 + 4 * (fq & 1)); snv[mm] = *(const f32x4*)(rope + 4096 * 8 + pos * 8 + 4 * (fq & 1)); }
; #pragma unroll
;             for (int mm = 0; mm < 2; ++mm) {
;                 const int m = 2 * mp + mm, row = row0 + ai * HALF + m * 16;
;                 f32x4 cs = {1.f, 1.f, 1.f, 1.f}, sn = {0.f, 0.f, 0.f, 0.f};
;                 if (rl) { cs = csv[mm]; sn = snv[mm]; }
; #pragma unroll
;                 for (int bj = 0; bj < 2; ++bj) {
;                     const f32x4 x1 = acc[ai][bj][m][0], x2 = acc[ai][bj][m][1];
;                     const f32x4 r1 = (x1 * cs - x2 * sn) * sc, r2 = (x2 * cs + x1 * sn) * sc;
;                     { const int tok = row_off + row - fr + tr_, hh = 4 * (u.pn & 1) + 2 * bj + (wc >> 1);
;                       *(u32x4*)(O + qkv_block(typ, gq_, tok >> 12, hh) + (size_t)qkv_row(tok & (SEQ - 1), gq_) * 64 + 32 * (wc & 1) + 8 * tq_) = xpose4x16(pack8(r1, r2), sa_); }
;                 }
;             }
;             asm volatile("" ::: "memory");
	global_store_dwordx4 v[116:117], v[112:115], off
	v_add_u32_e32 v116, 16, v184
	v_mov_b32_e32 v129, 0
	v_pk_mul_f32 v[114:115], v[104:105], v[138:139]
	v_pk_mul_f32 v[112:113], v[106:107], v[140:141]
	v_pk_fma_f32 v[114:115], v[108:109], v[134:135], v[114:115] neg_lo:[0,0,1] neg_hi:[0,0,1]
	v_pk_mul_f32 v[108:109], v[108:109], v[138:139]
	v_pk_fma_f32 v[112:113], v[110:111], v[136:137], v[112:113] neg_lo:[0,0,1] neg_hi:[0,0,1]
	v_pk_fma_f32 v[104:105], v[104:105], v[134:135], v[108:109]
	v_pk_mul_f32 v[114:115], v[172:173], v[114:115] op_sel_hi:[0,1]
	v_pk_mul_f32 v[110:111], v[110:111], v[140:141]
	v_pk_mul_f32 v[104:105], v[172:173], v[104:105] op_sel_hi:[0,1]
	v_cvt_pk_bf16_f32 v108, v114, v115
	v_pk_mul_f32 v[112:113], v[172:173], v[112:113] op_sel_hi:[0,1]
	v_pk_fma_f32 v[106:107], v[106:107], v[136:137], v[110:111]
	v_cvt_pk_bf16_f32 v109, v112, v113
	v_cvt_pk_bf16_f32 v110, v104, v105
	ds_bpermute_b32 v104, v179, v108
	v_ashrrev_i32_e32 v108, 9, v116
	v_and_b32_e32 v108, -8, v108
	v_add_u32_e32 v112, s29, v108
	v_pk_mul_f32 v[106:107], v[172:173], v[106:107] op_sel_hi:[0,1]
	v_or_b32_e32 v108, s28, v112
	v_cvt_pk_bf16_f32 v107, v106, v107
	ds_bpermute_b32 v105, v179, v109
	ds_bpermute_b32 v106, v179, v110
	v_ashrrev_i32_e32 v109, 31, v108
	v_and_b32_e32 v110, 0xfff, v116
	v_lshlrev_b32_e32 v111, s19, v116
	ds_bpermute_b32 v107, v179, v107
	v_lshlrev_b64 v[108:109], 19, v[108:109]
	v_and_b32_e32 v111, 0xfff, v111
	v_lshrrev_b32_e32 v110, s17, v110
	v_lshl_add_u64 v[108:109], s[6:7], 0, v[108:109]
	v_add_lshl_u32 v110, v111, v110, 7
	v_mov_b32_e32 v111, v159
	v_lshl_add_u64 v[108:109], v[108:109], 0, v[110:111]
	v_lshl_add_u64 v[108:109], v[108:109], 0, s[2:3]
	v_lshl_add_u64 v[108:109], v[108:109], 0, v[158:159]
	s_waitcnt lgkmcnt(0)
	global_store_dwordx4 v[108:109], v[104:107], off
	v_mov_b32_e32 v130, 0
	v_mov_b32_e32 v131, 0
	v_pk_mul_f32 v[106:107], v[96:97], v[138:139]
	v_pk_mul_f32 v[104:105], v[98:99], v[140:141]
	v_pk_fma_f32 v[106:107], v[100:101], v[134:135], v[106:107] neg_lo:[0,0,1] neg_hi:[0,0,1]
	v_pk_mul_f32 v[100:101], v[100:101], v[138:139]
	v_pk_fma_f32 v[104:105], v[102:103], v[136:137], v[104:105] neg_lo:[0,0,1] neg_hi:[0,0,1]
	v_pk_mul_f32 v[102:103], v[102:103], v[140:141]
	v_pk_fma_f32 v[96:97], v[96:97], v[134:135], v[100:101]
	v_pk_mul_f32 v[106:107], v[172:173], v[106:107] op_sel_hi:[0,1]
	v_pk_fma_f32 v[98:99], v[98:99], v[136:137], v[102:103]
	v_pk_mul_f32 v[96:97], v[172:173], v[96:97] op_sel_hi:[0,1]
	v_cvt_pk_bf16_f32 v100, v106, v107
	v_pk_mul_f32 v[104:105], v[172:173], v[104:105] op_sel_hi:[0,1]
	v_pk_mul_f32 v[98:99], v[172:173], v[98:99] op_sel_hi:[0,1]
	v_cvt_pk_bf16_f32 v101, v104, v105
	v_cvt_pk_bf16_f32 v102, v96, v97
	ds_bpermute_b32 v96, v179, v100
	v_or_b32_e32 v100, s30, v112
	v_cvt_pk_bf16_f32 v99, v98, v99
	ds_bpermute_b32 v97, v179, v101
	v_ashrrev_i32_e32 v101, 31, v100
	ds_bpermute_b32 v98, v179, v102
	ds_bpermute_b32 v99, v179, v99
	v_lshlrev_b64 v[100:101], 19, v[100:101]
	v_lshl_add_u64 v[100:101], s[6:7], 0, v[100:101]
	v_lshl_add_u64 v[100:101], v[100:101], 0, v[110:111]
	v_lshl_add_u64 v[100:101], v[100:101], 0, s[2:3]
	v_lshl_add_u64 v[100:101], v[100:101], 0, v[158:159]
	s_waitcnt lgkmcnt(0)
	global_store_dwordx4 v[100:101], v[96:99], off
	v_mov_b32_e32 v134, 1.0
	v_mov_b32_e32 v135, 1.0
	v_mov_b32_e32 v96, 0
	v_mov_b32_e32 v97, 0
	v_mov_b32_e32 v98, 0
	v_mov_b32_e32 v99, 0
	v_mov_b32_e32 v100, 1.0
	v_mov_b32_e32 v101, 1.0
	v_mov_b32_e32 v102, 1.0
	v_mov_b32_e32 v103, 1.0
	s_and_saveexec_b64 s[26:27], s[24:25]
	s_cbranch_execz .LBB0_1829
	v_mov_b32_e32 v175, v159
	v_lshl_add_u64 v[100:101], v[160:161], 0, v[174:175]
	v_lshl_add_u64 v[96:97], v[162:163], 0, v[174:175]
	global_load_dwordx4 v[128:131], v[96:97], off offset:1536
	s_nop 0
	global_load_dwordx4 v[96:99], v[96:97], off offset:1024
	s_nop 0
	global_load_dwordx4 v[132:135], v[100:101], off offset:1536
	s_nop 0
	global_load_dwordx4 v[100:103], v[100:101], off offset:1024
.LBB0_1829:
	s_or_b64 exec, exec, s[26:27]
	s_waitcnt vmcnt(2)
	v_pk_mul_f32 v[106:107], v[88:89], v[96:97]
	s_waitcnt vmcnt(0)
	v_pk_mul_f32 v[88:89], v[88:89], v[100:101]
	v_mov_b32_e32 v173, v172
	v_pk_mul_f32 v[104:105], v[90:91], v[98:99]
	v_pk_fma_f32 v[106:107], v[92:93], v[100:101], v[106:107] neg_lo:[0,0,1] neg_hi:[0,0,1]
	v_pk_fma_f32 v[88:89], v[92:93], v[96:97], v[88:89]
	v_add_u32_e32 v110, 32, v184
	v_pk_fma_f32 v[108:109], v[94:95], v[102:103], v[104:105] neg_lo:[0,0,1] neg_hi:[0,0,1]
	v_mov_b32_e32 v104, v172
	v_mov_b32_e32 v105, v172
	v_pk_mul_f32 v[106:107], v[172:173], v[106:107]
	v_pk_mul_f32 v[90:91], v[90:91], v[102:103]
	v_pk_mul_f32 v[88:89], v[172:173], v[88:89]
	v_cvt_pk_bf16_f32 v92, v106, v107
	v_pk_mul_f32 v[108:109], v[104:105], v[108:109]
	v_pk_fma_f32 v[90:91], v[94:95], v[98:99], v[90:91]
	v_cvt_pk_bf16_f32 v93, v108, v109
	v_cvt_pk_bf16_f32 v94, v88, v89
	ds_bpermute_b32 v88, v179, v92
	v_ashrrev_i32_e32 v92, 9, v110
	v_and_b32_e32 v92, -8, v92
	v_add_u32_e32 v106, s29, v92
	v_pk_mul_f32 v[90:91], v[104:105], v[90:91]
	v_or_b32_e32 v92, s28, v106
	v_cvt_pk_bf16_f32 v91, v90, v91
	ds_bpermute_b32 v89, v179, v93
	ds_bpermute_b32 v90, v179, v94
	v_ashrrev_i32_e32 v93, 31, v92
	v_and_b32_e32 v94, 0xfff, v110
	v_lshlrev_b32_e32 v95, s19, v110
	ds_bpermute_b32 v91, v179, v91
	v_lshlrev_b64 v[92:93], 19, v[92:93]
	v_and_b32_e32 v95, 0xfff, v95
	v_lshrrev_b32_e32 v94, s17, v94
	v_lshl_add_u64 v[92:93], s[6:7], 0, v[92:93]
	v_add_lshl_u32 v94, v95, v94, 7
	v_mov_b32_e32 v95, v159
	v_lshl_add_u64 v[92:93], v[92:93], 0, v[94:95]
	v_lshl_add_u64 v[92:93], v[92:93], 0, s[2:3]
	v_lshl_add_u64 v[92:93], v[92:93], 0, v[158:159]
	s_waitcnt lgkmcnt(0)
; __host__ __device__ __forceinline__ size_t qkv_block(int typ, int g, int b, int h) { return (size_t)((((typ * 3 + g) * 16 + b) * 8 + h)) * (4096 * 64); }
; __host__ __device__ __forceinline__ int qkv_row(int pos, int g) { const int dsh = 2 * g; return ((pos & ((1 << dsh) - 1)) << (12 - dsh)) + (pos >> dsh); }
; __device__ __forceinline__ u32x4 pack8(const f32x4 v0, const f32x4 v1) { u32x4 w; w.x = cvt_pk_bf16(v0[0], v0[1]); w.y = cvt_pk_bf16(v0[2], v0[3]); w.z = cvt_pk_bf16(v1[0], v1[1]); w.w = cvt_pk_bf16(v1[2], v1[3]); return w; }
;     __device__ __forceinline__ void operator()(const f32x4 (&acc)[2][2][4][2], const Unit& u, int wr, int wc, int fr, int fq) const {
;     ...
;             for (int mm = 0; mm < 2; ++mm) { const int pos = (row0 + ai * HALF + (2 * mp + mm) * 16) & (SEQ - 1);
;                 csv[mm] = *(const f32x4*)(rope + pos * 8 + 4 * (fq & 1)); snv[mm] = *(const f32x4*)(rope + 4096 * 8 + pos * 8 + 4 * (fq & 1)); }
; #pragma unroll
;             for (int mm = 0; mm < 2; ++mm) {
;                 const int m = 2 * mp + mm, row = row0 + ai * HALF + m * 16;
;                 f32x4 cs = {1.f, 1.f, 1.f, 1.f}, sn = {0.f, 0.f, 0.f, 0.f};
;                 if (rl) { cs = csv[mm]; sn = snv[mm]; }
; #pragma unroll
;                 for (int bj = 0; bj < 2; ++bj) {
;                     const f32x4 x1 = acc[ai][bj][m][0], x2 = acc[ai][bj][m][1];
;                     const f32x4 r1 = (x1 * cs - x2 * sn) * sc, r2 = (x2 * cs + x1 * sn) * sc;
;                     { const int tok = row_off + row - fr + tr_, hh = 4 * (u.pn & 1) + 2 * bj + (wc >> 1);
;                       *(u32x4*)(O + qkv_block(typ, gq_, tok >> 12, hh) + (size_t)qkv_row(tok & (SEQ - 1), gq_) * 64 + 32 * (wc & 1) + 8 * tq_) = xpose4x16(pack8(r1, r2), sa_); }
;                 }
;             }
;             asm volatile("" ::: "memory");
	global_store_dwordx4 v[92:93], v[88:91], off
	s_nop 1
	v_pk_mul_f32 v[90:91], v[80:81], v[96:97]
	v_pk_mul_f32 v[80:81], v[80:81], v[100:101]
	v_pk_mul_f32 v[88:89], v[82:83], v[98:99]
	v_pk_fma_f32 v[90:91], v[84:85], v[100:101], v[90:91] neg_lo:[0,0,1] neg_hi:[0,0,1]
	v_pk_mul_f32 v[82:83], v[82:83], v[102:103]
	v_pk_fma_f32 v[80:81], v[84:85], v[96:97], v[80:81]
	v_pk_fma_f32 v[88:89], v[86:87], v[102:103], v[88:89] neg_lo:[0,0,1] neg_hi:[0,0,1]
	v_pk_mul_f32 v[90:91], v[172:173], v[90:91]
	v_pk_fma_f32 v[82:83], v[86:87], v[98:99], v[82:83]
	v_pk_mul_f32 v[80:81], v[172:173], v[80:81]
	v_cvt_pk_bf16_f32 v84, v90, v91
	v_pk_mul_f32 v[88:89], v[104:105], v[88:89]
	v_pk_mul_f32 v[82:83], v[104:105], v[82:83]
	v_cvt_pk_bf16_f32 v85, v88, v89
	v_cvt_pk_bf16_f32 v86, v80, v81
	ds_bpermute_b32 v80, v179, v84
	v_or_b32_e32 v84, s30, v106
	v_cvt_pk_bf16_f32 v83, v82, v83
	ds_bpermute_b32 v81, v179, v85
	v_ashrrev_i32_e32 v85, 31, v84
	ds_bpermute_b32 v82, v179, v86
	ds_bpermute_b32 v83, v179, v83
	v_lshlrev_b64 v[84:85], 19, v[84:85]
	v_lshl_add_u64 v[84:85], s[6:7], 0, v[84:85]
	v_lshl_add_u64 v[84:85], v[84:85], 0, v[94:95]
	v_lshl_add_u64 v[84:85], v[84:85], 0, s[2:3]
	v_lshl_add_u64 v[84:85], v[84:85], 0, v[158:159]
	s_waitcnt lgkmcnt(0)
	global_store_dwordx4 v[84:85], v[80:83], off
	v_add_u32_e32 v84, 48, v184
	v_mov_b32_e32 v85, 1.0
	v_pk_mul_f32 v[82:83], v[72:73], v[128:129]
	v_pk_mul_f32 v[80:81], v[74:75], v[130:131]
	v_pk_fma_f32 v[82:83], v[76:77], v[132:133], v[82:83] neg_lo:[0,0,1] neg_hi:[0,0,1]
	v_pk_mul_f32 v[76:77], v[76:77], v[128:129]
	v_pk_fma_f32 v[80:81], v[78:79], v[134:135], v[80:81] neg_lo:[0,0,1] neg_hi:[0,0,1]
	v_pk_fma_f32 v[72:73], v[72:73], v[132:133], v[76:77]
	v_pk_mul_f32 v[82:83], v[172:173], v[82:83]
	v_pk_mul_f32 v[78:79], v[78:79], v[130:131]
	v_pk_mul_f32 v[72:73], v[172:173], v[72:73]
	v_cvt_pk_bf16_f32 v76, v82, v83
	v_pk_mul_f32 v[80:81], v[104:105], v[80:81]
	v_pk_fma_f32 v[74:75], v[74:75], v[134:135], v[78:79]
	v_cvt_pk_bf16_f32 v77, v80, v81
	v_cvt_pk_bf16_f32 v78, v72, v73
	ds_bpermute_b32 v72, v179, v76
	v_ashrrev_i32_e32 v76, 9, v84
	v_and_b32_e32 v76, -8, v76
	v_add_u32_e32 v80, s29, v76
	v_pk_mul_f32 v[74:75], v[104:105], v[74:75]
	v_or_b32_e32 v76, s28, v80
	v_cvt_pk_bf16_f32 v75, v74, v75
	ds_bpermute_b32 v73, v179, v77
	ds_bpermute_b32 v74, v179, v78
	v_ashrrev_i32_e32 v77, 31, v76
	v_and_b32_e32 v78, 0xfff, v84
	v_lshlrev_b32_e32 v79, s19, v84
	ds_bpermute_b32 v75, v179, v75
	v_lshlrev_b64 v[76:77], 19, v[76:77]
	v_and_b32_e32 v79, 0xfff, v79
	v_lshrrev_b32_e32 v78, s17, v78
	v_lshl_add_u64 v[76:77], s[6:7], 0, v[76:77]
	v_add_lshl_u32 v78, v79, v78, 7
	v_mov_b32_e32 v79, v159
	v_lshl_add_u64 v[76:77], v[76:77], 0, v[78:79]
	v_lshl_add_u64 v[76:77], v[76:77], 0, s[2:3]
	v_lshl_add_u64 v[76:77], v[76:77], 0, v[158:159]
	s_waitcnt lgkmcnt(0)
	global_store_dwordx4 v[76:77], v[72:75], off
	v_mov_b32_e32 v76, 0
	v_mov_b32_e32 v77, 0
	v_pk_mul_f32 v[74:75], v[64:65], v[128:129]
	v_pk_mul_f32 v[72:73], v[66:67], v[130:131]
	v_pk_fma_f32 v[74:75], v[68:69], v[132:133], v[74:75] neg_lo:[0,0,1] neg_hi:[0,0,1]
	v_pk_mul_f32 v[68:69], v[68:69], v[128:129]
	v_pk_fma_f32 v[72:73], v[70:71], v[134:135], v[72:73] neg_lo:[0,0,1] neg_hi:[0,0,1]
	v_pk_mul_f32 v[70:71], v[70:71], v[130:131]
	v_pk_fma_f32 v[64:65], v[64:65], v[132:133], v[68:69]
	v_pk_mul_f32 v[74:75], v[172:173], v[74:75]
	v_pk_fma_f32 v[66:67], v[66:67], v[134:135], v[70:71]
	v_pk_mul_f32 v[64:65], v[172:173], v[64:65]
	v_cvt_pk_bf16_f32 v68, v74, v75
	v_pk_mul_f32 v[72:73], v[104:105], v[72:73]
	v_pk_mul_f32 v[66:67], v[104:105], v[66:67]
	v_cvt_pk_bf16_f32 v69, v72, v73
	v_cvt_pk_bf16_f32 v70, v64, v65
	ds_bpermute_b32 v64, v179, v68
	v_or_b32_e32 v68, s30, v80
	v_cvt_pk_bf16_f32 v67, v66, v67
	ds_bpermute_b32 v65, v179, v69
	v_ashrrev_i32_e32 v69, 31, v68
	ds_bpermute_b32 v66, v179, v70
	ds_bpermute_b32 v67, v179, v67
	v_lshlrev_b64 v[68:69], 19, v[68:69]
	v_lshl_add_u64 v[68:69], s[6:7], 0, v[68:69]
	v_lshl_add_u64 v[68:69], v[68:69], 0, v[78:79]
	v_lshl_add_u64 v[68:69], v[68:69], 0, s[2:3]
	v_lshl_add_u64 v[68:69], v[68:69], 0, v[158:159]
	s_waitcnt lgkmcnt(0)
	global_store_dwordx4 v[68:69], v[64:67], off
	v_mov_b32_e32 v68, 1.0
	v_mov_b32_e32 v70, 1.0
	v_add_u32_e32 v64, 0x400, v185
	v_and_b32_e32 v65, 0x7e78, v64
	v_mov_b32_e32 v64, 0
	v_lshlrev_b32_e32 v86, 2, v65
	v_mov_b32_e32 v71, 1.0
	v_mov_b32_e32 v72, 1.0
	v_mov_b32_e32 v73, 1.0
	v_mov_b32_e32 v74, 0
	v_mov_b32_e32 v75, 0
	v_mov_b32_e32 v78, 0
	v_mov_b32_e32 v79, 0
	v_mov_b32_e32 v80, 0
	v_mov_b32_e32 v81, 0
	v_mov_b32_e32 v82, 1.0
	v_mov_b32_e32 v83, 1.0
	v_mov_b32_e32 v84, 1.0
	s_and_saveexec_b64 s[26:27], s[24:25]
	s_cbranch_execz .LBB0_1831
	v_mov_b32_e32 v87, v159
	v_lshl_add_u64 v[70:71], v[162:163], 0, v[86:87]
	v_lshl_add_u64 v[66:67], v[160:161], 0, v[86:87]
	global_load_dwordx4 v[74:77], v[70:71], off offset:512
	global_load_dwordx4 v[78:81], v[70:71], off
	s_nop 0
	global_load_dwordx4 v[70:73], v[66:67], off offset:512
	global_load_dwordx4 v[82:85], v[66:67], off
; __host__ __device__ __forceinline__ size_t qkv_block(int typ, int g, int b, int h) { return (size_t)((((typ * 3 + g) * 16 + b) * 8 + h)) * (4096 * 64); }
; __host__ __device__ __forceinline__ int qkv_row(int pos, int g) { const int dsh = 2 * g; return ((pos & ((1 << dsh) - 1)) << (12 - dsh)) + (pos >> dsh); }
; __device__ __forceinline__ u32x4 pack8(const f32x4 v0, const f32x4 v1) { u32x4 w; w.x = cvt_pk_bf16(v0[0], v0[1]); w.y = cvt_pk_bf16(v0[2], v0[3]); w.z = cvt_pk_bf16(v1[0], v1[1]); w.w = cvt_pk_bf16(v1[2], v1[3]); return w; }
;     __device__ __forceinline__ void operator()(const f32x4 (&acc)[2][2][4][2], const Unit& u, int wr, int wc, int fr, int fq) const {
;     ...
;             for (int mm = 0; mm < 2; ++mm) { const int pos = (row0 + ai * HALF + (2 * mp + mm) * 16) & (SEQ - 1);
;                 csv[mm] = *(const f32x4*)(rope + pos * 8 + 4 * (fq & 1)); snv[mm] = *(const f32x4*)(rope + 4096 * 8 + pos * 8 + 4 * (fq & 1)); }
; #pragma unroll
;             for (int mm = 0; mm < 2; ++mm) {
;                 const int m = 2 * mp + mm, row = row0 + ai * HALF + m * 16;
;                 f32x4 cs = {1.f, 1.f, 1.f, 1.f}, sn = {0.f, 0.f, 0.f, 0.f};
;                 if (rl) { cs = csv[mm]; sn = snv[mm]; }
; #pragma unroll
;                 for (int bj = 0; bj < 2; ++bj) {
;                     const f32x4 x1 = acc[ai][bj][m][0], x2 = acc[ai][bj][m][1];
;                     const f32x4 r1 = (x1 * cs - x2 * sn) * sc, r2 = (x2 * cs + x1 * sn) * sc;
;                     { const int tok = row_off + row - fr + tr_, hh = 4 * (u.pn & 1) + 2 * bj + (wc >> 1);
;                       *(u32x4*)(O + qkv_block(typ, gq_, tok >> 12, hh) + (size_t)qkv_row(tok & (SEQ - 1), gq_) * 64 + 32 * (wc & 1) + 8 * tq_) = xpose4x16(pack8(r1, r2), sa_); }
;                 }
;             }
;             asm volatile("" ::: "memory");
.LBB0_1831:
	s_or_b64 exec, exec, s[26:27]
	s_waitcnt vmcnt(2)
	v_pk_mul_f32 v[88:89], v[56:57], v[78:79]
	s_waitcnt vmcnt(0)
	v_pk_mul_f32 v[56:57], v[56:57], v[82:83]
	v_pk_mul_f32 v[66:67], v[58:59], v[80:81]
	v_pk_fma_f32 v[88:89], v[60:61], v[82:83], v[88:89] neg_lo:[0,0,1] neg_hi:[0,0,1]
	v_pk_fma_f32 v[56:57], v[60:61], v[78:79], v[56:57]
	v_add_u32_e32 v65, 0x80, v184
	v_pk_fma_f32 v[66:67], v[62:63], v[84:85], v[66:67] neg_lo:[0,0,1] neg_hi:[0,0,1]
	v_pk_mul_f32 v[88:89], v[172:173], v[88:89]
	v_pk_mul_f32 v[58:59], v[58:59], v[84:85]
	v_pk_mul_f32 v[56:57], v[172:173], v[56:57]
	v_cvt_pk_bf16_f32 v60, v88, v89
	v_pk_mul_f32 v[66:67], v[104:105], v[66:67]
	v_pk_fma_f32 v[58:59], v[62:63], v[80:81], v[58:59]
	v_cvt_pk_bf16_f32 v61, v66, v67
	v_cvt_pk_bf16_f32 v62, v56, v57
	ds_bpermute_b32 v56, v179, v60
	v_ashrrev_i32_e32 v60, 9, v65
	v_and_b32_e32 v60, -8, v60
	v_add_u32_e32 v66, s29, v60
	v_pk_mul_f32 v[58:59], v[104:105], v[58:59]
	v_or_b32_e32 v60, s28, v66
	v_cvt_pk_bf16_f32 v59, v58, v59
	ds_bpermute_b32 v57, v179, v61
	ds_bpermute_b32 v58, v179, v62
	v_ashrrev_i32_e32 v61, 31, v60
	v_and_b32_e32 v62, 0xfff, v65
	v_lshlrev_b32_e32 v63, s19, v65
	ds_bpermute_b32 v59, v179, v59
	v_lshlrev_b64 v[60:61], 19, v[60:61]
	v_and_b32_e32 v63, 0xfff, v63
	v_lshrrev_b32_e32 v62, s17, v62
	v_lshl_add_u64 v[60:61], s[6:7], 0, v[60:61]
	v_add_lshl_u32 v62, v63, v62, 7
	v_mov_b32_e32 v63, v159
	v_lshl_add_u64 v[60:61], v[60:61], 0, v[62:63]
	v_lshl_add_u64 v[60:61], v[60:61], 0, s[2:3]
	v_lshl_add_u64 v[60:61], v[60:61], 0, v[158:159]
	s_waitcnt lgkmcnt(0)
	global_store_dwordx4 v[60:61], v[56:59], off
	v_mov_b32_e32 v69, 1.0
	v_mov_b32_e32 v65, 0
	v_pk_mul_f32 v[58:59], v[48:49], v[78:79]
	v_pk_mul_f32 v[48:49], v[48:49], v[82:83]
	v_pk_mul_f32 v[56:57], v[50:51], v[80:81]
	v_pk_fma_f32 v[58:59], v[52:53], v[82:83], v[58:59] neg_lo:[0,0,1] neg_hi:[0,0,1]
	v_pk_mul_f32 v[50:51], v[50:51], v[84:85]
	v_pk_fma_f32 v[48:49], v[52:53], v[78:79], v[48:49]
	v_pk_fma_f32 v[56:57], v[54:55], v[84:85], v[56:57] neg_lo:[0,0,1] neg_hi:[0,0,1]
	v_pk_mul_f32 v[58:59], v[172:173], v[58:59]
	v_pk_fma_f32 v[50:51], v[54:55], v[80:81], v[50:51]
	v_pk_mul_f32 v[48:49], v[172:173], v[48:49]
	v_cvt_pk_bf16_f32 v52, v58, v59
	v_pk_mul_f32 v[56:57], v[104:105], v[56:57]
	v_pk_mul_f32 v[50:51], v[104:105], v[50:51]
	v_cvt_pk_bf16_f32 v53, v56, v57
	v_cvt_pk_bf16_f32 v54, v48, v49
	ds_bpermute_b32 v48, v179, v52
	v_or_b32_e32 v52, s30, v66
	v_cvt_pk_bf16_f32 v51, v50, v51
	ds_bpermute_b32 v49, v179, v53
	v_ashrrev_i32_e32 v53, 31, v52
	ds_bpermute_b32 v50, v179, v54
	ds_bpermute_b32 v51, v179, v51
	v_lshlrev_b64 v[52:53], 19, v[52:53]
	v_lshl_add_u64 v[52:53], s[6:7], 0, v[52:53]
	v_lshl_add_u64 v[52:53], v[52:53], 0, v[62:63]
	v_lshl_add_u64 v[52:53], v[52:53], 0, s[2:3]
	v_lshl_add_u64 v[52:53], v[52:53], 0, v[158:159]
	s_waitcnt lgkmcnt(0)
	global_store_dwordx4 v[52:53], v[48:51], off
	v_add_u32_e32 v52, 0x90, v184
	v_mov_b32_e32 v66, 0
	v_pk_mul_f32 v[50:51], v[40:41], v[74:75]
	v_pk_mul_f32 v[48:49], v[42:43], v[76:77]
	v_pk_fma_f32 v[50:51], v[44:45], v[70:71], v[50:51] neg_lo:[0,0,1] neg_hi:[0,0,1]
	v_pk_mul_f32 v[44:45], v[44:45], v[74:75]
	v_pk_fma_f32 v[48:49], v[46:47], v[72:73], v[48:49] neg_lo:[0,0,1] neg_hi:[0,0,1]
	v_pk_fma_f32 v[40:41], v[40:41], v[70:71], v[44:45]
	v_pk_mul_f32 v[50:51], v[172:173], v[50:51]
	v_pk_mul_f32 v[46:47], v[46:47], v[76:77]
	v_pk_mul_f32 v[40:41], v[172:173], v[40:41]
	v_cvt_pk_bf16_f32 v44, v50, v51
	v_pk_mul_f32 v[48:49], v[104:105], v[48:49]
	v_pk_fma_f32 v[42:43], v[42:43], v[72:73], v[46:47]
	v_cvt_pk_bf16_f32 v45, v48, v49
	v_cvt_pk_bf16_f32 v46, v40, v41
	ds_bpermute_b32 v40, v179, v44
	v_ashrrev_i32_e32 v44, 9, v52
	v_and_b32_e32 v44, -8, v44
	v_add_u32_e32 v48, s29, v44
	v_pk_mul_f32 v[42:43], v[104:105], v[42:43]
	v_or_b32_e32 v44, s28, v48
	v_cvt_pk_bf16_f32 v43, v42, v43
	ds_bpermute_b32 v41, v179, v45
	ds_bpermute_b32 v42, v179, v46
	v_ashrrev_i32_e32 v45, 31, v44
	v_and_b32_e32 v46, 0xfff, v52
	v_lshlrev_b32_e32 v47, s19, v52
	ds_bpermute_b32 v43, v179, v43
	v_lshlrev_b64 v[44:45], 19, v[44:45]
	v_and_b32_e32 v47, 0xfff, v47
	v_lshrrev_b32_e32 v46, s17, v46
	v_lshl_add_u64 v[44:45], s[6:7], 0, v[44:45]
	v_add_lshl_u32 v46, v47, v46, 7
	v_mov_b32_e32 v47, v159
	v_lshl_add_u64 v[44:45], v[44:45], 0, v[46:47]
	v_lshl_add_u64 v[44:45], v[44:45], 0, s[2:3]
	v_lshl_add_u64 v[44:45], v[44:45], 0, v[158:159]
	s_waitcnt lgkmcnt(0)
	global_store_dwordx4 v[44:45], v[40:43], off
	v_mov_b32_e32 v67, 0
	s_nop 0
	v_pk_mul_f32 v[42:43], v[32:33], v[74:75]
	v_pk_mul_f32 v[40:41], v[34:35], v[76:77]
	v_pk_fma_f32 v[42:43], v[36:37], v[70:71], v[42:43] neg_lo:[0,0,1] neg_hi:[0,0,1]
	v_pk_mul_f32 v[36:37], v[36:37], v[74:75]
	v_pk_fma_f32 v[40:41], v[38:39], v[72:73], v[40:41] neg_lo:[0,0,1] neg_hi:[0,0,1]
	v_pk_mul_f32 v[38:39], v[38:39], v[76:77]
	v_pk_fma_f32 v[32:33], v[32:33], v[70:71], v[36:37]
	v_pk_mul_f32 v[42:43], v[172:173], v[42:43]
	v_pk_fma_f32 v[34:35], v[34:35], v[72:73], v[38:39]
	v_pk_mul_f32 v[32:33], v[172:173], v[32:33]
	v_cvt_pk_bf16_f32 v36, v42, v43
	v_pk_mul_f32 v[40:41], v[104:105], v[40:41]
	v_pk_mul_f32 v[34:35], v[104:105], v[34:35]
	v_cvt_pk_bf16_f32 v37, v40, v41
	v_cvt_pk_bf16_f32 v38, v32, v33
	ds_bpermute_b32 v32, v179, v36
	v_or_b32_e32 v36, s30, v48
	v_cvt_pk_bf16_f32 v35, v34, v35
	ds_bpermute_b32 v33, v179, v37
	v_ashrrev_i32_e32 v37, 31, v36
	ds_bpermute_b32 v34, v179, v38
	ds_bpermute_b32 v35, v179, v35
	v_lshlrev_b64 v[36:37], 19, v[36:37]
	v_lshl_add_u64 v[36:37], s[6:7], 0, v[36:37]
	v_lshl_add_u64 v[36:37], v[36:37], 0, v[46:47]
	v_lshl_add_u64 v[36:37], v[36:37], 0, s[2:3]
	v_lshl_add_u64 v[36:37], v[36:37], 0, v[158:159]
	s_waitcnt lgkmcnt(0)
	global_store_dwordx4 v[36:37], v[32:35], off
	v_mov_b32_e32 v70, 1.0
	v_mov_b32_e32 v71, 1.0
	v_mov_b32_e32 v32, 0
	v_mov_b32_e32 v33, 0
	v_mov_b32_e32 v34, 0
	v_mov_b32_e32 v35, 0
	v_mov_b32_e32 v36, 1.0
	v_mov_b32_e32 v37, 1.0
	v_mov_b32_e32 v38, 1.0
	v_mov_b32_e32 v39, 1.0
	s_and_saveexec_b64 s[26:27], s[24:25]
	s_cbranch_execz .LBB0_1833
	v_mov_b32_e32 v87, v159
	v_lshl_add_u64 v[36:37], v[160:161], 0, v[86:87]
	v_lshl_add_u64 v[32:33], v[162:163], 0, v[86:87]
	global_load_dwordx4 v[64:67], v[32:33], off offset:1536
	s_nop 0
	global_load_dwordx4 v[32:35], v[32:33], off offset:1024
	s_nop 0
	global_load_dwordx4 v[68:71], v[36:37], off offset:1536
	s_nop 0
	global_load_dwordx4 v[36:39], v[36:37], off offset:1024
; __host__ __device__ __forceinline__ size_t qkv_block(int typ, int g, int b, int h) { return (size_t)((((typ * 3 + g) * 16 + b) * 8 + h)) * (4096 * 64); }
; __host__ __device__ __forceinline__ int qkv_row(int pos, int g) { const int dsh = 2 * g; return ((pos & ((1 << dsh) - 1)) << (12 - dsh)) + (pos >> dsh); }
; #define PG8_BAR __builtin_amdgcn_s_barrier()
; template <class Epi, class Sched, class AM, bool ALIGN_EPI = false, bool SP2 = false>
; __device__ __forceinline__ void gemm_phase(PG8_LAS unsigned char* lds, const Gemm g, const Sched& S, const Epi& E, const AM& am, const int wid_in) {
;     ...
;         if (!has_next) break;
; #pragma unroll
;         for (int a = 0; a < 2; ++a)
; #pragma unroll
;             for (int b = 0; b < 2; ++b)
; #pragma unroll
;                 for (int m = 0; m < 4; ++m)
; #pragma unroll
;                     for (int n = 0; n < 2; ++n) acc[a][b][m][n] = (f32x4){0.f, 0.f, 0.f, 0.f};
;         cur = nxt; cA = nA; cB = nB; ++ui;
;         if constexpr (AM::GATHER) { _Pragma("unroll") for (int h = 0; h < 2; ++h) _Pragma("unroll") for (int i = 0; i < 2; ++i) gao[h][i] = gno[h][i]; }
;         if constexpr (ALIGN_EPI) { if (wr == 1) PG8_BAR; }
;     __device__ __forceinline__ void operator()(const f32x4 (&acc)[2][2][4][2], const Unit& u, int wr, int wc, int fr, int fq) const {
;     ...
;             for (int mm = 0; mm < 2; ++mm) {
;                 const int m = 2 * mp + mm, row = row0 + ai * HALF + m * 16;
;                 f32x4 cs = {1.f, 1.f, 1.f, 1.f}, sn = {0.f, 0.f, 0.f, 0.f};
;                 if (rl) { cs = csv[mm]; sn = snv[mm]; }
; #pragma unroll
;                 for (int bj = 0; bj < 2; ++bj) {
;                     const f32x4 x1 = acc[ai][bj][m][0], x2 = acc[ai][bj][m][1];
;                     const f32x4 r1 = (x1 * cs - x2 * sn) * sc, r2 = (x2 * cs + x1 * sn) * sc;
;                     { const int tok = row_off + row - fr + tr_, hh = 4 * (u.pn & 1) + 2 * bj + (wc >> 1);
;                       *(u32x4*)(O + qkv_block(typ, gq_, tok >> 12, hh) + (size_t)qkv_row(tok & (SEQ - 1), gq_) * 64 + 32 * (wc & 1) + 8 * tq_) = xpose4x16(pack8(r1, r2), sa_); }
;                 }
;             }
;             asm volatile("" ::: "memory");
.LBB0_1833:
	s_or_b64 exec, exec, s[26:27]
	s_waitcnt vmcnt(2)
	v_pk_mul_f32 v[42:43], v[24:25], v[32:33]
	s_waitcnt vmcnt(0)
	v_pk_mul_f32 v[24:25], v[24:25], v[36:37]
	v_pk_mul_f32 v[40:41], v[26:27], v[34:35]
	v_pk_fma_f32 v[42:43], v[28:29], v[36:37], v[42:43] neg_lo:[0,0,1] neg_hi:[0,0,1]
	v_pk_fma_f32 v[24:25], v[28:29], v[32:33], v[24:25]
	v_add_u32_e32 v46, 0xa0, v184
	v_pk_fma_f32 v[40:41], v[30:31], v[38:39], v[40:41] neg_lo:[0,0,1] neg_hi:[0,0,1]
	v_mov_b32_e32 v44, v172
	v_mov_b32_e32 v45, v172
	v_pk_mul_f32 v[42:43], v[172:173], v[42:43]
	v_pk_mul_f32 v[26:27], v[26:27], v[38:39]
	v_pk_mul_f32 v[24:25], v[172:173], v[24:25]
	v_cvt_pk_bf16_f32 v28, v42, v43
	v_pk_mul_f32 v[40:41], v[44:45], v[40:41]
	v_pk_fma_f32 v[26:27], v[30:31], v[34:35], v[26:27]
	v_cvt_pk_bf16_f32 v29, v40, v41
	v_cvt_pk_bf16_f32 v30, v24, v25
	ds_bpermute_b32 v24, v179, v28
	v_ashrrev_i32_e32 v28, 9, v46
	v_and_b32_e32 v28, -8, v28
	v_add_u32_e32 v40, s29, v28
	v_pk_mul_f32 v[26:27], v[44:45], v[26:27]
	v_or_b32_e32 v28, s28, v40
	v_cvt_pk_bf16_f32 v27, v26, v27
	ds_bpermute_b32 v25, v179, v29
	ds_bpermute_b32 v26, v179, v30
	v_ashrrev_i32_e32 v29, 31, v28
	v_and_b32_e32 v30, 0xfff, v46
	v_lshlrev_b32_e32 v31, s19, v46
	ds_bpermute_b32 v27, v179, v27
	v_lshlrev_b64 v[28:29], 19, v[28:29]
	v_and_b32_e32 v31, 0xfff, v31
	v_lshrrev_b32_e32 v30, s17, v30
	v_lshl_add_u64 v[28:29], s[6:7], 0, v[28:29]
	v_add_lshl_u32 v30, v31, v30, 7
	v_mov_b32_e32 v31, v159
	v_lshl_add_u64 v[28:29], v[28:29], 0, v[30:31]
	v_lshl_add_u64 v[28:29], v[28:29], 0, s[2:3]
	v_lshl_add_u64 v[28:29], v[28:29], 0, v[158:159]
	s_waitcnt lgkmcnt(0)
	global_store_dwordx4 v[28:29], v[24:27], off
	s_andn2_b64 vcc, exec, s[0:1]
	s_mov_b64 s[0:1], -1
	v_pk_mul_f32 v[26:27], v[16:17], v[32:33]
	v_pk_mul_f32 v[16:17], v[16:17], v[36:37]
	v_pk_mul_f32 v[24:25], v[18:19], v[34:35]
	v_pk_fma_f32 v[26:27], v[20:21], v[36:37], v[26:27] neg_lo:[0,0,1] neg_hi:[0,0,1]
	v_pk_mul_f32 v[18:19], v[18:19], v[38:39]
	v_pk_fma_f32 v[16:17], v[20:21], v[32:33], v[16:17]
	v_pk_fma_f32 v[24:25], v[22:23], v[38:39], v[24:25] neg_lo:[0,0,1] neg_hi:[0,0,1]
	v_pk_mul_f32 v[26:27], v[172:173], v[26:27]
	v_pk_fma_f32 v[18:19], v[22:23], v[34:35], v[18:19]
	v_pk_mul_f32 v[16:17], v[172:173], v[16:17]
	v_cvt_pk_bf16_f32 v20, v26, v27
	v_pk_mul_f32 v[24:25], v[44:45], v[24:25]
	v_pk_mul_f32 v[18:19], v[44:45], v[18:19]
	v_cvt_pk_bf16_f32 v21, v24, v25
	v_cvt_pk_bf16_f32 v22, v16, v17
	ds_bpermute_b32 v16, v179, v20
	v_or_b32_e32 v20, s30, v40
	v_cvt_pk_bf16_f32 v19, v18, v19
	ds_bpermute_b32 v17, v179, v21
	v_ashrrev_i32_e32 v21, 31, v20
	ds_bpermute_b32 v18, v179, v22
	ds_bpermute_b32 v19, v179, v19
	v_lshlrev_b64 v[20:21], 19, v[20:21]
	v_lshl_add_u64 v[20:21], s[6:7], 0, v[20:21]
	v_lshl_add_u64 v[20:21], v[20:21], 0, v[30:31]
	v_lshl_add_u64 v[20:21], v[20:21], 0, s[2:3]
	v_lshl_add_u64 v[20:21], v[20:21], 0, v[158:159]
	s_waitcnt lgkmcnt(0)
	global_store_dwordx4 v[20:21], v[16:19], off
	v_add_u32_e32 v20, 0xb0, v184
	s_nop 0
	v_pk_mul_f32 v[18:19], v[8:9], v[64:65]
	v_pk_mul_f32 v[16:17], v[10:11], v[66:67]
	v_pk_fma_f32 v[18:19], v[12:13], v[68:69], v[18:19] neg_lo:[0,0,1] neg_hi:[0,0,1]
	v_pk_mul_f32 v[12:13], v[12:13], v[64:65]
	v_pk_fma_f32 v[16:17], v[14:15], v[70:71], v[16:17] neg_lo:[0,0,1] neg_hi:[0,0,1]
	v_pk_fma_f32 v[8:9], v[8:9], v[68:69], v[12:13]
	v_pk_mul_f32 v[18:19], v[172:173], v[18:19]
	v_pk_mul_f32 v[14:15], v[14:15], v[66:67]
	v_pk_mul_f32 v[8:9], v[172:173], v[8:9]
	v_cvt_pk_bf16_f32 v12, v18, v19
	v_pk_mul_f32 v[16:17], v[44:45], v[16:17]
	v_pk_fma_f32 v[10:11], v[10:11], v[70:71], v[14:15]
	v_cvt_pk_bf16_f32 v13, v16, v17
	v_cvt_pk_bf16_f32 v14, v8, v9
	ds_bpermute_b32 v8, v179, v12
	v_ashrrev_i32_e32 v12, 9, v20
	v_and_b32_e32 v12, -8, v12
	v_add_u32_e32 v16, s29, v12
	v_pk_mul_f32 v[10:11], v[44:45], v[10:11]
	v_or_b32_e32 v12, s28, v16
	v_cvt_pk_bf16_f32 v11, v10, v11
	ds_bpermute_b32 v9, v179, v13
	ds_bpermute_b32 v10, v179, v14
	v_ashrrev_i32_e32 v13, 31, v12
	v_and_b32_e32 v14, 0xfff, v20
	v_lshlrev_b32_e32 v15, s19, v20
	ds_bpermute_b32 v11, v179, v11
	v_lshlrev_b64 v[12:13], 19, v[12:13]
	v_and_b32_e32 v15, 0xfff, v15
	v_lshrrev_b32_e32 v14, s17, v14
	v_lshl_add_u64 v[12:13], s[6:7], 0, v[12:13]
	v_add_lshl_u32 v14, v15, v14, 7
	v_mov_b32_e32 v15, v159
	v_lshl_add_u64 v[12:13], v[12:13], 0, v[14:15]
	v_lshl_add_u64 v[12:13], v[12:13], 0, s[2:3]
	v_lshl_add_u64 v[12:13], v[12:13], 0, v[158:159]
	s_waitcnt lgkmcnt(0)
	global_store_dwordx4 v[12:13], v[8:11], off
	s_nop 1
	v_pk_mul_f32 v[10:11], v[0:1], v[64:65]
	v_pk_mul_f32 v[8:9], v[2:3], v[66:67]
	v_pk_fma_f32 v[10:11], v[4:5], v[68:69], v[10:11] neg_lo:[0,0,1] neg_hi:[0,0,1]
	v_pk_mul_f32 v[4:5], v[4:5], v[64:65]
	v_pk_fma_f32 v[8:9], v[6:7], v[70:71], v[8:9] neg_lo:[0,0,1] neg_hi:[0,0,1]
	v_pk_mul_f32 v[6:7], v[6:7], v[66:67]
	v_pk_fma_f32 v[0:1], v[0:1], v[68:69], v[4:5]
	v_pk_mul_f32 v[10:11], v[172:173], v[10:11]
	v_pk_fma_f32 v[2:3], v[2:3], v[70:71], v[6:7]
	v_pk_mul_f32 v[0:1], v[172:173], v[0:1]
	v_cvt_pk_bf16_f32 v4, v10, v11
	v_pk_mul_f32 v[8:9], v[44:45], v[8:9]
	v_pk_mul_f32 v[2:3], v[44:45], v[2:3]
	v_cvt_pk_bf16_f32 v5, v8, v9
	v_cvt_pk_bf16_f32 v6, v0, v1
	ds_bpermute_b32 v0, v179, v4
	v_or_b32_e32 v4, s30, v16
	v_cvt_pk_bf16_f32 v3, v2, v3
	ds_bpermute_b32 v1, v179, v5
	v_ashrrev_i32_e32 v5, 31, v4
	ds_bpermute_b32 v2, v179, v6
	ds_bpermute_b32 v3, v179, v3
	v_lshlrev_b64 v[4:5], 19, v[4:5]
	v_lshl_add_u64 v[4:5], s[6:7], 0, v[4:5]
	v_lshl_add_u64 v[4:5], v[4:5], 0, v[14:15]
	v_lshl_add_u64 v[4:5], v[4:5], 0, s[2:3]
	v_lshl_add_u64 v[4:5], v[4:5], 0, v[158:159]
	s_waitcnt lgkmcnt(0)
	global_store_dwordx4 v[4:5], v[0:3], off
	s_cbranch_vccnz .LBB0_1817
	s_andn2_b64 vcc, exec, s[4:5]
	s_cbranch_vccnz .LBB0_1816
	s_barrier
	s_branch .LBB0_1816

; #define PG8_LAS __attribute__((address_space(3)))
; #define PG8_STAGE(bufoff, gbase, voff) do { _Pragma("unroll") for (int _i = 0; _i < 2; ++_i) \
;         __builtin_amdgcn_global_load_lds((const unsigned*)((const char*)(gbase) + (voff)[_i]), (PG8_LAS unsigned*)(lds + (bufoff) + ldsw + _i * 8192), 16, 0, 0); } while (0)
; #define PG8_STAGE_A(b, h, gbase, NX) do { if constexpr (AM::GATHER) { const unsigned so_[2] = {(NX) ? gno[h][0] : gao[h][0], (NX) ? gno[h][1] : gao[h][1]}; PG8_STAGE(PG8_SA(b, h), gbase, so_); } \
;         else { PG8_STAGE(PG8_SA(b, h), (gbase) + (h) * hstep, voffA); } } while (0)
; #define PG8_WAIT_V(n) asm volatile("s_waitcnt vmcnt(" #n ")" ::: "memory")
; #define PG8_BAR __builtin_amdgcn_s_barrier()
; template <class Epi, class Sched, class AM, bool ALIGN_EPI = false, bool SP2 = false>
; __device__ __forceinline__ void gemm_phase(PG8_LAS unsigned char* lds, const Gemm g, const Sched& S, const Epi& E, const AM& am, const int wid_in) {
;     ...
;             const char* a1 = cA + (size_t)(t + 1) * kstep;
;             const char* a2 = last ? nA : cA + (size_t)(t + 2) * kstep; const char* b2 = last ? nB : cB + (size_t)(t + 2) * kstep;
;             const char* a3 = a2 + kstep; const char* b3 = b2 + kstep;
;             if (last && has_next) S.a_ready(nxt);
;             if (false) E.prefetch(cur, tid, (PG8_LAS unsigned*)(lds + 162816 + 512));
;             if constexpr (SP2) {
;             PG8_LDB(B0, 0, 0); PG8_LDB(B1, 0, 1); PG8_SCHED; PG8_LDA(At, 0, 0); PG8_STAGE_A(1, 1, a1, false);
;             PG8_WAIT_V(8); PG8_WAIT_L(0); PG8_BAR; PG8_MMA(0, 0, At, B0); PG8_MMA(0, 1, At, B1); PG8_BAR; PG8_SCHED;
;             PG8_LDA(At, 0, 1); PG8_STAGE(PG8_SB(0, 0), b2, voffB); PG8_STAGE(PG8_SB(0, 1), b2 + hstep, voffB); PG8_STAGE_A(0, 0, a2, last);
;             PG8_WAIT_V(8); PG8_WAIT_L(0); PG8_BAR; PG8_MMA(1, 0, At, B0); PG8_MMA(1, 1, At, B1); PG8_BAR; PG8_SCHED;
;             PG8_LDB(B0, 1, 0); PG8_LDB(B1, 1, 1); PG8_SCHED; PG8_LDA(At, 1, 0); PG8_STAGE_A(0, 1, a2, last);
;             PG8_WAIT_V(8); PG8_WAIT_L(0); PG8_BAR; PG8_MMA(0, 0, At, B0); PG8_MMA(0, 1, At, B1); PG8_BAR; PG8_SCHED;
;             PG8_LDA(At, 1, 1); PG8_STAGE(PG8_SB(1, 0), b3, voffB); PG8_STAGE(PG8_SB(1, 1), b3 + hstep, voffB); PG8_STAGE_A(1, 0, a3, last);
;             PG8_WAIT_V(8); PG8_WAIT_L(0); PG8_BAR; PG8_MMA(1, 0, At, B0); PG8_MMA(1, 1, At, B1); PG8_BAR; PG8_SCHED;
.LBB0_2129:
	ds_read_b128 v[128:131], v217
	ds_read_b128 v[132:135], v217 offset:1024
	ds_read_b128 v[136:139], v217 offset:2048
	ds_read_b128 v[140:143], v217 offset:3072
	ds_read_b128 v[144:147], v218
	ds_read_b128 v[148:151], v218 offset:1024
	ds_read_b128 v[152:155], v218 offset:2048
	ds_read_b128 v[156:159], v218 offset:3072
	s_add_u32 s30, s28, 0xfffe0080
	s_addc_u32 s31, s29, -1
	s_cmp_eq_u32 s61, 4
	s_cselect_b32 s35, s21, s31
	s_cselect_b32 s34, s57, s30
	s_cselect_b32 s31, s19, s60
	s_cselect_b32 s30, s58, s59
	s_add_i32 m0, s27, 0xc000
	ds_read_b128 v[160:163], v219
	ds_read_b128 v[164:167], v219 offset:1024
	ds_read_b128 v[168:171], v219 offset:2048
	ds_read_b128 v[172:175], v219 offset:3072
	ds_read_b128 v[176:179], v219 offset:4096
	ds_read_b128 v[180:183], v219 offset:5120
	ds_read_b128 v[184:187], v219 offset:6144
	ds_read_b128 v[208:211], v219 offset:7168
	global_load_lds_dwordx4 v198, s[28:29]
	s_add_i32 m0, s27, 0xe000
	s_nop 0
	global_load_lds_dwordx4 v200, s[28:29]
	s_waitcnt vmcnt(8)
	s_waitcnt lgkmcnt(0)
	s_barrier
	s_setprio 1
	s_waitcnt lgkmcnt(0)
	v_mfma_f32_16x16x32_bf16 v[124:127], v[128:131], v[160:163], v[124:127]
	v_mfma_f32_16x16x32_bf16 v[120:123], v[136:139], v[160:163], v[120:123]
	v_mfma_f32_16x16x32_bf16 v[108:111], v[128:131], v[168:171], v[108:111]
	v_mfma_f32_16x16x32_bf16 v[104:107], v[136:139], v[168:171], v[104:107]
	v_mfma_f32_16x16x32_bf16 v[92:95], v[128:131], v[176:179], v[92:95]
	v_mfma_f32_16x16x32_bf16 v[88:91], v[136:139], v[176:179], v[88:91]
	v_mfma_f32_16x16x32_bf16 v[76:79], v[128:131], v[184:187], v[76:79]
	v_mfma_f32_16x16x32_bf16 v[72:75], v[136:139], v[184:187], v[72:75]
	v_mfma_f32_16x16x32_bf16 v[124:127], v[132:135], v[164:167], v[124:127]
	v_mfma_f32_16x16x32_bf16 v[120:123], v[140:143], v[164:167], v[120:123]
	v_mfma_f32_16x16x32_bf16 v[108:111], v[132:135], v[172:175], v[108:111]
	v_mfma_f32_16x16x32_bf16 v[104:107], v[140:143], v[172:175], v[104:107]
	v_mfma_f32_16x16x32_bf16 v[92:95], v[132:135], v[180:183], v[92:95]
	v_mfma_f32_16x16x32_bf16 v[88:91], v[140:143], v[180:183], v[88:91]
	v_mfma_f32_16x16x32_bf16 v[76:79], v[132:135], v[208:211], v[76:79]
	v_mfma_f32_16x16x32_bf16 v[72:75], v[140:143], v[208:211], v[72:75]
	s_setprio 0
	s_setprio 1
	v_mfma_f32_16x16x32_bf16 v[116:119], v[144:147], v[160:163], v[116:119]
	v_mfma_f32_16x16x32_bf16 v[112:115], v[152:155], v[160:163], v[112:115]
	v_mfma_f32_16x16x32_bf16 v[100:103], v[144:147], v[168:171], v[100:103]
	v_mfma_f32_16x16x32_bf16 v[96:99], v[152:155], v[168:171], v[96:99]
	v_mfma_f32_16x16x32_bf16 v[84:87], v[144:147], v[176:179], v[84:87]
	v_mfma_f32_16x16x32_bf16 v[80:83], v[152:155], v[176:179], v[80:83]
	v_mfma_f32_16x16x32_bf16 v[68:71], v[144:147], v[184:187], v[68:71]
	v_mfma_f32_16x16x32_bf16 v[64:67], v[152:155], v[184:187], v[64:67]
	v_mfma_f32_16x16x32_bf16 v[116:119], v[148:151], v[164:167], v[116:119]
	v_mfma_f32_16x16x32_bf16 v[112:115], v[156:159], v[164:167], v[112:115]
	v_mfma_f32_16x16x32_bf16 v[100:103], v[148:151], v[172:175], v[100:103]
	v_mfma_f32_16x16x32_bf16 v[96:99], v[156:159], v[172:175], v[96:99]
	v_mfma_f32_16x16x32_bf16 v[84:87], v[148:151], v[180:183], v[84:87]
	v_mfma_f32_16x16x32_bf16 v[80:83], v[156:159], v[180:183], v[80:83]
	v_mfma_f32_16x16x32_bf16 v[68:71], v[148:151], v[208:211], v[68:71]
	v_mfma_f32_16x16x32_bf16 v[64:67], v[156:159], v[208:211], v[64:67]
	s_setprio 0
	s_barrier
	s_add_u32 s98, s30, s6
	s_addc_u32 s99, s31, s7
	s_add_u32 s100, s34, s6
	s_addc_u32 s101, s35, s7
	s_add_i32 s62, s50, s40
	s_mov_b32 m0, s62
	ds_read_b128 v[160:163], v219 offset:16384
	ds_read_b128 v[164:167], v219 offset:17408
	ds_read_b128 v[168:171], v219 offset:18432
	ds_read_b128 v[172:175], v219 offset:19456
	ds_read_b128 v[176:179], v219 offset:20480
	ds_read_b128 v[180:183], v219 offset:21504
	ds_read_b128 v[184:187], v219 offset:22528
	ds_read_b128 v[208:211], v219 offset:23552
	global_load_lds_dwordx4 v190, s[30:31]
	s_add_i32 m0, s62, 0x2000
	s_add_u32 s62, s30, 0x20000
	s_addc_u32 s63, s31, 0
	s_add_i32 s64, s51, s40
	global_load_lds_dwordx4 v194, s[30:31]
	s_mov_b32 m0, s64
	s_nop 0
	global_load_lds_dwordx4 v190, s[62:63]
	s_add_i32 m0, s64, 0x2000
	s_nop 0
	global_load_lds_dwordx4 v194, s[62:63]
	s_mov_b32 m0, s27
	s_nop 0
	global_load_lds_dwordx4 v188, s[34:35]
	s_mov_b32 m0, s41
	s_nop 0
	global_load_lds_dwordx4 v192, s[34:35]
	s_waitcnt vmcnt(8)
	s_waitcnt lgkmcnt(0)
	s_barrier
	s_setprio 1
	s_waitcnt lgkmcnt(0)
	v_mfma_f32_16x16x32_bf16 v[60:63], v[128:131], v[160:163], v[60:63]
	v_mfma_f32_16x16x32_bf16 v[56:59], v[136:139], v[160:163], v[56:59]
	v_mfma_f32_16x16x32_bf16 v[44:47], v[128:131], v[168:171], v[44:47]
	v_mfma_f32_16x16x32_bf16 v[40:43], v[136:139], v[168:171], v[40:43]
	v_mfma_f32_16x16x32_bf16 v[28:31], v[128:131], v[176:179], v[28:31]
	v_mfma_f32_16x16x32_bf16 v[24:27], v[136:139], v[176:179], v[24:27]
	v_mfma_f32_16x16x32_bf16 v[12:15], v[128:131], v[184:187], v[12:15]
	v_mfma_f32_16x16x32_bf16 v[8:11], v[136:139], v[184:187], v[8:11]
	v_mfma_f32_16x16x32_bf16 v[60:63], v[132:135], v[164:167], v[60:63]
	v_mfma_f32_16x16x32_bf16 v[56:59], v[140:143], v[164:167], v[56:59]
	v_mfma_f32_16x16x32_bf16 v[44:47], v[132:135], v[172:175], v[44:47]
	v_mfma_f32_16x16x32_bf16 v[40:43], v[140:143], v[172:175], v[40:43]
	v_mfma_f32_16x16x32_bf16 v[28:31], v[132:135], v[180:183], v[28:31]
	v_mfma_f32_16x16x32_bf16 v[24:27], v[140:143], v[180:183], v[24:27]
	v_mfma_f32_16x16x32_bf16 v[12:15], v[132:135], v[208:211], v[12:15]
	v_mfma_f32_16x16x32_bf16 v[8:11], v[140:143], v[208:211], v[8:11]
	s_setprio 0
	s_setprio 1
	v_mfma_f32_16x16x32_bf16 v[52:55], v[144:147], v[160:163], v[52:55]
	v_mfma_f32_16x16x32_bf16 v[48:51], v[152:155], v[160:163], v[48:51]
	v_mfma_f32_16x16x32_bf16 v[36:39], v[144:147], v[168:171], v[36:39]
	v_mfma_f32_16x16x32_bf16 v[32:35], v[152:155], v[168:171], v[32:35]
	v_mfma_f32_16x16x32_bf16 v[20:23], v[144:147], v[176:179], v[20:23]
	v_mfma_f32_16x16x32_bf16 v[16:19], v[152:155], v[176:179], v[16:19]
	v_mfma_f32_16x16x32_bf16 v[4:7], v[144:147], v[184:187], v[4:7]
	v_mfma_f32_16x16x32_bf16 v[0:3], v[152:155], v[184:187], v[0:3]
	v_mfma_f32_16x16x32_bf16 v[52:55], v[148:151], v[164:167], v[52:55]
	v_mfma_f32_16x16x32_bf16 v[48:51], v[156:159], v[164:167], v[48:51]
	v_mfma_f32_16x16x32_bf16 v[36:39], v[148:151], v[172:175], v[36:39]
	v_mfma_f32_16x16x32_bf16 v[32:35], v[156:159], v[172:175], v[32:35]
	v_mfma_f32_16x16x32_bf16 v[20:23], v[148:151], v[180:183], v[20:23]
	v_mfma_f32_16x16x32_bf16 v[16:19], v[156:159], v[180:183], v[16:19]
	v_mfma_f32_16x16x32_bf16 v[4:7], v[148:151], v[208:211], v[4:7]
	v_mfma_f32_16x16x32_bf16 v[0:3], v[156:159], v[208:211], v[0:3]
	s_setprio 0
	s_barrier
; #define PG8_STAGE(bufoff, gbase, voff) do { _Pragma("unroll") for (int _i = 0; _i < 2; ++_i) \
;         __builtin_amdgcn_global_load_lds((const unsigned*)((const char*)(gbase) + (voff)[_i]), (PG8_LAS unsigned*)(lds + (bufoff) + ldsw + _i * 8192), 16, 0, 0); } while (0)
; #define PG8_STAGE_A(b, h, gbase, NX) do { if constexpr (AM::GATHER) { const unsigned so_[2] = {(NX) ? gno[h][0] : gao[h][0], (NX) ? gno[h][1] : gao[h][1]}; PG8_STAGE(PG8_SA(b, h), gbase, so_); } \
;         else { PG8_STAGE(PG8_SA(b, h), (gbase) + (h) * hstep, voffA); } } while (0)
; #define PG8_LDA(dst, b, h) do { _Pragma("unroll") for (int m = 0; m < 4; ++m) _Pragma("unroll") for (int k = 0; k < 2; ++k) dst[m][k] = *(const PG8_LAS bf16x8*)(lds + PG8_SA(b, h) + aoff + m * 2048 + k * 1024); } while (0)
; #define PG8_LDB(dst, b, h) do { _Pragma("unroll") for (int n = 0; n < 2; ++n) _Pragma("unroll") for (int k = 0; k < 2; ++k) dst[n][k] = *(const PG8_LAS bf16x8*)(lds + PG8_SB(b, h) + boff + n * 2048 + k * 1024); } while (0)
; #define PG8_MMA(ai, bj, At, Bt) do { __builtin_amdgcn_s_setprio(1); _Pragma("unroll") for (int m = 0; m < 4; ++m) _Pragma("unroll") for (int n = 0; n < 2; ++n) _Pragma("unroll") for (int k = 0; k < 2; ++k) \
;         acc[ai][bj][m][n] = __builtin_amdgcn_mfma_f32_16x16x32_bf16(Bt[n][k], At[m][k], acc[ai][bj][m][n], 0, 0, 0); __builtin_amdgcn_s_setprio(0); } while (0)
; #define PG8_WAIT_V(n) asm volatile("s_waitcnt vmcnt(" #n ")" ::: "memory")
; #define PG8_WAIT_L(n) asm volatile("s_waitcnt lgkmcnt(" #n ")" ::: "memory")
; #define PG8_BAR __builtin_amdgcn_s_barrier()
; #define PG8_SCHED __builtin_amdgcn_sched_barrier(0)
; template <class Epi, class Sched, class AM, bool ALIGN_EPI = false, bool SP2 = false>
; __device__ __forceinline__ void gemm_phase(PG8_LAS unsigned char* lds, const Gemm g, const Sched& S, const Epi& E, const AM& am, const int wid_in) {
;     ...
;             PG8_LDB(B0, 1, 0); PG8_LDB(B1, 1, 1); PG8_SCHED; PG8_LDA(At, 1, 0); PG8_STAGE_A(0, 1, a2, last);
;             PG8_WAIT_V(8); PG8_WAIT_L(0); PG8_BAR; PG8_MMA(0, 0, At, B0); PG8_MMA(0, 1, At, B1); PG8_BAR; PG8_SCHED;
;             PG8_LDA(At, 1, 1); PG8_STAGE(PG8_SB(1, 0), b3, voffB); PG8_STAGE(PG8_SB(1, 1), b3 + hstep, voffB); PG8_STAGE_A(1, 0, a3, last);
;             PG8_WAIT_V(8); PG8_WAIT_L(0); PG8_BAR; PG8_MMA(1, 0, At, B0); PG8_MMA(1, 1, At, B1); PG8_BAR; PG8_SCHED;
	s_add_i32 s62, 0, 0x18000
	s_add_i32 s63, 0, 0x1c000
	v_add_u32_e32 v140, s62, v213
	v_add_u32_e32 v156, s63, v213
	ds_read_b128 v[128:131], v140
	ds_read_b128 v[132:135], v140 offset:1024
	ds_read_b128 v[136:139], v140 offset:2048
	ds_read_b128 v[140:143], v140 offset:3072
	ds_read_b128 v[144:147], v156
	ds_read_b128 v[148:151], v156 offset:1024
	ds_read_b128 v[152:155], v156 offset:2048
	ds_read_b128 v[156:159], v156 offset:3072
	s_add_u32 s34, s34, 0x20000
	s_addc_u32 s35, s35, 0
	s_mov_b32 m0, s42
	ds_read_b128 v[160:163], v219 offset:32768
	ds_read_b128 v[164:167], v219 offset:33792
	ds_read_b128 v[168:171], v219 offset:34816
	ds_read_b128 v[172:175], v219 offset:35840
	ds_read_b128 v[176:179], v219 offset:36864
	ds_read_b128 v[180:183], v219 offset:37888
	ds_read_b128 v[184:187], v219 offset:38912
	ds_read_b128 v[208:211], v219 offset:39936
	global_load_lds_dwordx4 v188, s[34:35]
	s_mov_b32 m0, s43
	s_nop 0
	global_load_lds_dwordx4 v192, s[34:35]
	s_waitcnt vmcnt(8)
	s_waitcnt lgkmcnt(0)
	s_barrier
	s_setprio 1
	s_waitcnt lgkmcnt(0)
	v_mfma_f32_16x16x32_bf16 v[124:127], v[128:131], v[160:163], v[124:127]
	v_mfma_f32_16x16x32_bf16 v[120:123], v[136:139], v[160:163], v[120:123]
	v_mfma_f32_16x16x32_bf16 v[108:111], v[128:131], v[168:171], v[108:111]
	v_mfma_f32_16x16x32_bf16 v[104:107], v[136:139], v[168:171], v[104:107]
	v_mfma_f32_16x16x32_bf16 v[92:95], v[128:131], v[176:179], v[92:95]
	v_mfma_f32_16x16x32_bf16 v[88:91], v[136:139], v[176:179], v[88:91]
	v_mfma_f32_16x16x32_bf16 v[76:79], v[128:131], v[184:187], v[76:79]
	v_mfma_f32_16x16x32_bf16 v[72:75], v[136:139], v[184:187], v[72:75]
	v_mfma_f32_16x16x32_bf16 v[124:127], v[132:135], v[164:167], v[124:127]
	v_mfma_f32_16x16x32_bf16 v[120:123], v[140:143], v[164:167], v[120:123]
	v_mfma_f32_16x16x32_bf16 v[108:111], v[132:135], v[172:175], v[108:111]
	v_mfma_f32_16x16x32_bf16 v[104:107], v[140:143], v[172:175], v[104:107]
	v_mfma_f32_16x16x32_bf16 v[92:95], v[132:135], v[180:183], v[92:95]
	v_mfma_f32_16x16x32_bf16 v[88:91], v[140:143], v[180:183], v[88:91]
	v_mfma_f32_16x16x32_bf16 v[76:79], v[132:135], v[208:211], v[76:79]
	v_mfma_f32_16x16x32_bf16 v[72:75], v[140:143], v[208:211], v[72:75]
	s_setprio 0
	s_setprio 1
	v_mfma_f32_16x16x32_bf16 v[116:119], v[144:147], v[160:163], v[116:119]
	v_mfma_f32_16x16x32_bf16 v[112:115], v[152:155], v[160:163], v[112:115]
	v_mfma_f32_16x16x32_bf16 v[100:103], v[144:147], v[168:171], v[100:103]
	v_mfma_f32_16x16x32_bf16 v[96:99], v[152:155], v[168:171], v[96:99]
	v_mfma_f32_16x16x32_bf16 v[84:87], v[144:147], v[176:179], v[84:87]
	v_mfma_f32_16x16x32_bf16 v[80:83], v[152:155], v[176:179], v[80:83]
	v_mfma_f32_16x16x32_bf16 v[68:71], v[144:147], v[184:187], v[68:71]
	v_mfma_f32_16x16x32_bf16 v[64:67], v[152:155], v[184:187], v[64:67]
	v_mfma_f32_16x16x32_bf16 v[116:119], v[148:151], v[164:167], v[116:119]
	v_mfma_f32_16x16x32_bf16 v[112:115], v[156:159], v[164:167], v[112:115]
	v_mfma_f32_16x16x32_bf16 v[100:103], v[148:151], v[172:175], v[100:103]
	v_mfma_f32_16x16x32_bf16 v[96:99], v[156:159], v[172:175], v[96:99]
	v_mfma_f32_16x16x32_bf16 v[84:87], v[148:151], v[180:183], v[84:87]
	v_mfma_f32_16x16x32_bf16 v[80:83], v[156:159], v[180:183], v[80:83]
	v_mfma_f32_16x16x32_bf16 v[68:71], v[148:151], v[208:211], v[68:71]
	v_mfma_f32_16x16x32_bf16 v[64:67], v[156:159], v[208:211], v[64:67]
	s_setprio 0
	s_barrier
	s_add_i32 s34, s62, s40
	s_mov_b32 m0, s34
	ds_read_b128 v[160:163], v219 offset:49152
	ds_read_b128 v[164:167], v219 offset:50176
	ds_read_b128 v[168:171], v219 offset:51200
	ds_read_b128 v[172:175], v219 offset:52224
	ds_read_b128 v[176:179], v219 offset:53248
	ds_read_b128 v[180:183], v219 offset:54272
	ds_read_b128 v[184:187], v219 offset:55296
	ds_read_b128 v[208:211], v219 offset:56320
	global_load_lds_dwordx4 v190, s[98:99]
	s_add_i32 m0, s34, 0x2000
	s_add_u32 s30, s30, 0x20080
	s_addc_u32 s31, s31, 0
	s_add_i32 s34, s63, s40
	global_load_lds_dwordx4 v194, s[98:99]
	s_mov_b32 m0, s34
	s_nop 0
	global_load_lds_dwordx4 v190, s[30:31]
	s_add_i32 m0, s34, 0x2000
	s_nop 0
	global_load_lds_dwordx4 v194, s[30:31]
	s_mov_b32 m0, s48
	s_nop 0
	global_load_lds_dwordx4 v188, s[100:101]
	s_mov_b32 m0, s49
	s_nop 0
	global_load_lds_dwordx4 v192, s[100:101]
	s_waitcnt vmcnt(8)
	s_waitcnt lgkmcnt(0)
	s_barrier
	s_setprio 1
	s_waitcnt lgkmcnt(0)
	v_mfma_f32_16x16x32_bf16 v[60:63], v[128:131], v[160:163], v[60:63]
	v_mfma_f32_16x16x32_bf16 v[56:59], v[136:139], v[160:163], v[56:59]
	v_mfma_f32_16x16x32_bf16 v[44:47], v[128:131], v[168:171], v[44:47]
	v_mfma_f32_16x16x32_bf16 v[40:43], v[136:139], v[168:171], v[40:43]
	v_mfma_f32_16x16x32_bf16 v[28:31], v[128:131], v[176:179], v[28:31]
	v_mfma_f32_16x16x32_bf16 v[24:27], v[136:139], v[176:179], v[24:27]
	v_mfma_f32_16x16x32_bf16 v[12:15], v[128:131], v[184:187], v[12:15]
	v_mfma_f32_16x16x32_bf16 v[8:11], v[136:139], v[184:187], v[8:11]
	v_mfma_f32_16x16x32_bf16 v[60:63], v[132:135], v[164:167], v[60:63]
	v_mfma_f32_16x16x32_bf16 v[56:59], v[140:143], v[164:167], v[56:59]
	v_mfma_f32_16x16x32_bf16 v[44:47], v[132:135], v[172:175], v[44:47]
	v_mfma_f32_16x16x32_bf16 v[40:43], v[140:143], v[172:175], v[40:43]
	v_mfma_f32_16x16x32_bf16 v[28:31], v[132:135], v[180:183], v[28:31]
	v_mfma_f32_16x16x32_bf16 v[24:27], v[140:143], v[180:183], v[24:27]
	v_mfma_f32_16x16x32_bf16 v[12:15], v[132:135], v[208:211], v[12:15]
	v_mfma_f32_16x16x32_bf16 v[8:11], v[140:143], v[208:211], v[8:11]
	s_setprio 0
	s_setprio 1
	v_mfma_f32_16x16x32_bf16 v[52:55], v[144:147], v[160:163], v[52:55]
	v_mfma_f32_16x16x32_bf16 v[48:51], v[152:155], v[160:163], v[48:51]
	v_mfma_f32_16x16x32_bf16 v[36:39], v[144:147], v[168:171], v[36:39]
	v_mfma_f32_16x16x32_bf16 v[32:35], v[152:155], v[168:171], v[32:35]
	v_mfma_f32_16x16x32_bf16 v[20:23], v[144:147], v[176:179], v[20:23]
	v_mfma_f32_16x16x32_bf16 v[16:19], v[152:155], v[176:179], v[16:19]
	v_mfma_f32_16x16x32_bf16 v[4:7], v[144:147], v[184:187], v[4:7]
	v_mfma_f32_16x16x32_bf16 v[0:3], v[152:155], v[184:187], v[0:3]
	v_mfma_f32_16x16x32_bf16 v[52:55], v[148:151], v[164:167], v[52:55]
	v_mfma_f32_16x16x32_bf16 v[48:51], v[156:159], v[164:167], v[48:51]
	v_mfma_f32_16x16x32_bf16 v[36:39], v[148:151], v[172:175], v[36:39]
	v_mfma_f32_16x16x32_bf16 v[32:35], v[156:159], v[172:175], v[32:35]
	v_mfma_f32_16x16x32_bf16 v[20:23], v[148:151], v[180:183], v[20:23]
	v_mfma_f32_16x16x32_bf16 v[16:19], v[156:159], v[180:183], v[16:19]
	v_mfma_f32_16x16x32_bf16 v[4:7], v[148:151], v[208:211], v[4:7]
	v_mfma_f32_16x16x32_bf16 v[0:3], v[156:159], v[208:211], v[0:3]
	s_setprio 0
	s_barrier
	s_add_i32 s61, s61, 2
	s_add_u32 s28, s28, 0x100
	s_addc_u32 s29, s29, 0
	s_add_u32 s59, s59, 0x100
	s_addc_u32 s60, s60, 0
	s_cmp_gt_u32 s61, 5
	s_cbranch_scc0 .LBB0_2129
	s_and_b64 vcc, exec, s[8:9]
	s_cbranch_vccz .LBB0_2132
	s_barrier

; #define PG8_LAS __attribute__((address_space(3)))
; #define PG8_STAGE(bufoff, gbase, voff) do { _Pragma("unroll") for (int _i = 0; _i < 2; ++_i) \
;         __builtin_amdgcn_global_load_lds((const unsigned*)((const char*)(gbase) + (voff)[_i]), (PG8_LAS unsigned*)(lds + (bufoff) + ldsw + _i * 8192), 16, 0, 0); } while (0)
; #define PG8_STAGE_A(b, h, gbase, NX) do { if constexpr (AM::GATHER) { const unsigned so_[2] = {(NX) ? gno[h][0] : gao[h][0], (NX) ? gno[h][1] : gao[h][1]}; PG8_STAGE(PG8_SA(b, h), gbase, so_); } \
;         else { PG8_STAGE(PG8_SA(b, h), (gbase) + (h) * hstep, voffA); } } while (0)
; #define PG8_WAIT_V(n) asm volatile("s_waitcnt vmcnt(" #n ")" ::: "memory")
; #define PG8_BAR __builtin_amdgcn_s_barrier()
; template <class Epi, class Sched, class AM, bool ALIGN_EPI = false, bool SP2 = false>
; __device__ __forceinline__ void gemm_phase(PG8_LAS unsigned char* lds, const Gemm g, const Sched& S, const Epi& E, const AM& am, const int wid_in) {
;     ...
;             const char* a1 = cA + (size_t)(t + 1) * kstep;
;             const char* a2 = last ? nA : cA + (size_t)(t + 2) * kstep; const char* b2 = last ? nB : cB + (size_t)(t + 2) * kstep;
;             const char* a3 = a2 + kstep; const char* b3 = b2 + kstep;
;             if (last && has_next) S.a_ready(nxt);
;             if (false) E.prefetch(cur, tid, (PG8_LAS unsigned*)(lds + 162816 + 512));
;             if constexpr (SP2) {
;             PG8_LDB(B0, 0, 0); PG8_LDB(B1, 0, 1); PG8_SCHED; PG8_LDA(At, 0, 0); PG8_STAGE_A(1, 1, a1, false);
;             PG8_WAIT_V(8); PG8_WAIT_L(0); PG8_BAR; PG8_MMA(0, 0, At, B0); PG8_MMA(0, 1, At, B1); PG8_BAR; PG8_SCHED;
;             PG8_LDA(At, 0, 1); PG8_STAGE(PG8_SB(0, 0), b2, voffB); PG8_STAGE(PG8_SB(0, 1), b2 + hstep, voffB); PG8_STAGE_A(0, 0, a2, last);
;             PG8_WAIT_V(8); PG8_WAIT_L(0); PG8_BAR; PG8_MMA(1, 0, At, B0); PG8_MMA(1, 1, At, B1); PG8_BAR; PG8_SCHED;
;             PG8_LDB(B0, 1, 0); PG8_LDB(B1, 1, 1); PG8_SCHED; PG8_LDA(At, 1, 0); PG8_STAGE_A(0, 1, a2, last);
;             PG8_WAIT_V(8); PG8_WAIT_L(0); PG8_BAR; PG8_MMA(0, 0, At, B0); PG8_MMA(0, 1, At, B1); PG8_BAR; PG8_SCHED;
;             PG8_LDA(At, 1, 1); PG8_STAGE(PG8_SB(1, 0), b3, voffB); PG8_STAGE(PG8_SB(1, 1), b3 + hstep, voffB); PG8_STAGE_A(1, 0, a3, last);
;             PG8_WAIT_V(8); PG8_WAIT_L(0); PG8_BAR; PG8_MMA(1, 0, At, B0); PG8_MMA(1, 1, At, B1); PG8_BAR; PG8_SCHED;
.LBB0_2724:
	ds_read_b128 v[144:147], v159
	ds_read_b128 v[162:165], v159 offset:1024
	ds_read_b128 v[166:169], v159 offset:2048
	ds_read_b128 v[170:173], v159 offset:3072
	ds_read_b128 v[174:177], v160
	ds_read_b128 v[178:181], v160 offset:1024
	ds_read_b128 v[182:185], v160 offset:2048
	ds_read_b128 v[186:189], v160 offset:3072
	s_add_u32 s26, s24, 0xfffe0080
	s_addc_u32 s27, s25, -1
	s_cmp_eq_u32 s61, 4
	s_cselect_b32 s29, s11, s27
	s_cselect_b32 s28, s57, s26
	s_cselect_b32 s27, s13, s60
	s_cselect_b32 s26, s58, s59
	s_add_i32 m0, s21, 0xc000
	ds_read_b128 v[190:193], v161
	ds_read_b128 v[194:197], v161 offset:1024
	ds_read_b128 v[198:201], v161 offset:2048
	ds_read_b128 v[202:205], v161 offset:3072
	ds_read_b128 v[206:209], v161 offset:4096
	ds_read_b128 v[210:213], v161 offset:5120
	ds_read_b128 v[214:217], v161 offset:6144
	ds_read_b128 v[218:221], v161 offset:7168
	global_load_lds_dwordx4 v138, s[24:25]
	s_add_i32 m0, s21, 0xe000
	s_nop 0
	global_load_lds_dwordx4 v140, s[24:25]
	s_waitcnt vmcnt(8)
	s_waitcnt lgkmcnt(0)
	s_barrier
	s_setprio 1
	s_waitcnt lgkmcnt(0)
	v_mfma_f32_16x16x32_bf16 v[124:127], v[144:147], v[190:193], v[124:127]
	v_mfma_f32_16x16x32_bf16 v[120:123], v[166:169], v[190:193], v[120:123]
	v_mfma_f32_16x16x32_bf16 v[116:119], v[144:147], v[198:201], v[116:119]
	v_mfma_f32_16x16x32_bf16 v[112:115], v[166:169], v[198:201], v[112:115]
	v_mfma_f32_16x16x32_bf16 v[100:103], v[144:147], v[206:209], v[100:103]
	v_mfma_f32_16x16x32_bf16 v[96:99], v[166:169], v[206:209], v[96:99]
	v_mfma_f32_16x16x32_bf16 v[84:87], v[144:147], v[214:217], v[84:87]
	v_mfma_f32_16x16x32_bf16 v[76:79], v[166:169], v[214:217], v[76:79]
	v_mfma_f32_16x16x32_bf16 v[124:127], v[162:165], v[194:197], v[124:127]
	v_mfma_f32_16x16x32_bf16 v[120:123], v[170:173], v[194:197], v[120:123]
	v_mfma_f32_16x16x32_bf16 v[116:119], v[162:165], v[202:205], v[116:119]
	v_mfma_f32_16x16x32_bf16 v[112:115], v[170:173], v[202:205], v[112:115]
	v_mfma_f32_16x16x32_bf16 v[100:103], v[162:165], v[210:213], v[100:103]
	v_mfma_f32_16x16x32_bf16 v[96:99], v[170:173], v[210:213], v[96:99]
	v_mfma_f32_16x16x32_bf16 v[84:87], v[162:165], v[218:221], v[84:87]
	v_mfma_f32_16x16x32_bf16 v[76:79], v[170:173], v[218:221], v[76:79]
	s_setprio 0
	s_setprio 1
	v_mfma_f32_16x16x32_bf16 v[108:111], v[174:177], v[190:193], v[108:111]
	v_mfma_f32_16x16x32_bf16 v[104:107], v[182:185], v[190:193], v[104:107]
	v_mfma_f32_16x16x32_bf16 v[92:95], v[174:177], v[198:201], v[92:95]
	v_mfma_f32_16x16x32_bf16 v[88:91], v[182:185], v[198:201], v[88:91]
	v_mfma_f32_16x16x32_bf16 v[80:83], v[174:177], v[206:209], v[80:83]
	v_mfma_f32_16x16x32_bf16 v[72:75], v[182:185], v[206:209], v[72:75]
	v_mfma_f32_16x16x32_bf16 v[68:71], v[174:177], v[214:217], v[68:71]
	v_mfma_f32_16x16x32_bf16 v[64:67], v[182:185], v[214:217], v[64:67]
	v_mfma_f32_16x16x32_bf16 v[108:111], v[178:181], v[194:197], v[108:111]
	v_mfma_f32_16x16x32_bf16 v[104:107], v[186:189], v[194:197], v[104:107]
	v_mfma_f32_16x16x32_bf16 v[92:95], v[178:181], v[202:205], v[92:95]
	v_mfma_f32_16x16x32_bf16 v[88:91], v[186:189], v[202:205], v[88:91]
	v_mfma_f32_16x16x32_bf16 v[80:83], v[178:181], v[210:213], v[80:83]
	v_mfma_f32_16x16x32_bf16 v[72:75], v[186:189], v[210:213], v[72:75]
	v_mfma_f32_16x16x32_bf16 v[68:71], v[178:181], v[218:221], v[68:71]
	v_mfma_f32_16x16x32_bf16 v[64:67], v[186:189], v[218:221], v[64:67]
	s_setprio 0
	s_barrier
	s_add_u32 s98, s26, s6
	s_addc_u32 s99, s27, s7
	s_add_u32 s100, s28, s6
	s_addc_u32 s101, s29, s7
	s_add_i32 s62, s53, s37
	s_mov_b32 m0, s62
	ds_read_b128 v[190:193], v161 offset:16384
	ds_read_b128 v[194:197], v161 offset:17408
	ds_read_b128 v[198:201], v161 offset:18432
	ds_read_b128 v[202:205], v161 offset:19456
	ds_read_b128 v[206:209], v161 offset:20480
	ds_read_b128 v[210:213], v161 offset:21504
	ds_read_b128 v[214:217], v161 offset:22528
	ds_read_b128 v[218:221], v161 offset:23552
	global_load_lds_dwordx4 v130, s[26:27]
	s_add_i32 m0, s62, 0x2000
	s_add_u32 s62, s26, 0x20000
	s_addc_u32 s63, s27, 0
	s_add_i32 s64, s54, s37
	global_load_lds_dwordx4 v134, s[26:27]
	s_mov_b32 m0, s64
	s_nop 0
	global_load_lds_dwordx4 v130, s[62:63]
	s_add_i32 m0, s64, 0x2000
	s_nop 0
	global_load_lds_dwordx4 v134, s[62:63]
	s_mov_b32 m0, s21
	s_nop 0
	global_load_lds_dwordx4 v128, s[28:29]
	s_mov_b32 m0, s23
	s_nop 0
	global_load_lds_dwordx4 v132, s[28:29]
	s_waitcnt vmcnt(8)
	s_waitcnt lgkmcnt(0)
	s_barrier
	s_setprio 1
	s_waitcnt lgkmcnt(0)
	v_mfma_f32_16x16x32_bf16 v[60:63], v[144:147], v[190:193], v[60:63]
	v_mfma_f32_16x16x32_bf16 v[56:59], v[166:169], v[190:193], v[56:59]
	v_mfma_f32_16x16x32_bf16 v[44:47], v[144:147], v[198:201], v[44:47]
	v_mfma_f32_16x16x32_bf16 v[40:43], v[166:169], v[198:201], v[40:43]
	v_mfma_f32_16x16x32_bf16 v[28:31], v[144:147], v[206:209], v[28:31]
	v_mfma_f32_16x16x32_bf16 v[24:27], v[166:169], v[206:209], v[24:27]
	v_mfma_f32_16x16x32_bf16 v[12:15], v[144:147], v[214:217], v[12:15]
	v_mfma_f32_16x16x32_bf16 v[8:11], v[166:169], v[214:217], v[8:11]
	v_mfma_f32_16x16x32_bf16 v[60:63], v[162:165], v[194:197], v[60:63]
	v_mfma_f32_16x16x32_bf16 v[56:59], v[170:173], v[194:197], v[56:59]
	v_mfma_f32_16x16x32_bf16 v[44:47], v[162:165], v[202:205], v[44:47]
	v_mfma_f32_16x16x32_bf16 v[40:43], v[170:173], v[202:205], v[40:43]
	v_mfma_f32_16x16x32_bf16 v[28:31], v[162:165], v[210:213], v[28:31]
	v_mfma_f32_16x16x32_bf16 v[24:27], v[170:173], v[210:213], v[24:27]
	v_mfma_f32_16x16x32_bf16 v[12:15], v[162:165], v[218:221], v[12:15]
	v_mfma_f32_16x16x32_bf16 v[8:11], v[170:173], v[218:221], v[8:11]
	s_setprio 0
	s_setprio 1
	v_mfma_f32_16x16x32_bf16 v[52:55], v[174:177], v[190:193], v[52:55]
	v_mfma_f32_16x16x32_bf16 v[48:51], v[182:185], v[190:193], v[48:51]
	v_mfma_f32_16x16x32_bf16 v[36:39], v[174:177], v[198:201], v[36:39]
	v_mfma_f32_16x16x32_bf16 v[32:35], v[182:185], v[198:201], v[32:35]
	v_mfma_f32_16x16x32_bf16 v[20:23], v[174:177], v[206:209], v[20:23]
	v_mfma_f32_16x16x32_bf16 v[16:19], v[182:185], v[206:209], v[16:19]
	v_mfma_f32_16x16x32_bf16 v[4:7], v[174:177], v[214:217], v[4:7]
	v_mfma_f32_16x16x32_bf16 v[0:3], v[182:185], v[214:217], v[0:3]
	v_mfma_f32_16x16x32_bf16 v[52:55], v[178:181], v[194:197], v[52:55]
	v_mfma_f32_16x16x32_bf16 v[48:51], v[186:189], v[194:197], v[48:51]
	v_mfma_f32_16x16x32_bf16 v[36:39], v[178:181], v[202:205], v[36:39]
	v_mfma_f32_16x16x32_bf16 v[32:35], v[186:189], v[202:205], v[32:35]
	v_mfma_f32_16x16x32_bf16 v[20:23], v[178:181], v[210:213], v[20:23]
	v_mfma_f32_16x16x32_bf16 v[16:19], v[186:189], v[210:213], v[16:19]
	v_mfma_f32_16x16x32_bf16 v[4:7], v[178:181], v[218:221], v[4:7]
	v_mfma_f32_16x16x32_bf16 v[0:3], v[186:189], v[218:221], v[0:3]
	s_setprio 0
	s_barrier
; #define PG8_STAGE(bufoff, gbase, voff) do { _Pragma("unroll") for (int _i = 0; _i < 2; ++_i) \
;         __builtin_amdgcn_global_load_lds((const unsigned*)((const char*)(gbase) + (voff)[_i]), (PG8_LAS unsigned*)(lds + (bufoff) + ldsw + _i * 8192), 16, 0, 0); } while (0)
; #define PG8_STAGE_A(b, h, gbase, NX) do { if constexpr (AM::GATHER) { const unsigned so_[2] = {(NX) ? gno[h][0] : gao[h][0], (NX) ? gno[h][1] : gao[h][1]}; PG8_STAGE(PG8_SA(b, h), gbase, so_); } \
;         else { PG8_STAGE(PG8_SA(b, h), (gbase) + (h) * hstep, voffA); } } while (0)
; #define PG8_LDA(dst, b, h) do { _Pragma("unroll") for (int m = 0; m < 4; ++m) _Pragma("unroll") for (int k = 0; k < 2; ++k) dst[m][k] = *(const PG8_LAS bf16x8*)(lds + PG8_SA(b, h) + aoff + m * 2048 + k * 1024); } while (0)
; #define PG8_LDB(dst, b, h) do { _Pragma("unroll") for (int n = 0; n < 2; ++n) _Pragma("unroll") for (int k = 0; k < 2; ++k) dst[n][k] = *(const PG8_LAS bf16x8*)(lds + PG8_SB(b, h) + boff + n * 2048 + k * 1024); } while (0)
; #define PG8_MMA(ai, bj, At, Bt) do { __builtin_amdgcn_s_setprio(1); _Pragma("unroll") for (int m = 0; m < 4; ++m) _Pragma("unroll") for (int n = 0; n < 2; ++n) _Pragma("unroll") for (int k = 0; k < 2; ++k) \
;         acc[ai][bj][m][n] = __builtin_amdgcn_mfma_f32_16x16x32_bf16(Bt[n][k], At[m][k], acc[ai][bj][m][n], 0, 0, 0); __builtin_amdgcn_s_setprio(0); } while (0)
; #define PG8_WAIT_V(n) asm volatile("s_waitcnt vmcnt(" #n ")" ::: "memory")
; #define PG8_WAIT_L(n) asm volatile("s_waitcnt lgkmcnt(" #n ")" ::: "memory")
; #define PG8_BAR __builtin_amdgcn_s_barrier()
; #define PG8_SCHED __builtin_amdgcn_sched_barrier(0)
; template <class Epi, class Sched, class AM, bool ALIGN_EPI = false, bool SP2 = false>
; __device__ __forceinline__ void gemm_phase(PG8_LAS unsigned char* lds, const Gemm g, const Sched& S, const Epi& E, const AM& am, const int wid_in) {
;     ...
;             PG8_LDB(B0, 1, 0); PG8_LDB(B1, 1, 1); PG8_SCHED; PG8_LDA(At, 1, 0); PG8_STAGE_A(0, 1, a2, last);
;             PG8_WAIT_V(8); PG8_WAIT_L(0); PG8_BAR; PG8_MMA(0, 0, At, B0); PG8_MMA(0, 1, At, B1); PG8_BAR; PG8_SCHED;
;             PG8_LDA(At, 1, 1); PG8_STAGE(PG8_SB(1, 0), b3, voffB); PG8_STAGE(PG8_SB(1, 1), b3 + hstep, voffB); PG8_STAGE_A(1, 0, a3, last);
;             PG8_WAIT_V(8); PG8_WAIT_L(0); PG8_BAR; PG8_MMA(1, 0, At, B0); PG8_MMA(1, 1, At, B1); PG8_BAR; PG8_SCHED;
	s_add_i32 s62, 0, 0x18000
	v_add_u32_e32 v148, s62, v151
	s_add_i32 s63, 0, 0x1c000
	ds_read_b128 v[144:147], v148
	ds_read_b128 v[162:165], v148 offset:1024
	ds_read_b128 v[166:169], v148 offset:2048
	ds_read_b128 v[170:173], v148 offset:3072
	v_add_u32_e32 v148, s63, v151
	ds_read_b128 v[174:177], v148
	ds_read_b128 v[178:181], v148 offset:1024
	ds_read_b128 v[182:185], v148 offset:2048
	ds_read_b128 v[186:189], v148 offset:3072
	s_add_u32 s28, s28, 0x20000
	s_addc_u32 s29, s29, 0
	s_mov_b32 m0, s40
	ds_read_b128 v[190:193], v161 offset:32768
	ds_read_b128 v[194:197], v161 offset:33792
	ds_read_b128 v[198:201], v161 offset:34816
	ds_read_b128 v[202:205], v161 offset:35840
	ds_read_b128 v[206:209], v161 offset:36864
	ds_read_b128 v[210:213], v161 offset:37888
	ds_read_b128 v[214:217], v161 offset:38912
	ds_read_b128 v[218:221], v161 offset:39936
	global_load_lds_dwordx4 v128, s[28:29]
	s_mov_b32 m0, s41
	s_nop 0
	global_load_lds_dwordx4 v132, s[28:29]
	s_waitcnt vmcnt(8)
	s_waitcnt lgkmcnt(0)
	s_barrier
	s_setprio 1
	s_waitcnt lgkmcnt(0)
	v_mfma_f32_16x16x32_bf16 v[124:127], v[144:147], v[190:193], v[124:127]
	v_mfma_f32_16x16x32_bf16 v[120:123], v[166:169], v[190:193], v[120:123]
	v_mfma_f32_16x16x32_bf16 v[116:119], v[144:147], v[198:201], v[116:119]
	v_mfma_f32_16x16x32_bf16 v[112:115], v[166:169], v[198:201], v[112:115]
	v_mfma_f32_16x16x32_bf16 v[100:103], v[144:147], v[206:209], v[100:103]
	v_mfma_f32_16x16x32_bf16 v[96:99], v[166:169], v[206:209], v[96:99]
	v_mfma_f32_16x16x32_bf16 v[84:87], v[144:147], v[214:217], v[84:87]
	v_mfma_f32_16x16x32_bf16 v[76:79], v[166:169], v[214:217], v[76:79]
	v_mfma_f32_16x16x32_bf16 v[124:127], v[162:165], v[194:197], v[124:127]
	v_mfma_f32_16x16x32_bf16 v[120:123], v[170:173], v[194:197], v[120:123]
	v_mfma_f32_16x16x32_bf16 v[116:119], v[162:165], v[202:205], v[116:119]
	v_mfma_f32_16x16x32_bf16 v[112:115], v[170:173], v[202:205], v[112:115]
	v_mfma_f32_16x16x32_bf16 v[100:103], v[162:165], v[210:213], v[100:103]
	v_mfma_f32_16x16x32_bf16 v[96:99], v[170:173], v[210:213], v[96:99]
	v_mfma_f32_16x16x32_bf16 v[84:87], v[162:165], v[218:221], v[84:87]
	v_mfma_f32_16x16x32_bf16 v[76:79], v[170:173], v[218:221], v[76:79]
	s_setprio 0
	s_setprio 1
	v_mfma_f32_16x16x32_bf16 v[108:111], v[174:177], v[190:193], v[108:111]
	v_mfma_f32_16x16x32_bf16 v[104:107], v[182:185], v[190:193], v[104:107]
	v_mfma_f32_16x16x32_bf16 v[92:95], v[174:177], v[198:201], v[92:95]
	v_mfma_f32_16x16x32_bf16 v[88:91], v[182:185], v[198:201], v[88:91]
	v_mfma_f32_16x16x32_bf16 v[80:83], v[174:177], v[206:209], v[80:83]
	v_mfma_f32_16x16x32_bf16 v[72:75], v[182:185], v[206:209], v[72:75]
	v_mfma_f32_16x16x32_bf16 v[68:71], v[174:177], v[214:217], v[68:71]
	v_mfma_f32_16x16x32_bf16 v[64:67], v[182:185], v[214:217], v[64:67]
	v_mfma_f32_16x16x32_bf16 v[108:111], v[178:181], v[194:197], v[108:111]
	v_mfma_f32_16x16x32_bf16 v[104:107], v[186:189], v[194:197], v[104:107]
	v_mfma_f32_16x16x32_bf16 v[92:95], v[178:181], v[202:205], v[92:95]
	v_mfma_f32_16x16x32_bf16 v[88:91], v[186:189], v[202:205], v[88:91]
	v_mfma_f32_16x16x32_bf16 v[80:83], v[178:181], v[210:213], v[80:83]
	v_mfma_f32_16x16x32_bf16 v[72:75], v[186:189], v[210:213], v[72:75]
	v_mfma_f32_16x16x32_bf16 v[68:71], v[178:181], v[218:221], v[68:71]
	v_mfma_f32_16x16x32_bf16 v[64:67], v[186:189], v[218:221], v[64:67]
	s_setprio 0
	s_barrier
	s_add_i32 s28, s62, s37
	s_mov_b32 m0, s28
	ds_read_b128 v[190:193], v161 offset:49152
	ds_read_b128 v[194:197], v161 offset:50176
	ds_read_b128 v[198:201], v161 offset:51200
	ds_read_b128 v[202:205], v161 offset:52224
	ds_read_b128 v[206:209], v161 offset:53248
	ds_read_b128 v[210:213], v161 offset:54272
	ds_read_b128 v[214:217], v161 offset:55296
	ds_read_b128 v[218:221], v161 offset:56320
	global_load_lds_dwordx4 v130, s[98:99]
	s_add_i32 m0, s28, 0x2000
	s_add_u32 s26, s26, 0x20080
	s_addc_u32 s27, s27, 0
	s_add_i32 s28, s63, s37
	global_load_lds_dwordx4 v134, s[98:99]
	s_mov_b32 m0, s28
	s_nop 0
	global_load_lds_dwordx4 v130, s[26:27]
	s_add_i32 m0, s28, 0x2000
	s_nop 0
	global_load_lds_dwordx4 v134, s[26:27]
	s_mov_b32 m0, s45
	s_nop 0
	global_load_lds_dwordx4 v128, s[100:101]
	s_mov_b32 m0, s46
	s_nop 0
	global_load_lds_dwordx4 v132, s[100:101]
	s_waitcnt vmcnt(8)
	s_waitcnt lgkmcnt(0)
	s_barrier
	s_setprio 1
	s_waitcnt lgkmcnt(0)
	v_mfma_f32_16x16x32_bf16 v[60:63], v[144:147], v[190:193], v[60:63]
	v_mfma_f32_16x16x32_bf16 v[56:59], v[166:169], v[190:193], v[56:59]
	v_mfma_f32_16x16x32_bf16 v[44:47], v[144:147], v[198:201], v[44:47]
	v_mfma_f32_16x16x32_bf16 v[40:43], v[166:169], v[198:201], v[40:43]
	v_mfma_f32_16x16x32_bf16 v[28:31], v[144:147], v[206:209], v[28:31]
	v_mfma_f32_16x16x32_bf16 v[24:27], v[166:169], v[206:209], v[24:27]
	v_mfma_f32_16x16x32_bf16 v[12:15], v[144:147], v[214:217], v[12:15]
	v_mfma_f32_16x16x32_bf16 v[8:11], v[166:169], v[214:217], v[8:11]
	v_mfma_f32_16x16x32_bf16 v[60:63], v[162:165], v[194:197], v[60:63]
	v_mfma_f32_16x16x32_bf16 v[56:59], v[170:173], v[194:197], v[56:59]
	v_mfma_f32_16x16x32_bf16 v[44:47], v[162:165], v[202:205], v[44:47]
	v_mfma_f32_16x16x32_bf16 v[40:43], v[170:173], v[202:205], v[40:43]
	v_mfma_f32_16x16x32_bf16 v[28:31], v[162:165], v[210:213], v[28:31]
	v_mfma_f32_16x16x32_bf16 v[24:27], v[170:173], v[210:213], v[24:27]
	v_mfma_f32_16x16x32_bf16 v[12:15], v[162:165], v[218:221], v[12:15]
	v_mfma_f32_16x16x32_bf16 v[8:11], v[170:173], v[218:221], v[8:11]
	s_setprio 0
	s_setprio 1
	v_mfma_f32_16x16x32_bf16 v[52:55], v[174:177], v[190:193], v[52:55]
	v_mfma_f32_16x16x32_bf16 v[48:51], v[182:185], v[190:193], v[48:51]
	v_mfma_f32_16x16x32_bf16 v[36:39], v[174:177], v[198:201], v[36:39]
	v_mfma_f32_16x16x32_bf16 v[32:35], v[182:185], v[198:201], v[32:35]
	v_mfma_f32_16x16x32_bf16 v[20:23], v[174:177], v[206:209], v[20:23]
	v_mfma_f32_16x16x32_bf16 v[16:19], v[182:185], v[206:209], v[16:19]
	v_mfma_f32_16x16x32_bf16 v[4:7], v[174:177], v[214:217], v[4:7]
	v_mfma_f32_16x16x32_bf16 v[0:3], v[182:185], v[214:217], v[0:3]
	v_mfma_f32_16x16x32_bf16 v[52:55], v[178:181], v[194:197], v[52:55]
	v_mfma_f32_16x16x32_bf16 v[48:51], v[186:189], v[194:197], v[48:51]
	v_mfma_f32_16x16x32_bf16 v[36:39], v[178:181], v[202:205], v[36:39]
	v_mfma_f32_16x16x32_bf16 v[32:35], v[186:189], v[202:205], v[32:35]
	v_mfma_f32_16x16x32_bf16 v[20:23], v[178:181], v[210:213], v[20:23]
	v_mfma_f32_16x16x32_bf16 v[16:19], v[186:189], v[210:213], v[16:19]
	v_mfma_f32_16x16x32_bf16 v[4:7], v[178:181], v[218:221], v[4:7]
	v_mfma_f32_16x16x32_bf16 v[0:3], v[186:189], v[218:221], v[0:3]
	s_setprio 0
	s_barrier
	s_add_i32 s61, s61, 2
	s_add_u32 s24, s24, 0x100
	s_addc_u32 s25, s25, 0
	s_add_u32 s59, s59, 0x100
	s_addc_u32 s60, s60, 0
	s_cmp_gt_u32 s61, 5
	s_cbranch_scc0 .LBB0_2724
	s_and_b64 vcc, exec, s[8:9]
	s_cbranch_vccz .LBB0_2727
	s_barrier
